# GEMM MMA segments: redundant lgkmcnt wait at the segment head and the mid-segment s_setprio 0/1 pair removed (3 fewer scalar instructions per MMA segment)
# speedup vs baseline: 1.0039x; 1.0038x over previous
; #define PG8_STAGE(bufoff, gbase, voff) do { _Pragma("unroll") for (int _i = 0; _i < 2; ++_i) \
;         __builtin_amdgcn_global_load_lds((const unsigned*)((const char*)(gbase) + (voff)[_i]), (LAS unsigned*)(lds + (bufoff) + ldsw + _i * 8192), 16, 0, 0); } while (0)
; #define PG8_LDA(dst, b, h) do { _Pragma("unroll") for (int m = 0; m < 4; ++m) dst[m] = PG8_LD32(lds + PG8_SA(b, h) + aoff + m * 2048); } while (0)
; #define PG8_LDB(dst, b, h) do { _Pragma("unroll") for (int n = 0; n < 2; ++n) dst[n] = PG8_LD32(lds + PG8_SB(b, h) + boff + n * 2048); } while (0)
; #define PG8_WAIT_V(n) asm volatile("s_waitcnt vmcnt(" #n ")" ::: "memory")
; #define PG8_WAIT_L(n) asm volatile("s_waitcnt lgkmcnt(" #n ")" ::: "memory")
; #define PG8_BAR __builtin_amdgcn_s_barrier()
; #define PG8_SCHED __builtin_amdgcn_sched_barrier(0)
; #define PG8_STA(bufoff, nextflag, h, koff) do { if constexpr (Sched::GATHER) { unsigned _o[2]; _o[0] = (nextflag) ? nxtA[h][0] : curA[h][0]; _o[1] = (nextflag) ? nxtA[h][1] : curA[h][1]; PG8_STAGE(bufoff, Ab + (koff), _o); } \
;         else { PG8_STAGE(bufoff, ((nextflag) ? nA : cA) + (size_t)(h) * hstep + (koff), voffA); } } while (0)
; template <class Epi, class Sched, bool ALIGN_EPI, int DT>
; __device__ __forceinline__ void gemm_phase(LAS unsigned char* lds, const int KB, const Sched& S, const Epi& E) {
;     ...
;         for (int t = 0; t < nt; t += 2) {
;             const bool last = (t == nt - 2);
;             const size_t k1 = (size_t)(t + 1) * kstep, k2 = last ? 0 : (size_t)(t + 2) * kstep, k3 = k2 + kstep;
;             const char* b2 = last ? nB : cB + (size_t)(t + 2) * kstep; const char* b3 = b2 + kstep;
;             PG8_LDB(B0, 0, 0); PG8_LDB(B1, 0, 1); PG8_SCHED; PG8_LDA(At, 0, 0); PG8_STA(PG8_SA(1, 1), false, 1, k1);
;             PG8_WAIT_V(8); PG8_WAIT_L(0); PG8_BAR; PG8_MMA(0, 0, At, B0); PG8_MMA(0, 1, At, B1); PG8_BAR; PG8_SCHED;
;             PG8_LDA(At, 0, 1); PG8_STAGE(PG8_SB(0, 0), b2, voffB); PG8_STAGE(PG8_SB(0, 1), b2 + hstep, voffB); PG8_STA(PG8_SA(0, 0), last, 0, k2);
;             PG8_WAIT_V(8); PG8_WAIT_L(0); PG8_BAR; PG8_MMA(1, 0, At, B0); PG8_MMA(1, 1, At, B1); PG8_BAR; PG8_SCHED;
.LBB0_193:
	ds_read_b128 v[152:155], v175
	ds_read_b128 v[156:159], v175 offset:1024
	ds_read_b128 v[160:163], v175 offset:2048
	ds_read_b128 v[164:167], v175 offset:3072
	ds_read_b128 v[168:171], v176
	ds_read_b128 v[182:185], v176 offset:1024
	ds_read_b128 v[186:189], v176 offset:2048
	ds_read_b128 v[190:193], v176 offset:3072
	s_add_u32 s38, s36, 0x100
	s_addc_u32 s39, s37, 0
	s_add_u32 s68, s25, s36
	s_addc_u32 s69, s66, s37
	s_cmp_eq_u32 s67, 12
	s_cselect_b64 s[42:43], -1, 0
	s_and_b64 s[40:41], s[42:43], exec
	s_cselect_b32 s70, 0, s38
	s_cselect_b32 s41, s0, s69
	s_cselect_b32 s40, s23, s68
	v_lshl_add_u64 v[228:229], v[148:149], 0, s[36:37]
	s_add_i32 m0, s45, 0xc000
	ds_read_b128 v[196:199], v177
	ds_read_b128 v[200:203], v177 offset:1024
	ds_read_b128 v[204:207], v177 offset:2048
	ds_read_b128 v[208:211], v177 offset:3072
	ds_read_b128 v[212:215], v177 offset:4096
	ds_read_b128 v[216:219], v177 offset:5120
	ds_read_b128 v[220:223], v177 offset:6144
	ds_read_b128 v[224:227], v177 offset:7168
	global_load_lds_dwordx4 v[228:229], off
	v_lshl_add_u64 v[228:229], v[150:151], 0, s[36:37]
	s_add_i32 m0, s45, 0xe000
	s_nop 0
	global_load_lds_dwordx4 v[228:229], off
	s_waitcnt vmcnt(8)
	s_waitcnt lgkmcnt(0)
	s_barrier
	s_setprio 1
	v_mfma_i32_16x16x64_i8 v[126:129], v[152:155], v[196:199], v[126:129]
	v_mfma_i32_16x16x64_i8 v[122:125], v[160:163], v[196:199], v[122:125]
	v_mfma_i32_16x16x64_i8 v[110:113], v[152:155], v[204:207], v[110:113]
	v_mfma_i32_16x16x64_i8 v[106:109], v[160:163], v[204:207], v[106:109]
	v_mfma_i32_16x16x64_i8 v[94:97], v[152:155], v[212:215], v[94:97]
	v_mfma_i32_16x16x64_i8 v[90:93], v[160:163], v[212:215], v[90:93]
	v_mfma_i32_16x16x64_i8 v[78:81], v[152:155], v[220:223], v[78:81]
	v_mfma_i32_16x16x64_i8 v[74:77], v[160:163], v[220:223], v[74:77]
	v_mfma_i32_16x16x64_i8 v[126:129], v[156:159], v[200:203], v[126:129]
	v_mfma_i32_16x16x64_i8 v[122:125], v[164:167], v[200:203], v[122:125]
	v_mfma_i32_16x16x64_i8 v[110:113], v[156:159], v[208:211], v[110:113]
	v_mfma_i32_16x16x64_i8 v[106:109], v[164:167], v[208:211], v[106:109]
	v_mfma_i32_16x16x64_i8 v[94:97], v[156:159], v[216:219], v[94:97]
	v_mfma_i32_16x16x64_i8 v[90:93], v[164:167], v[216:219], v[90:93]
	v_mfma_i32_16x16x64_i8 v[78:81], v[156:159], v[224:227], v[78:81]
	v_mfma_i32_16x16x64_i8 v[74:77], v[164:167], v[224:227], v[74:77]
	v_mfma_i32_16x16x64_i8 v[118:121], v[168:171], v[196:199], v[118:121]
	v_mfma_i32_16x16x64_i8 v[114:117], v[186:189], v[196:199], v[114:117]
	v_mfma_i32_16x16x64_i8 v[102:105], v[168:171], v[204:207], v[102:105]
	v_mfma_i32_16x16x64_i8 v[98:101], v[186:189], v[204:207], v[98:101]
	v_mfma_i32_16x16x64_i8 v[86:89], v[168:171], v[212:215], v[86:89]
	v_mfma_i32_16x16x64_i8 v[82:85], v[186:189], v[212:215], v[82:85]
	v_mfma_i32_16x16x64_i8 v[70:73], v[168:171], v[220:223], v[70:73]
	v_mfma_i32_16x16x64_i8 v[66:69], v[186:189], v[220:223], v[66:69]
	v_mfma_i32_16x16x64_i8 v[118:121], v[182:185], v[200:203], v[118:121]
	v_mfma_i32_16x16x64_i8 v[114:117], v[190:193], v[200:203], v[114:117]
	v_mfma_i32_16x16x64_i8 v[102:105], v[182:185], v[208:211], v[102:105]
	v_mfma_i32_16x16x64_i8 v[98:101], v[190:193], v[208:211], v[98:101]
	v_mfma_i32_16x16x64_i8 v[86:89], v[182:185], v[216:219], v[86:89]
	v_mfma_i32_16x16x64_i8 v[82:85], v[190:193], v[216:219], v[82:85]
	v_mfma_i32_16x16x64_i8 v[70:73], v[182:185], v[224:227], v[70:73]
	v_mfma_i32_16x16x64_i8 v[66:69], v[190:193], v[224:227], v[66:69]
	s_setprio 0
	s_barrier
	s_add_i32 s36, s62, s5
	v_lshl_add_u64 v[228:229], s[40:41], 0, v[134:135]
	s_mov_b32 m0, s36
	ds_read_b128 v[196:199], v177 offset:16384
	ds_read_b128 v[200:203], v177 offset:17408
	ds_read_b128 v[204:207], v177 offset:18432
	ds_read_b128 v[208:211], v177 offset:19456
	ds_read_b128 v[212:215], v177 offset:20480
	ds_read_b128 v[216:219], v177 offset:21504
	ds_read_b128 v[220:223], v177 offset:22528
	ds_read_b128 v[224:227], v177 offset:23552
	global_load_lds_dwordx4 v[228:229], off
	s_add_i32 m0, s36, 0x2000
	s_add_u32 s36, s40, 0x40000
	v_lshl_add_u64 v[230:231], s[40:41], 0, v[132:133]
	s_addc_u32 s37, s41, 0
	s_add_i32 s68, s63, s5
	global_load_lds_dwordx4 v[230:231], off
	v_lshl_add_u64 v[232:233], s[36:37], 0, v[134:135]
	s_mov_b32 m0, s68
	s_nop 0
	global_load_lds_dwordx4 v[232:233], off
	v_lshl_add_u64 v[232:233], s[36:37], 0, v[132:133]
	s_add_i32 m0, s68, 0x2000
	s_and_b64 s[36:37], s[8:9], s[42:43]
	s_and_b64 s[36:37], s[36:37], exec
	s_cselect_b32 s36, s26, s34
	s_cselect_b32 s37, s27, s35
	s_add_u32 s36, s36, s70
	s_addc_u32 s37, s37, 0
	global_load_lds_dwordx4 v[232:233], off
	v_lshl_add_u64 v[232:233], s[36:37], 0, v[136:137]
	s_mov_b32 m0, s45
	v_lshl_add_u64 v[234:235], s[36:37], 0, v[138:139]
	global_load_lds_dwordx4 v[232:233], off
	s_mov_b32 m0, s46
	s_nop 0
	global_load_lds_dwordx4 v[234:235], off
	s_waitcnt vmcnt(8)
	s_waitcnt lgkmcnt(0)
	s_barrier
; #define PG8_STAGE(bufoff, gbase, voff) do { _Pragma("unroll") for (int _i = 0; _i < 2; ++_i) \
;         __builtin_amdgcn_global_load_lds((const unsigned*)((const char*)(gbase) + (voff)[_i]), (LAS unsigned*)(lds + (bufoff) + ldsw + _i * 8192), 16, 0, 0); } while (0)
; #define PG8_LDA(dst, b, h) do { _Pragma("unroll") for (int m = 0; m < 4; ++m) dst[m] = PG8_LD32(lds + PG8_SA(b, h) + aoff + m * 2048); } while (0)
; #define PG8_LDB(dst, b, h) do { _Pragma("unroll") for (int n = 0; n < 2; ++n) dst[n] = PG8_LD32(lds + PG8_SB(b, h) + boff + n * 2048); } while (0)
; #define PG8_WAIT_V(n) asm volatile("s_waitcnt vmcnt(" #n ")" ::: "memory")
; #define PG8_WAIT_L(n) asm volatile("s_waitcnt lgkmcnt(" #n ")" ::: "memory")
; #define PG8_BAR __builtin_amdgcn_s_barrier()
; #define PG8_SCHED __builtin_amdgcn_sched_barrier(0)
; #define PG8_STA(bufoff, nextflag, h, koff) do { if constexpr (Sched::GATHER) { unsigned _o[2]; _o[0] = (nextflag) ? nxtA[h][0] : curA[h][0]; _o[1] = (nextflag) ? nxtA[h][1] : curA[h][1]; PG8_STAGE(bufoff, Ab + (koff), _o); } \
;         else { PG8_STAGE(bufoff, ((nextflag) ? nA : cA) + (size_t)(h) * hstep + (koff), voffA); } } while (0)
; template <class Epi, class Sched, bool ALIGN_EPI, int DT>
; __device__ __forceinline__ void gemm_phase(LAS unsigned char* lds, const int KB, const Sched& S, const Epi& E) {
;     ...
;             PG8_WAIT_V(8); PG8_WAIT_L(0); PG8_BAR; PG8_MMA(0, 0, At, B0); PG8_MMA(0, 1, At, B1); PG8_BAR; PG8_SCHED;
;             PG8_LDA(At, 0, 1); PG8_STAGE(PG8_SB(0, 0), b2, voffB); PG8_STAGE(PG8_SB(0, 1), b2 + hstep, voffB); PG8_STA(PG8_SA(0, 0), last, 0, k2);
;             PG8_WAIT_V(8); PG8_WAIT_L(0); PG8_BAR; PG8_MMA(1, 0, At, B0); PG8_MMA(1, 1, At, B1); PG8_BAR; PG8_SCHED;
;             PG8_LDB(B0, 1, 0); PG8_LDB(B1, 1, 1); PG8_SCHED; PG8_LDA(At, 1, 0); PG8_STA(PG8_SA(0, 1), last, 1, k2);
;             PG8_WAIT_V(8); PG8_WAIT_L(0); PG8_BAR; PG8_MMA(0, 0, At, B0); PG8_MMA(0, 1, At, B1); PG8_BAR; PG8_SCHED;
	s_setprio 1
	v_mfma_i32_16x16x64_i8 v[62:65], v[152:155], v[196:199], v[62:65]
	v_mfma_i32_16x16x64_i8 v[58:61], v[160:163], v[196:199], v[58:61]
	v_mfma_i32_16x16x64_i8 v[46:49], v[152:155], v[204:207], v[46:49]
	v_mfma_i32_16x16x64_i8 v[42:45], v[160:163], v[204:207], v[42:45]
	v_mfma_i32_16x16x64_i8 v[30:33], v[152:155], v[212:215], v[30:33]
	v_mfma_i32_16x16x64_i8 v[26:29], v[160:163], v[212:215], v[26:29]
	v_mfma_i32_16x16x64_i8 v[6:9], v[152:155], v[220:223], v[6:9]
	v_mfma_i32_16x16x64_i8 v[2:5], v[160:163], v[220:223], v[2:5]
	v_mfma_i32_16x16x64_i8 v[62:65], v[156:159], v[200:203], v[62:65]
	v_mfma_i32_16x16x64_i8 v[58:61], v[164:167], v[200:203], v[58:61]
	v_mfma_i32_16x16x64_i8 v[46:49], v[156:159], v[208:211], v[46:49]
	v_mfma_i32_16x16x64_i8 v[42:45], v[164:167], v[208:211], v[42:45]
	v_mfma_i32_16x16x64_i8 v[30:33], v[156:159], v[216:219], v[30:33]
	v_mfma_i32_16x16x64_i8 v[26:29], v[164:167], v[216:219], v[26:29]
	v_mfma_i32_16x16x64_i8 v[6:9], v[156:159], v[224:227], v[6:9]
	v_mfma_i32_16x16x64_i8 v[2:5], v[164:167], v[224:227], v[2:5]
	v_mfma_i32_16x16x64_i8 v[54:57], v[168:171], v[196:199], v[54:57]
	v_mfma_i32_16x16x64_i8 v[50:53], v[186:189], v[196:199], v[50:53]
	v_mfma_i32_16x16x64_i8 v[38:41], v[168:171], v[204:207], v[38:41]
	v_mfma_i32_16x16x64_i8 v[34:37], v[186:189], v[204:207], v[34:37]
	v_mfma_i32_16x16x64_i8 v[14:17], v[168:171], v[212:215], v[14:17]
	v_mfma_i32_16x16x64_i8 v[10:13], v[186:189], v[212:215], v[10:13]
	v_mfma_i32_16x16x64_i8 v[22:25], v[168:171], v[220:223], v[22:25]
	v_mfma_i32_16x16x64_i8 v[18:21], v[186:189], v[220:223], v[18:21]
	v_mfma_i32_16x16x64_i8 v[54:57], v[182:185], v[200:203], v[54:57]
	v_mfma_i32_16x16x64_i8 v[50:53], v[190:193], v[200:203], v[50:53]
	v_mfma_i32_16x16x64_i8 v[38:41], v[182:185], v[208:211], v[38:41]
	v_mfma_i32_16x16x64_i8 v[34:37], v[190:193], v[208:211], v[34:37]
	v_mfma_i32_16x16x64_i8 v[14:17], v[182:185], v[216:219], v[14:17]
	v_mfma_i32_16x16x64_i8 v[10:13], v[190:193], v[216:219], v[10:13]
	v_mfma_i32_16x16x64_i8 v[22:25], v[182:185], v[224:227], v[22:25]
	v_mfma_i32_16x16x64_i8 v[18:21], v[190:193], v[224:227], v[18:21]
	s_setprio 0
	s_barrier
	s_add_i32 s42, 0, 0x18000
	v_add_u32_e32 v1, s42, v173
	s_add_i32 s43, 0, 0x1c000
	ds_read_b128 v[152:155], v1
	ds_read_b128 v[156:159], v1 offset:1024
	ds_read_b128 v[160:163], v1 offset:2048
	ds_read_b128 v[164:167], v1 offset:3072
	v_add_u32_e32 v1, s43, v173
	ds_read_b128 v[168:171], v1
	ds_read_b128 v[182:185], v1 offset:1024
	ds_read_b128 v[186:189], v1 offset:2048
	ds_read_b128 v[190:193], v1 offset:3072
	s_add_u32 s36, s36, 0x40000
	s_addc_u32 s37, s37, 0
	s_mov_b32 m0, s47
	v_lshl_add_u64 v[236:237], s[36:37], 0, v[136:137]
	ds_read_b128 v[196:199], v177 offset:32768
	ds_read_b128 v[200:203], v177 offset:33792
	ds_read_b128 v[204:207], v177 offset:34816
	ds_read_b128 v[208:211], v177 offset:35840
	ds_read_b128 v[212:215], v177 offset:36864
	ds_read_b128 v[216:219], v177 offset:37888
	ds_read_b128 v[220:223], v177 offset:38912
	ds_read_b128 v[224:227], v177 offset:39936
	global_load_lds_dwordx4 v[236:237], off
	v_lshl_add_u64 v[236:237], s[36:37], 0, v[138:139]
	s_mov_b32 m0, s49
	s_nop 0
	global_load_lds_dwordx4 v[236:237], off
	s_waitcnt vmcnt(8)
	s_waitcnt lgkmcnt(0)
	s_barrier
	s_setprio 1
	v_mfma_i32_16x16x64_i8 v[126:129], v[152:155], v[196:199], v[126:129]
	v_mfma_i32_16x16x64_i8 v[122:125], v[160:163], v[196:199], v[122:125]
	v_mfma_i32_16x16x64_i8 v[110:113], v[152:155], v[204:207], v[110:113]
	v_mfma_i32_16x16x64_i8 v[106:109], v[160:163], v[204:207], v[106:109]
	v_mfma_i32_16x16x64_i8 v[94:97], v[152:155], v[212:215], v[94:97]
	v_mfma_i32_16x16x64_i8 v[90:93], v[160:163], v[212:215], v[90:93]
	v_mfma_i32_16x16x64_i8 v[78:81], v[152:155], v[220:223], v[78:81]
	v_mfma_i32_16x16x64_i8 v[74:77], v[160:163], v[220:223], v[74:77]
	v_mfma_i32_16x16x64_i8 v[126:129], v[156:159], v[200:203], v[126:129]
	v_mfma_i32_16x16x64_i8 v[122:125], v[164:167], v[200:203], v[122:125]
	v_mfma_i32_16x16x64_i8 v[110:113], v[156:159], v[208:211], v[110:113]
	v_mfma_i32_16x16x64_i8 v[106:109], v[164:167], v[208:211], v[106:109]
	v_mfma_i32_16x16x64_i8 v[94:97], v[156:159], v[216:219], v[94:97]
	v_mfma_i32_16x16x64_i8 v[90:93], v[164:167], v[216:219], v[90:93]
	v_mfma_i32_16x16x64_i8 v[78:81], v[156:159], v[224:227], v[78:81]
	v_mfma_i32_16x16x64_i8 v[74:77], v[164:167], v[224:227], v[74:77]
	v_mfma_i32_16x16x64_i8 v[118:121], v[168:171], v[196:199], v[118:121]
	v_mfma_i32_16x16x64_i8 v[114:117], v[186:189], v[196:199], v[114:117]
	v_mfma_i32_16x16x64_i8 v[102:105], v[168:171], v[204:207], v[102:105]
	v_mfma_i32_16x16x64_i8 v[98:101], v[186:189], v[204:207], v[98:101]
	v_mfma_i32_16x16x64_i8 v[86:89], v[168:171], v[212:215], v[86:89]
	v_mfma_i32_16x16x64_i8 v[82:85], v[186:189], v[212:215], v[82:85]
	v_mfma_i32_16x16x64_i8 v[70:73], v[168:171], v[220:223], v[70:73]
	v_mfma_i32_16x16x64_i8 v[66:69], v[186:189], v[220:223], v[66:69]
	v_mfma_i32_16x16x64_i8 v[118:121], v[182:185], v[200:203], v[118:121]
	v_mfma_i32_16x16x64_i8 v[114:117], v[190:193], v[200:203], v[114:117]
	v_mfma_i32_16x16x64_i8 v[102:105], v[182:185], v[208:211], v[102:105]
	v_mfma_i32_16x16x64_i8 v[98:101], v[190:193], v[208:211], v[98:101]
	v_mfma_i32_16x16x64_i8 v[86:89], v[182:185], v[216:219], v[86:89]
	v_mfma_i32_16x16x64_i8 v[82:85], v[190:193], v[216:219], v[82:85]
	v_mfma_i32_16x16x64_i8 v[70:73], v[182:185], v[224:227], v[70:73]
	v_mfma_i32_16x16x64_i8 v[66:69], v[190:193], v[224:227], v[66:69]
	s_setprio 0
	s_barrier
; #define PG8_STAGE(bufoff, gbase, voff) do { _Pragma("unroll") for (int _i = 0; _i < 2; ++_i) \
;         __builtin_amdgcn_global_load_lds((const unsigned*)((const char*)(gbase) + (voff)[_i]), (LAS unsigned*)(lds + (bufoff) + ldsw + _i * 8192), 16, 0, 0); } while (0)
; #define PG8_LDA(dst, b, h) do { _Pragma("unroll") for (int m = 0; m < 4; ++m) dst[m] = PG8_LD32(lds + PG8_SA(b, h) + aoff + m * 2048); } while (0)
; #define PG8_WAIT_V(n) asm volatile("s_waitcnt vmcnt(" #n ")" ::: "memory")
; #define PG8_WAIT_L(n) asm volatile("s_waitcnt lgkmcnt(" #n ")" ::: "memory")
; #define PG8_BAR __builtin_amdgcn_s_barrier()
; #define PG8_SCHED __builtin_amdgcn_sched_barrier(0)
; #define PG8_STA(bufoff, nextflag, h, koff) do { if constexpr (Sched::GATHER) { unsigned _o[2]; _o[0] = (nextflag) ? nxtA[h][0] : curA[h][0]; _o[1] = (nextflag) ? nxtA[h][1] : curA[h][1]; PG8_STAGE(bufoff, Ab + (koff), _o); } \
;         else { PG8_STAGE(bufoff, ((nextflag) ? nA : cA) + (size_t)(h) * hstep + (koff), voffA); } } while (0)
; template <class Epi, class Sched, bool ALIGN_EPI, int DT>
; __device__ __forceinline__ void gemm_phase(LAS unsigned char* lds, const int KB, const Sched& S, const Epi& E) {
;     ...
;             PG8_LDA(At, 1, 1); PG8_STAGE(PG8_SB(1, 0), b3, voffB); PG8_STAGE(PG8_SB(1, 1), b3 + hstep, voffB); PG8_STA(PG8_SA(1, 0), last, 0, k3);
;             PG8_WAIT_V(8); PG8_WAIT_L(0); PG8_BAR; PG8_MMA(1, 0, At, B0); PG8_MMA(1, 1, At, B1); PG8_BAR; PG8_SCHED;
;         }
;         if constexpr (ALIGN_EPI) { if (wr == 0) PG8_BAR; }
	s_add_i32 s36, s42, s5
	v_lshl_add_u64 v[228:229], v[228:229], 0, s[18:19]
	s_mov_b32 m0, s36
	ds_read_b128 v[196:199], v177 offset:49152
	ds_read_b128 v[200:203], v177 offset:50176
	ds_read_b128 v[204:207], v177 offset:51200
	ds_read_b128 v[208:211], v177 offset:52224
	ds_read_b128 v[212:215], v177 offset:53248
	ds_read_b128 v[216:219], v177 offset:54272
	ds_read_b128 v[220:223], v177 offset:55296
	ds_read_b128 v[224:227], v177 offset:56320
	global_load_lds_dwordx4 v[228:229], off
	s_add_i32 m0, s36, 0x2000
	s_add_u32 s36, s40, 0x40080
	v_lshl_add_u64 v[228:229], v[230:231], 0, s[18:19]
	s_addc_u32 s37, s41, 0
	s_add_i32 s40, s43, s5
	global_load_lds_dwordx4 v[228:229], off
	v_lshl_add_u64 v[228:229], s[36:37], 0, v[134:135]
	s_mov_b32 m0, s40
	s_nop 0
	global_load_lds_dwordx4 v[228:229], off
	v_lshl_add_u64 v[228:229], s[36:37], 0, v[132:133]
	s_add_i32 m0, s40, 0x2000
	s_nop 0
	global_load_lds_dwordx4 v[228:229], off
	v_lshl_add_u64 v[228:229], v[232:233], 0, s[18:19]
	s_mov_b32 m0, s55
	s_nop 0
	global_load_lds_dwordx4 v[228:229], off
	v_lshl_add_u64 v[228:229], v[234:235], 0, s[18:19]
	s_mov_b32 m0, s56
	s_nop 0
	global_load_lds_dwordx4 v[228:229], off
	s_waitcnt vmcnt(8)
	s_waitcnt lgkmcnt(0)
	s_barrier
	s_setprio 1
	v_mfma_i32_16x16x64_i8 v[62:65], v[152:155], v[196:199], v[62:65]
	v_mfma_i32_16x16x64_i8 v[58:61], v[160:163], v[196:199], v[58:61]
	v_mfma_i32_16x16x64_i8 v[46:49], v[152:155], v[204:207], v[46:49]
	v_mfma_i32_16x16x64_i8 v[42:45], v[160:163], v[204:207], v[42:45]
	v_mfma_i32_16x16x64_i8 v[30:33], v[152:155], v[212:215], v[30:33]
	v_mfma_i32_16x16x64_i8 v[26:29], v[160:163], v[212:215], v[26:29]
	v_mfma_i32_16x16x64_i8 v[6:9], v[152:155], v[220:223], v[6:9]
	v_mfma_i32_16x16x64_i8 v[2:5], v[160:163], v[220:223], v[2:5]
	v_mfma_i32_16x16x64_i8 v[62:65], v[156:159], v[200:203], v[62:65]
	v_mfma_i32_16x16x64_i8 v[58:61], v[164:167], v[200:203], v[58:61]
	v_mfma_i32_16x16x64_i8 v[46:49], v[156:159], v[208:211], v[46:49]
	v_mfma_i32_16x16x64_i8 v[42:45], v[164:167], v[208:211], v[42:45]
	v_mfma_i32_16x16x64_i8 v[30:33], v[156:159], v[216:219], v[30:33]
	v_mfma_i32_16x16x64_i8 v[26:29], v[164:167], v[216:219], v[26:29]
	v_mfma_i32_16x16x64_i8 v[6:9], v[156:159], v[224:227], v[6:9]
	v_mfma_i32_16x16x64_i8 v[2:5], v[164:167], v[224:227], v[2:5]
	v_mfma_i32_16x16x64_i8 v[54:57], v[168:171], v[196:199], v[54:57]
	v_mfma_i32_16x16x64_i8 v[50:53], v[186:189], v[196:199], v[50:53]
	v_mfma_i32_16x16x64_i8 v[38:41], v[168:171], v[204:207], v[38:41]
	v_mfma_i32_16x16x64_i8 v[34:37], v[186:189], v[204:207], v[34:37]
	v_mfma_i32_16x16x64_i8 v[14:17], v[168:171], v[212:215], v[14:17]
	v_mfma_i32_16x16x64_i8 v[10:13], v[186:189], v[212:215], v[10:13]
	v_mfma_i32_16x16x64_i8 v[22:25], v[168:171], v[220:223], v[22:25]
	v_mfma_i32_16x16x64_i8 v[18:21], v[186:189], v[220:223], v[18:21]
	v_mfma_i32_16x16x64_i8 v[54:57], v[182:185], v[200:203], v[54:57]
	v_mfma_i32_16x16x64_i8 v[50:53], v[190:193], v[200:203], v[50:53]
	v_mfma_i32_16x16x64_i8 v[38:41], v[182:185], v[208:211], v[38:41]
	v_mfma_i32_16x16x64_i8 v[34:37], v[190:193], v[208:211], v[34:37]
	v_mfma_i32_16x16x64_i8 v[14:17], v[182:185], v[216:219], v[14:17]
	v_mfma_i32_16x16x64_i8 v[10:13], v[190:193], v[216:219], v[10:13]
	v_mfma_i32_16x16x64_i8 v[22:25], v[182:185], v[224:227], v[22:25]
	v_mfma_i32_16x16x64_i8 v[18:21], v[190:193], v[224:227], v[18:21]
	s_setprio 0
	s_barrier
	s_add_i32 s67, s67, 2
	s_cmp_gt_u32 s67, 13
	s_mov_b64 s[36:37], s[38:39]
	s_cbranch_scc0 .LBB0_193
	s_and_b64 vcc, exec, s[20:21]
	s_cbranch_vccz .LBB0_196
	s_barrier

; #define PG8_STAGE(bufoff, gbase, voff) do { _Pragma("unroll") for (int _i = 0; _i < 2; ++_i) \
;         __builtin_amdgcn_global_load_lds((const unsigned*)((const char*)(gbase) + (voff)[_i]), (LAS unsigned*)(lds + (bufoff) + ldsw + _i * 8192), 16, 0, 0); } while (0)
; #define PG8_LDA(dst, b, h) do { _Pragma("unroll") for (int m = 0; m < 4; ++m) dst[m] = PG8_LD32(lds + PG8_SA(b, h) + aoff + m * 2048); } while (0)
; #define PG8_LDB(dst, b, h) do { _Pragma("unroll") for (int n = 0; n < 2; ++n) dst[n] = PG8_LD32(lds + PG8_SB(b, h) + boff + n * 2048); } while (0)
; #define PG8_WAIT_V(n) asm volatile("s_waitcnt vmcnt(" #n ")" ::: "memory")
; #define PG8_WAIT_L(n) asm volatile("s_waitcnt lgkmcnt(" #n ")" ::: "memory")
; #define PG8_BAR __builtin_amdgcn_s_barrier()
; #define PG8_SCHED __builtin_amdgcn_sched_barrier(0)
; #define PG8_STA(bufoff, nextflag, h, koff) do { if constexpr (Sched::GATHER) { unsigned _o[2]; _o[0] = (nextflag) ? nxtA[h][0] : curA[h][0]; _o[1] = (nextflag) ? nxtA[h][1] : curA[h][1]; PG8_STAGE(bufoff, Ab + (koff), _o); } \
;         else { PG8_STAGE(bufoff, ((nextflag) ? nA : cA) + (size_t)(h) * hstep + (koff), voffA); } } while (0)
; template <class Epi, class Sched, bool ALIGN_EPI, int DT>
; __device__ __forceinline__ void gemm_phase(LAS unsigned char* lds, const int KB, const Sched& S, const Epi& E) {
;     ...
;             PG8_LDB(B0, 0, 0); PG8_LDB(B1, 0, 1); PG8_SCHED; PG8_LDA(At, 0, 0); PG8_STA(PG8_SA(1, 1), false, 1, k1);
;             PG8_WAIT_V(8); PG8_WAIT_L(0); PG8_BAR; PG8_MMA(0, 0, At, B0); PG8_MMA(0, 1, At, B1); PG8_BAR; PG8_SCHED;
;             PG8_LDA(At, 0, 1); PG8_STAGE(PG8_SB(0, 0), b2, voffB); PG8_STAGE(PG8_SB(0, 1), b2 + hstep, voffB); PG8_STA(PG8_SA(0, 0), last, 0, k2);
;             PG8_WAIT_V(8); PG8_WAIT_L(0); PG8_BAR; PG8_MMA(1, 0, At, B0); PG8_MMA(1, 1, At, B1); PG8_BAR; PG8_SCHED;
.LBB0_1018:
	ds_read_b128 v[18:21], v193
	ds_read_b128 v[22:25], v193 offset:1024
	ds_read_b128 v[26:29], v193 offset:2048
	ds_read_b128 v[30:33], v193 offset:3072
	ds_read_b128 v[2:5], v195
	ds_read_b128 v[6:9], v195 offset:1024
	ds_read_b128 v[10:13], v195 offset:2048
	ds_read_b128 v[14:17], v195 offset:3072
	s_add_u32 s34, s38, 0x100
	s_addc_u32 s35, s39, 0
	s_add_u32 s68, s63, s38
	s_addc_u32 s69, s66, s39
	s_cmp_eq_u32 s67, 12
	s_cselect_b64 s[40:41], -1, 0
	s_and_b64 s[36:37], s[40:41], exec
	s_cselect_b32 s37, s21, s69
	s_cselect_b32 s36, s23, s68
	s_cselect_b32 s68, 0, s35
	s_cselect_b32 s69, 0, s34
	v_lshl_add_u64 v[222:223], v[178:179], 0, s[38:39]
	s_add_i32 m0, s29, 0xc000
	ds_read_b128 v[182:185], v196
	ds_read_b128 v[186:189], v196 offset:1024
	ds_read_b128 v[198:201], v196 offset:2048
	ds_read_b128 v[202:205], v196 offset:3072
	ds_read_b128 v[206:209], v196 offset:4096
	ds_read_b128 v[210:213], v196 offset:5120
	ds_read_b128 v[214:217], v196 offset:6144
	ds_read_b128 v[218:221], v196 offset:7168
	global_load_lds_dwordx4 v[222:223], off
	v_lshl_add_u64 v[222:223], v[180:181], 0, s[38:39]
	s_add_i32 m0, s29, 0xe000
	s_nop 0
	global_load_lds_dwordx4 v[222:223], off
	s_waitcnt vmcnt(8)
	s_waitcnt lgkmcnt(0)
	s_barrier
	s_setprio 1
	v_mfma_scale_f32_16x16x128_f8f6f4 v[158:161], v[18:25], v[182:189], v[158:161], v190, v190 op_sel_hi:[0,0,0]
	v_mfma_scale_f32_16x16x128_f8f6f4 v[154:157], v[26:33], v[182:189], v[154:157], v190, v190 op_sel_hi:[0,0,0]
	v_mfma_scale_f32_16x16x128_f8f6f4 v[150:153], v[18:25], v[198:205], v[150:153], v190, v190 op_sel_hi:[0,0,0]
	v_mfma_scale_f32_16x16x128_f8f6f4 v[142:145], v[26:33], v[198:205], v[142:145], v190, v190 op_sel_hi:[0,0,0]
	v_mfma_scale_f32_16x16x128_f8f6f4 v[134:137], v[18:25], v[206:213], v[134:137], v190, v190 op_sel_hi:[0,0,0]
	v_mfma_scale_f32_16x16x128_f8f6f4 v[126:129], v[26:33], v[206:213], v[126:129], v190, v190 op_sel_hi:[0,0,0]
	v_mfma_scale_f32_16x16x128_f8f6f4 v[118:121], v[18:25], v[214:221], v[118:121], v190, v190 op_sel_hi:[0,0,0]
	v_mfma_scale_f32_16x16x128_f8f6f4 v[110:113], v[26:33], v[214:221], v[110:113], v190, v190 op_sel_hi:[0,0,0]
	v_mfma_scale_f32_16x16x128_f8f6f4 v[146:149], v[2:9], v[182:189], v[146:149], v190, v190 op_sel_hi:[0,0,0]
	v_mfma_scale_f32_16x16x128_f8f6f4 v[138:141], v[10:17], v[182:189], v[138:141], v190, v190 op_sel_hi:[0,0,0]
	v_mfma_scale_f32_16x16x128_f8f6f4 v[130:133], v[2:9], v[198:205], v[130:133], v190, v190 op_sel_hi:[0,0,0]
	v_mfma_scale_f32_16x16x128_f8f6f4 v[122:125], v[10:17], v[198:205], v[122:125], v190, v190 op_sel_hi:[0,0,0]
	v_mfma_scale_f32_16x16x128_f8f6f4 v[114:117], v[2:9], v[206:213], v[114:117], v190, v190 op_sel_hi:[0,0,0]
	v_mfma_scale_f32_16x16x128_f8f6f4 v[106:109], v[10:17], v[206:213], v[106:109], v190, v190 op_sel_hi:[0,0,0]
	v_mfma_scale_f32_16x16x128_f8f6f4 v[102:105], v[2:9], v[214:221], v[102:105], v190, v190 op_sel_hi:[0,0,0]
	v_mfma_scale_f32_16x16x128_f8f6f4 v[98:101], v[10:17], v[214:221], v[98:101], v190, v190 op_sel_hi:[0,0,0]
	s_setprio 0
	s_barrier
	s_add_i32 s38, s53, s42
	v_lshl_add_u64 v[182:183], s[36:37], 0, v[162:163]
	s_mov_b32 m0, s38
	ds_read_b128 v[198:201], v196 offset:16384
	ds_read_b128 v[202:205], v196 offset:17408
	ds_read_b128 v[206:209], v196 offset:18432
	ds_read_b128 v[210:213], v196 offset:19456
	ds_read_b128 v[214:217], v196 offset:20480
	ds_read_b128 v[218:221], v196 offset:21504
	ds_read_b128 v[222:225], v196 offset:22528
	ds_read_b128 v[226:229], v196 offset:23552
	global_load_lds_dwordx4 v[182:183], off
	s_add_i32 m0, s38, 0x2000
	s_add_u32 s38, s36, 0x40000
	v_lshl_add_u64 v[184:185], s[36:37], 0, v[164:165]
	s_addc_u32 s39, s37, 0
	s_add_i32 s70, s54, s42
	global_load_lds_dwordx4 v[184:185], off
	v_lshl_add_u64 v[186:187], s[38:39], 0, v[162:163]
	s_mov_b32 m0, s70
	s_nop 0
	global_load_lds_dwordx4 v[186:187], off
	v_lshl_add_u64 v[186:187], s[38:39], 0, v[164:165]
	s_add_i32 m0, s70, 0x2000
	s_and_b64 s[38:39], s[6:7], s[40:41]
	s_and_b64 s[38:39], s[38:39], exec
	s_cselect_b32 s38, s24, s30
	s_cselect_b32 s39, s25, s31
	s_add_u32 s38, s38, s69
	s_addc_u32 s39, s39, s68
	global_load_lds_dwordx4 v[186:187], off
	v_lshl_add_u64 v[186:187], s[38:39], 0, v[166:167]
	s_mov_b32 m0, s29
	v_lshl_add_u64 v[188:189], s[38:39], 0, v[168:169]
	global_load_lds_dwordx4 v[186:187], off
	s_mov_b32 m0, s43
	s_nop 0
	global_load_lds_dwordx4 v[188:189], off
	s_waitcnt vmcnt(8)
	s_waitcnt lgkmcnt(0)
	s_barrier
	s_setprio 1
	v_mfma_scale_f32_16x16x128_f8f6f4 v[94:97], v[18:25], v[198:205], v[94:97], v190, v190 op_sel_hi:[0,0,0]
	v_mfma_scale_f32_16x16x128_f8f6f4 v[90:93], v[26:33], v[198:205], v[90:93], v190, v190 op_sel_hi:[0,0,0]
	v_mfma_scale_f32_16x16x128_f8f6f4 v[86:89], v[18:25], v[206:213], v[86:89], v190, v190 op_sel_hi:[0,0,0]
	v_mfma_scale_f32_16x16x128_f8f6f4 v[78:81], v[26:33], v[206:213], v[78:81], v190, v190 op_sel_hi:[0,0,0]
	v_mfma_scale_f32_16x16x128_f8f6f4 v[62:65], v[18:25], v[214:221], v[62:65], v190, v190 op_sel_hi:[0,0,0]
	v_mfma_scale_f32_16x16x128_f8f6f4 v[54:57], v[26:33], v[214:221], v[54:57], v190, v190 op_sel_hi:[0,0,0]
	v_mfma_scale_f32_16x16x128_f8f6f4 v[46:49], v[18:25], v[222:229], v[46:49], v190, v190 op_sel_hi:[0,0,0]
	v_mfma_scale_f32_16x16x128_f8f6f4 v[38:41], v[26:33], v[222:229], v[38:41], v190, v190 op_sel_hi:[0,0,0]
	v_mfma_scale_f32_16x16x128_f8f6f4 v[82:85], v[2:9], v[198:205], v[82:85], v190, v190 op_sel_hi:[0,0,0]
	v_mfma_scale_f32_16x16x128_f8f6f4 v[74:77], v[10:17], v[198:205], v[74:77], v190, v190 op_sel_hi:[0,0,0]
	v_mfma_scale_f32_16x16x128_f8f6f4 v[58:61], v[2:9], v[206:213], v[58:61], v190, v190 op_sel_hi:[0,0,0]
	v_mfma_scale_f32_16x16x128_f8f6f4 v[50:53], v[10:17], v[206:213], v[50:53], v190, v190 op_sel_hi:[0,0,0]
	v_mfma_scale_f32_16x16x128_f8f6f4 v[42:45], v[2:9], v[214:221], v[42:45], v190, v190 op_sel_hi:[0,0,0]
	v_mfma_scale_f32_16x16x128_f8f6f4 v[34:37], v[10:17], v[214:221], v[34:37], v190, v190 op_sel_hi:[0,0,0]
	v_mfma_scale_f32_16x16x128_f8f6f4 v[70:73], v[2:9], v[222:229], v[70:73], v190, v190 op_sel_hi:[0,0,0]
	v_mfma_scale_f32_16x16x128_f8f6f4 v[66:69], v[10:17], v[222:229], v[66:69], v190, v190 op_sel_hi:[0,0,0]
	s_setprio 0
	s_barrier
; #define PG8_STAGE(bufoff, gbase, voff) do { _Pragma("unroll") for (int _i = 0; _i < 2; ++_i) \
;         __builtin_amdgcn_global_load_lds((const unsigned*)((const char*)(gbase) + (voff)[_i]), (LAS unsigned*)(lds + (bufoff) + ldsw + _i * 8192), 16, 0, 0); } while (0)
; #define PG8_LDA(dst, b, h) do { _Pragma("unroll") for (int m = 0; m < 4; ++m) dst[m] = PG8_LD32(lds + PG8_SA(b, h) + aoff + m * 2048); } while (0)
; #define PG8_LDB(dst, b, h) do { _Pragma("unroll") for (int n = 0; n < 2; ++n) dst[n] = PG8_LD32(lds + PG8_SB(b, h) + boff + n * 2048); } while (0)
; #define PG8_WAIT_V(n) asm volatile("s_waitcnt vmcnt(" #n ")" ::: "memory")
; #define PG8_WAIT_L(n) asm volatile("s_waitcnt lgkmcnt(" #n ")" ::: "memory")
; #define PG8_BAR __builtin_amdgcn_s_barrier()
; #define PG8_SCHED __builtin_amdgcn_sched_barrier(0)
; #define PG8_STA(bufoff, nextflag, h, koff) do { if constexpr (Sched::GATHER) { unsigned _o[2]; _o[0] = (nextflag) ? nxtA[h][0] : curA[h][0]; _o[1] = (nextflag) ? nxtA[h][1] : curA[h][1]; PG8_STAGE(bufoff, Ab + (koff), _o); } \
;         else { PG8_STAGE(bufoff, ((nextflag) ? nA : cA) + (size_t)(h) * hstep + (koff), voffA); } } while (0)
; template <class Epi, class Sched, bool ALIGN_EPI, int DT>
; __device__ __forceinline__ void gemm_phase(LAS unsigned char* lds, const int KB, const Sched& S, const Epi& E) {
;     ...
;             PG8_LDB(B0, 1, 0); PG8_LDB(B1, 1, 1); PG8_SCHED; PG8_LDA(At, 1, 0); PG8_STA(PG8_SA(0, 1), last, 1, k2);
;             PG8_WAIT_V(8); PG8_WAIT_L(0); PG8_BAR; PG8_MMA(0, 0, At, B0); PG8_MMA(0, 1, At, B1); PG8_BAR; PG8_SCHED;
;             PG8_LDA(At, 1, 1); PG8_STAGE(PG8_SB(1, 0), b3, voffB); PG8_STAGE(PG8_SB(1, 1), b3 + hstep, voffB); PG8_STA(PG8_SA(1, 0), last, 0, k3);
;             PG8_WAIT_V(8); PG8_WAIT_L(0); PG8_BAR; PG8_MMA(1, 0, At, B0); PG8_MMA(1, 1, At, B1); PG8_BAR; PG8_SCHED;
;         }
;         if constexpr (ALIGN_EPI) { if (wr == 0) PG8_BAR; }
	s_add_i32 s40, 0, 0x18000
	s_add_i32 s41, 0, 0x1c000
	v_add_u32_e32 v14, s40, v191
	v_add_u32_e32 v30, s41, v191
	ds_read_b128 v[2:5], v14
	ds_read_b128 v[6:9], v14 offset:1024
	ds_read_b128 v[10:13], v14 offset:2048
	ds_read_b128 v[14:17], v14 offset:3072
	ds_read_b128 v[18:21], v30
	ds_read_b128 v[22:25], v30 offset:1024
	ds_read_b128 v[26:29], v30 offset:2048
	ds_read_b128 v[30:33], v30 offset:3072
	s_add_u32 s38, s38, 0x40000
	s_addc_u32 s39, s39, 0
	s_mov_b32 m0, s44
	v_lshl_add_u64 v[230:231], s[38:39], 0, v[166:167]
	ds_read_b128 v[198:201], v196 offset:32768
	ds_read_b128 v[202:205], v196 offset:33792
	ds_read_b128 v[206:209], v196 offset:34816
	ds_read_b128 v[210:213], v196 offset:35840
	ds_read_b128 v[214:217], v196 offset:36864
	ds_read_b128 v[218:221], v196 offset:37888
	ds_read_b128 v[222:225], v196 offset:38912
	ds_read_b128 v[226:229], v196 offset:39936
	global_load_lds_dwordx4 v[230:231], off
	v_lshl_add_u64 v[230:231], s[38:39], 0, v[168:169]
	s_mov_b32 m0, s45
	s_nop 0
	global_load_lds_dwordx4 v[230:231], off
	s_waitcnt vmcnt(8)
	s_waitcnt lgkmcnt(0)
	s_barrier
	s_setprio 1
	v_mfma_scale_f32_16x16x128_f8f6f4 v[158:161], v[2:9], v[198:205], v[158:161], v190, v190 op_sel_hi:[0,0,0]
	v_mfma_scale_f32_16x16x128_f8f6f4 v[154:157], v[10:17], v[198:205], v[154:157], v190, v190 op_sel_hi:[0,0,0]
	v_mfma_scale_f32_16x16x128_f8f6f4 v[150:153], v[2:9], v[206:213], v[150:153], v190, v190 op_sel_hi:[0,0,0]
	v_mfma_scale_f32_16x16x128_f8f6f4 v[142:145], v[10:17], v[206:213], v[142:145], v190, v190 op_sel_hi:[0,0,0]
	v_mfma_scale_f32_16x16x128_f8f6f4 v[134:137], v[2:9], v[214:221], v[134:137], v190, v190 op_sel_hi:[0,0,0]
	v_mfma_scale_f32_16x16x128_f8f6f4 v[126:129], v[10:17], v[214:221], v[126:129], v190, v190 op_sel_hi:[0,0,0]
	v_mfma_scale_f32_16x16x128_f8f6f4 v[118:121], v[2:9], v[222:229], v[118:121], v190, v190 op_sel_hi:[0,0,0]
	v_mfma_scale_f32_16x16x128_f8f6f4 v[110:113], v[10:17], v[222:229], v[110:113], v190, v190 op_sel_hi:[0,0,0]
	v_mfma_scale_f32_16x16x128_f8f6f4 v[146:149], v[18:25], v[198:205], v[146:149], v190, v190 op_sel_hi:[0,0,0]
	v_mfma_scale_f32_16x16x128_f8f6f4 v[138:141], v[26:33], v[198:205], v[138:141], v190, v190 op_sel_hi:[0,0,0]
	v_mfma_scale_f32_16x16x128_f8f6f4 v[130:133], v[18:25], v[206:213], v[130:133], v190, v190 op_sel_hi:[0,0,0]
	v_mfma_scale_f32_16x16x128_f8f6f4 v[122:125], v[26:33], v[206:213], v[122:125], v190, v190 op_sel_hi:[0,0,0]
	v_mfma_scale_f32_16x16x128_f8f6f4 v[114:117], v[18:25], v[214:221], v[114:117], v190, v190 op_sel_hi:[0,0,0]
	v_mfma_scale_f32_16x16x128_f8f6f4 v[106:109], v[26:33], v[214:221], v[106:109], v190, v190 op_sel_hi:[0,0,0]
	v_mfma_scale_f32_16x16x128_f8f6f4 v[102:105], v[18:25], v[222:229], v[102:105], v190, v190 op_sel_hi:[0,0,0]
	v_mfma_scale_f32_16x16x128_f8f6f4 v[98:101], v[26:33], v[222:229], v[98:101], v190, v190 op_sel_hi:[0,0,0]
	s_setprio 0
	s_barrier
	s_add_i32 s38, s40, s42
	v_lshl_add_u64 v[182:183], v[182:183], 0, s[10:11]
	s_mov_b32 m0, s38
	ds_read_b128 v[198:201], v196 offset:49152
	ds_read_b128 v[202:205], v196 offset:50176
	ds_read_b128 v[206:209], v196 offset:51200
	ds_read_b128 v[210:213], v196 offset:52224
	ds_read_b128 v[214:217], v196 offset:53248
	ds_read_b128 v[218:221], v196 offset:54272
	ds_read_b128 v[222:225], v196 offset:55296
	ds_read_b128 v[226:229], v196 offset:56320
	global_load_lds_dwordx4 v[182:183], off
	s_add_i32 m0, s38, 0x2000
	s_add_u32 s36, s36, 0x40080
	v_lshl_add_u64 v[182:183], v[184:185], 0, s[10:11]
	s_addc_u32 s37, s37, 0
	s_add_i32 s38, s41, s42
	global_load_lds_dwordx4 v[182:183], off
	v_lshl_add_u64 v[182:183], s[36:37], 0, v[162:163]
	s_mov_b32 m0, s38
	s_nop 0
	global_load_lds_dwordx4 v[182:183], off
	v_lshl_add_u64 v[182:183], s[36:37], 0, v[164:165]
	s_add_i32 m0, s38, 0x2000
	s_nop 0
	global_load_lds_dwordx4 v[182:183], off
	v_lshl_add_u64 v[182:183], v[186:187], 0, s[10:11]
	s_mov_b32 m0, s47
	s_nop 0
	global_load_lds_dwordx4 v[182:183], off
	v_lshl_add_u64 v[182:183], v[188:189], 0, s[10:11]
	s_mov_b32 m0, s49
	s_nop 0
	global_load_lds_dwordx4 v[182:183], off
	s_waitcnt vmcnt(8)
	s_waitcnt lgkmcnt(0)
	s_barrier
	s_setprio 1
	v_mfma_scale_f32_16x16x128_f8f6f4 v[94:97], v[2:9], v[198:205], v[94:97], v190, v190 op_sel_hi:[0,0,0]
	v_mfma_scale_f32_16x16x128_f8f6f4 v[90:93], v[10:17], v[198:205], v[90:93], v190, v190 op_sel_hi:[0,0,0]
	v_mfma_scale_f32_16x16x128_f8f6f4 v[86:89], v[2:9], v[206:213], v[86:89], v190, v190 op_sel_hi:[0,0,0]
	v_mfma_scale_f32_16x16x128_f8f6f4 v[78:81], v[10:17], v[206:213], v[78:81], v190, v190 op_sel_hi:[0,0,0]
	v_mfma_scale_f32_16x16x128_f8f6f4 v[62:65], v[2:9], v[214:221], v[62:65], v190, v190 op_sel_hi:[0,0,0]
	v_mfma_scale_f32_16x16x128_f8f6f4 v[54:57], v[10:17], v[214:221], v[54:57], v190, v190 op_sel_hi:[0,0,0]
	v_mfma_scale_f32_16x16x128_f8f6f4 v[46:49], v[2:9], v[222:229], v[46:49], v190, v190 op_sel_hi:[0,0,0]
	v_mfma_scale_f32_16x16x128_f8f6f4 v[38:41], v[10:17], v[222:229], v[38:41], v190, v190 op_sel_hi:[0,0,0]
	v_mfma_scale_f32_16x16x128_f8f6f4 v[82:85], v[18:25], v[198:205], v[82:85], v190, v190 op_sel_hi:[0,0,0]
	v_mfma_scale_f32_16x16x128_f8f6f4 v[74:77], v[26:33], v[198:205], v[74:77], v190, v190 op_sel_hi:[0,0,0]
	v_mfma_scale_f32_16x16x128_f8f6f4 v[58:61], v[18:25], v[206:213], v[58:61], v190, v190 op_sel_hi:[0,0,0]
	v_mfma_scale_f32_16x16x128_f8f6f4 v[50:53], v[26:33], v[206:213], v[50:53], v190, v190 op_sel_hi:[0,0,0]
	v_mfma_scale_f32_16x16x128_f8f6f4 v[42:45], v[18:25], v[214:221], v[42:45], v190, v190 op_sel_hi:[0,0,0]
	v_mfma_scale_f32_16x16x128_f8f6f4 v[34:37], v[26:33], v[214:221], v[34:37], v190, v190 op_sel_hi:[0,0,0]
	v_mfma_scale_f32_16x16x128_f8f6f4 v[70:73], v[18:25], v[222:229], v[70:73], v190, v190 op_sel_hi:[0,0,0]
	v_mfma_scale_f32_16x16x128_f8f6f4 v[66:69], v[26:33], v[222:229], v[66:69], v190, v190 op_sel_hi:[0,0,0]
	s_setprio 0
	s_barrier
	s_add_i32 s67, s67, 2
	s_cmp_gt_u32 s67, 13
	s_mov_b64 s[38:39], s[34:35]
	s_cbranch_scc0 .LBB0_1018
	s_and_b64 vcc, exec, s[12:13]
	s_cbranch_vccz .LBB0_1021
	s_barrier

; #define PG8_STAGE(bufoff, gbase, voff) do { _Pragma("unroll") for (int _i = 0; _i < 2; ++_i) \
;         __builtin_amdgcn_global_load_lds((const unsigned*)((const char*)(gbase) + (voff)[_i]), (LAS unsigned*)(lds + (bufoff) + ldsw + _i * 8192), 16, 0, 0); } while (0)
; #define PG8_LDA(dst, b, h) do { _Pragma("unroll") for (int m = 0; m < 4; ++m) dst[m] = PG8_LD32(lds + PG8_SA(b, h) + aoff + m * 2048); } while (0)
; #define PG8_LDB(dst, b, h) do { _Pragma("unroll") for (int n = 0; n < 2; ++n) dst[n] = PG8_LD32(lds + PG8_SB(b, h) + boff + n * 2048); } while (0)
; #define PG8_WAIT_V(n) asm volatile("s_waitcnt vmcnt(" #n ")" ::: "memory")
; #define PG8_WAIT_L(n) asm volatile("s_waitcnt lgkmcnt(" #n ")" ::: "memory")
; #define PG8_BAR __builtin_amdgcn_s_barrier()
; #define PG8_SCHED __builtin_amdgcn_sched_barrier(0)
; #define PG8_STA(bufoff, nextflag, h, koff) do { if constexpr (Sched::GATHER) { unsigned _o[2]; _o[0] = (nextflag) ? nxtA[h][0] : curA[h][0]; _o[1] = (nextflag) ? nxtA[h][1] : curA[h][1]; PG8_STAGE(bufoff, Ab + (koff), _o); } \
;         else { PG8_STAGE(bufoff, ((nextflag) ? nA : cA) + (size_t)(h) * hstep + (koff), voffA); } } while (0)
; template <class Epi, class Sched, bool ALIGN_EPI, int DT>
; __device__ __forceinline__ void gemm_phase(LAS unsigned char* lds, const int KB, const Sched& S, const Epi& E) {
;     ...
;             PG8_LDB(B0, 0, 0); PG8_LDB(B1, 0, 1); PG8_SCHED; PG8_LDA(At, 0, 0); PG8_STA(PG8_SA(1, 1), false, 1, k1);
;             PG8_WAIT_V(8); PG8_WAIT_L(0); PG8_BAR; PG8_MMA(0, 0, At, B0); PG8_MMA(0, 1, At, B1); PG8_BAR; PG8_SCHED;
;             PG8_LDA(At, 0, 1); PG8_STAGE(PG8_SB(0, 0), b2, voffB); PG8_STAGE(PG8_SB(0, 1), b2 + hstep, voffB); PG8_STA(PG8_SA(0, 0), last, 0, k2);
;             PG8_WAIT_V(8); PG8_WAIT_L(0); PG8_BAR; PG8_MMA(1, 0, At, B0); PG8_MMA(1, 1, At, B1); PG8_BAR; PG8_SCHED;
.LBB0_1154:
	ds_read_b128 v[70:73], v167
	ds_read_b128 v[156:159], v167 offset:1024
	ds_read_b128 v[160:163], v167 offset:2048
	ds_read_b128 v[172:175], v167 offset:3072
	ds_read_b128 v[176:179], v168
	ds_read_b128 v[180:183], v168 offset:1024
	ds_read_b128 v[184:187], v168 offset:2048
	ds_read_b128 v[188:191], v168 offset:3072
	s_add_u32 s30, s28, 0x100
	s_addc_u32 s31, s29, 0
	s_add_u32 s63, s56, s28
	s_addc_u32 s66, s57, s29
	s_cmp_eq_u32 s62, 12
	s_cselect_b64 s[36:37], -1, 0
	s_and_b64 s[34:35], s[36:37], exec
	s_cselect_b32 s67, 0, s30
	s_cselect_b32 s35, s17, s66
	s_cselect_b32 s34, s19, s63
	v_lshl_add_u64 v[192:193], v[66:67], 0, s[28:29]
	s_add_i32 m0, s25, 0xc000
	ds_read_b128 v[196:199], v169
	ds_read_b128 v[200:203], v169 offset:1024
	ds_read_b128 v[204:207], v169 offset:2048
	ds_read_b128 v[208:211], v169 offset:3072
	ds_read_b128 v[212:215], v169 offset:4096
	ds_read_b128 v[216:219], v169 offset:5120
	ds_read_b128 v[220:223], v169 offset:6144
	ds_read_b128 v[224:227], v169 offset:7168
	global_load_lds_dwordx4 v[192:193], off
	v_lshl_add_u64 v[192:193], v[68:69], 0, s[28:29]
	s_add_i32 m0, s25, 0xe000
	s_nop 0
	global_load_lds_dwordx4 v[192:193], off
	s_waitcnt vmcnt(8)
	s_waitcnt lgkmcnt(0)
	s_barrier
	s_setprio 1
	v_mfma_i32_16x16x64_i8 v[134:137], v[70:73], v[196:199], v[134:137]
	v_mfma_i32_16x16x64_i8 v[126:129], v[160:163], v[196:199], v[126:129]
	v_mfma_i32_16x16x64_i8 v[118:121], v[70:73], v[204:207], v[118:121]
	v_mfma_i32_16x16x64_i8 v[110:113], v[160:163], v[204:207], v[110:113]
	v_mfma_i32_16x16x64_i8 v[102:105], v[70:73], v[212:215], v[102:105]
	v_mfma_i32_16x16x64_i8 v[94:97], v[160:163], v[212:215], v[94:97]
	v_mfma_i32_16x16x64_i8 v[86:89], v[70:73], v[220:223], v[86:89]
	v_mfma_i32_16x16x64_i8 v[78:81], v[160:163], v[220:223], v[78:81]
	v_mfma_i32_16x16x64_i8 v[134:137], v[156:159], v[200:203], v[134:137]
	v_mfma_i32_16x16x64_i8 v[126:129], v[172:175], v[200:203], v[126:129]
	v_mfma_i32_16x16x64_i8 v[118:121], v[156:159], v[208:211], v[118:121]
	v_mfma_i32_16x16x64_i8 v[110:113], v[172:175], v[208:211], v[110:113]
	v_mfma_i32_16x16x64_i8 v[102:105], v[156:159], v[216:219], v[102:105]
	v_mfma_i32_16x16x64_i8 v[94:97], v[172:175], v[216:219], v[94:97]
	v_mfma_i32_16x16x64_i8 v[86:89], v[156:159], v[224:227], v[86:89]
	v_mfma_i32_16x16x64_i8 v[78:81], v[172:175], v[224:227], v[78:81]
	v_mfma_i32_16x16x64_i8 v[130:133], v[176:179], v[196:199], v[130:133]
	v_mfma_i32_16x16x64_i8 v[122:125], v[184:187], v[196:199], v[122:125]
	v_mfma_i32_16x16x64_i8 v[114:117], v[176:179], v[204:207], v[114:117]
	v_mfma_i32_16x16x64_i8 v[106:109], v[184:187], v[204:207], v[106:109]
	v_mfma_i32_16x16x64_i8 v[98:101], v[176:179], v[212:215], v[98:101]
	v_mfma_i32_16x16x64_i8 v[90:93], v[184:187], v[212:215], v[90:93]
	v_mfma_i32_16x16x64_i8 v[82:85], v[176:179], v[220:223], v[82:85]
	v_mfma_i32_16x16x64_i8 v[74:77], v[184:187], v[220:223], v[74:77]
	v_mfma_i32_16x16x64_i8 v[130:133], v[180:183], v[200:203], v[130:133]
	v_mfma_i32_16x16x64_i8 v[122:125], v[188:191], v[200:203], v[122:125]
	v_mfma_i32_16x16x64_i8 v[114:117], v[180:183], v[208:211], v[114:117]
	v_mfma_i32_16x16x64_i8 v[106:109], v[188:191], v[208:211], v[106:109]
	v_mfma_i32_16x16x64_i8 v[98:101], v[180:183], v[216:219], v[98:101]
	v_mfma_i32_16x16x64_i8 v[90:93], v[188:191], v[216:219], v[90:93]
	v_mfma_i32_16x16x64_i8 v[82:85], v[180:183], v[224:227], v[82:85]
	v_mfma_i32_16x16x64_i8 v[74:77], v[188:191], v[224:227], v[74:77]
	s_setprio 0
	s_barrier
	s_add_i32 s28, s49, s38
	v_lshl_add_u64 v[192:193], s[34:35], 0, v[140:141]
	s_mov_b32 m0, s28
	ds_read_b128 v[196:199], v169 offset:16384
	ds_read_b128 v[200:203], v169 offset:17408
	ds_read_b128 v[204:207], v169 offset:18432
	ds_read_b128 v[208:211], v169 offset:19456
	ds_read_b128 v[212:215], v169 offset:20480
	ds_read_b128 v[216:219], v169 offset:21504
	ds_read_b128 v[220:223], v169 offset:22528
	ds_read_b128 v[224:227], v169 offset:23552
	global_load_lds_dwordx4 v[192:193], off
	s_add_i32 m0, s28, 0x2000
	s_add_u32 s28, s34, 0x40000
	v_lshl_add_u64 v[228:229], s[34:35], 0, v[138:139]
	s_addc_u32 s29, s35, 0
	s_add_i32 s63, s52, s38
	global_load_lds_dwordx4 v[228:229], off
	v_lshl_add_u64 v[230:231], s[28:29], 0, v[140:141]
	s_mov_b32 m0, s63
	s_nop 0
	global_load_lds_dwordx4 v[230:231], off
	v_lshl_add_u64 v[230:231], s[28:29], 0, v[138:139]
	s_add_i32 m0, s63, 0x2000
	s_and_b64 s[28:29], s[6:7], s[36:37]
	s_and_b64 s[28:29], s[28:29], exec
	s_cselect_b32 s28, s20, s26
	s_cselect_b32 s29, s21, s27
	s_add_u32 s28, s28, s67
	s_addc_u32 s29, s29, 0
	global_load_lds_dwordx4 v[230:231], off
	v_lshl_add_u64 v[230:231], s[28:29], 0, v[142:143]
	s_mov_b32 m0, s25
	v_lshl_add_u64 v[232:233], s[28:29], 0, v[144:145]
	global_load_lds_dwordx4 v[230:231], off
	s_mov_b32 m0, s41
	s_nop 0
	global_load_lds_dwordx4 v[232:233], off
	s_waitcnt vmcnt(8)
	s_waitcnt lgkmcnt(0)
	s_barrier
; #define PG8_LDA(dst, b, h) do { _Pragma("unroll") for (int m = 0; m < 4; ++m) dst[m] = PG8_LD32(lds + PG8_SA(b, h) + aoff + m * 2048); } while (0)
; #define PG8_LDB(dst, b, h) do { _Pragma("unroll") for (int n = 0; n < 2; ++n) dst[n] = PG8_LD32(lds + PG8_SB(b, h) + boff + n * 2048); } while (0)
; #define PG8_WAIT_V(n) asm volatile("s_waitcnt vmcnt(" #n ")" ::: "memory")
; #define PG8_WAIT_L(n) asm volatile("s_waitcnt lgkmcnt(" #n ")" ::: "memory")
; #define PG8_BAR __builtin_amdgcn_s_barrier()
; #define PG8_SCHED __builtin_amdgcn_sched_barrier(0)
; #define PG8_STA(bufoff, nextflag, h, koff) do { if constexpr (Sched::GATHER) { unsigned _o[2]; _o[0] = (nextflag) ? nxtA[h][0] : curA[h][0]; _o[1] = (nextflag) ? nxtA[h][1] : curA[h][1]; PG8_STAGE(bufoff, Ab + (koff), _o); } \
;         else { PG8_STAGE(bufoff, ((nextflag) ? nA : cA) + (size_t)(h) * hstep + (koff), voffA); } } while (0)
; template <class Epi, class Sched, bool ALIGN_EPI, int DT>
; __device__ __forceinline__ void gemm_phase(LAS unsigned char* lds, const int KB, const Sched& S, const Epi& E) {
;     ...
;             PG8_WAIT_V(8); PG8_WAIT_L(0); PG8_BAR; PG8_MMA(1, 0, At, B0); PG8_MMA(1, 1, At, B1); PG8_BAR; PG8_SCHED;
;             PG8_LDB(B0, 1, 0); PG8_LDB(B1, 1, 1); PG8_SCHED; PG8_LDA(At, 1, 0); PG8_STA(PG8_SA(0, 1), last, 1, k2);
;             PG8_WAIT_V(8); PG8_WAIT_L(0); PG8_BAR; PG8_MMA(0, 0, At, B0); PG8_MMA(0, 1, At, B1); PG8_BAR; PG8_SCHED;
	s_setprio 1
	v_mfma_i32_16x16x64_i8 v[62:65], v[70:73], v[196:199], v[62:65]
	v_mfma_i32_16x16x64_i8 v[54:57], v[160:163], v[196:199], v[54:57]
	v_mfma_i32_16x16x64_i8 v[46:49], v[70:73], v[204:207], v[46:49]
	v_mfma_i32_16x16x64_i8 v[38:41], v[160:163], v[204:207], v[38:41]
	v_mfma_i32_16x16x64_i8 v[30:33], v[70:73], v[212:215], v[30:33]
	v_mfma_i32_16x16x64_i8 v[22:25], v[160:163], v[212:215], v[22:25]
	v_mfma_i32_16x16x64_i8 v[6:9], v[70:73], v[220:223], v[6:9]
	v_mfma_i32_16x16x64_i8 v[2:5], v[160:163], v[220:223], v[2:5]
	v_mfma_i32_16x16x64_i8 v[62:65], v[156:159], v[200:203], v[62:65]
	v_mfma_i32_16x16x64_i8 v[54:57], v[172:175], v[200:203], v[54:57]
	v_mfma_i32_16x16x64_i8 v[46:49], v[156:159], v[208:211], v[46:49]
	v_mfma_i32_16x16x64_i8 v[38:41], v[172:175], v[208:211], v[38:41]
	v_mfma_i32_16x16x64_i8 v[30:33], v[156:159], v[216:219], v[30:33]
	v_mfma_i32_16x16x64_i8 v[22:25], v[172:175], v[216:219], v[22:25]
	v_mfma_i32_16x16x64_i8 v[6:9], v[156:159], v[224:227], v[6:9]
	v_mfma_i32_16x16x64_i8 v[2:5], v[172:175], v[224:227], v[2:5]
	v_mfma_i32_16x16x64_i8 v[58:61], v[176:179], v[196:199], v[58:61]
	v_mfma_i32_16x16x64_i8 v[50:53], v[184:187], v[196:199], v[50:53]
	v_mfma_i32_16x16x64_i8 v[42:45], v[176:179], v[204:207], v[42:45]
	v_mfma_i32_16x16x64_i8 v[34:37], v[184:187], v[204:207], v[34:37]
	v_mfma_i32_16x16x64_i8 v[26:29], v[176:179], v[212:215], v[26:29]
	v_mfma_i32_16x16x64_i8 v[18:21], v[184:187], v[212:215], v[18:21]
	v_mfma_i32_16x16x64_i8 v[14:17], v[176:179], v[220:223], v[14:17]
	v_mfma_i32_16x16x64_i8 v[10:13], v[184:187], v[220:223], v[10:13]
	v_mfma_i32_16x16x64_i8 v[58:61], v[180:183], v[200:203], v[58:61]
	v_mfma_i32_16x16x64_i8 v[50:53], v[188:191], v[200:203], v[50:53]
	v_mfma_i32_16x16x64_i8 v[42:45], v[180:183], v[208:211], v[42:45]
	v_mfma_i32_16x16x64_i8 v[34:37], v[188:191], v[208:211], v[34:37]
	v_mfma_i32_16x16x64_i8 v[26:29], v[180:183], v[216:219], v[26:29]
	v_mfma_i32_16x16x64_i8 v[18:21], v[188:191], v[216:219], v[18:21]
	v_mfma_i32_16x16x64_i8 v[14:17], v[180:183], v[224:227], v[14:17]
	v_mfma_i32_16x16x64_i8 v[10:13], v[188:191], v[224:227], v[10:13]
	s_setprio 0
	s_barrier
	s_add_i32 s36, 0, 0x18000
	v_add_u32_e32 v1, s36, v165
	s_add_i32 s37, 0, 0x1c000
	ds_read_b128 v[70:73], v1
	ds_read_b128 v[156:159], v1 offset:1024
	ds_read_b128 v[160:163], v1 offset:2048
	ds_read_b128 v[172:175], v1 offset:3072
	v_add_u32_e32 v1, s37, v165
	ds_read_b128 v[176:179], v1
	ds_read_b128 v[180:183], v1 offset:1024
	ds_read_b128 v[184:187], v1 offset:2048
	ds_read_b128 v[188:191], v1 offset:3072
	s_add_u32 s28, s28, 0x40000
	s_addc_u32 s29, s29, 0
	s_mov_b32 m0, s42
	v_lshl_add_u64 v[234:235], s[28:29], 0, v[142:143]
	ds_read_b128 v[196:199], v169 offset:32768
	ds_read_b128 v[200:203], v169 offset:33792
	ds_read_b128 v[204:207], v169 offset:34816
	ds_read_b128 v[208:211], v169 offset:35840
	ds_read_b128 v[212:215], v169 offset:36864
	ds_read_b128 v[216:219], v169 offset:37888
	ds_read_b128 v[220:223], v169 offset:38912
	ds_read_b128 v[224:227], v169 offset:39936
	global_load_lds_dwordx4 v[234:235], off
	v_lshl_add_u64 v[234:235], s[28:29], 0, v[144:145]
	s_mov_b32 m0, s43
	s_nop 0
	global_load_lds_dwordx4 v[234:235], off
	s_waitcnt vmcnt(8)
	s_waitcnt lgkmcnt(0)
	s_barrier
	s_setprio 1
	v_mfma_i32_16x16x64_i8 v[134:137], v[70:73], v[196:199], v[134:137]
	v_mfma_i32_16x16x64_i8 v[126:129], v[160:163], v[196:199], v[126:129]
	v_mfma_i32_16x16x64_i8 v[118:121], v[70:73], v[204:207], v[118:121]
	v_mfma_i32_16x16x64_i8 v[110:113], v[160:163], v[204:207], v[110:113]
	v_mfma_i32_16x16x64_i8 v[102:105], v[70:73], v[212:215], v[102:105]
	v_mfma_i32_16x16x64_i8 v[94:97], v[160:163], v[212:215], v[94:97]
	v_mfma_i32_16x16x64_i8 v[86:89], v[70:73], v[220:223], v[86:89]
	v_mfma_i32_16x16x64_i8 v[78:81], v[160:163], v[220:223], v[78:81]
	v_mfma_i32_16x16x64_i8 v[134:137], v[156:159], v[200:203], v[134:137]
	v_mfma_i32_16x16x64_i8 v[126:129], v[172:175], v[200:203], v[126:129]
	v_mfma_i32_16x16x64_i8 v[118:121], v[156:159], v[208:211], v[118:121]
	v_mfma_i32_16x16x64_i8 v[110:113], v[172:175], v[208:211], v[110:113]
	v_mfma_i32_16x16x64_i8 v[102:105], v[156:159], v[216:219], v[102:105]
	v_mfma_i32_16x16x64_i8 v[94:97], v[172:175], v[216:219], v[94:97]
	v_mfma_i32_16x16x64_i8 v[86:89], v[156:159], v[224:227], v[86:89]
	v_mfma_i32_16x16x64_i8 v[78:81], v[172:175], v[224:227], v[78:81]
	v_mfma_i32_16x16x64_i8 v[130:133], v[176:179], v[196:199], v[130:133]
	v_mfma_i32_16x16x64_i8 v[122:125], v[184:187], v[196:199], v[122:125]
	v_mfma_i32_16x16x64_i8 v[114:117], v[176:179], v[204:207], v[114:117]
	v_mfma_i32_16x16x64_i8 v[106:109], v[184:187], v[204:207], v[106:109]
	v_mfma_i32_16x16x64_i8 v[98:101], v[176:179], v[212:215], v[98:101]
	v_mfma_i32_16x16x64_i8 v[90:93], v[184:187], v[212:215], v[90:93]
	v_mfma_i32_16x16x64_i8 v[82:85], v[176:179], v[220:223], v[82:85]
	v_mfma_i32_16x16x64_i8 v[74:77], v[184:187], v[220:223], v[74:77]
	v_mfma_i32_16x16x64_i8 v[130:133], v[180:183], v[200:203], v[130:133]
	v_mfma_i32_16x16x64_i8 v[122:125], v[188:191], v[200:203], v[122:125]
	v_mfma_i32_16x16x64_i8 v[114:117], v[180:183], v[208:211], v[114:117]
	v_mfma_i32_16x16x64_i8 v[106:109], v[188:191], v[208:211], v[106:109]
	v_mfma_i32_16x16x64_i8 v[98:101], v[180:183], v[216:219], v[98:101]
	v_mfma_i32_16x16x64_i8 v[90:93], v[188:191], v[216:219], v[90:93]
	v_mfma_i32_16x16x64_i8 v[82:85], v[180:183], v[224:227], v[82:85]
	v_mfma_i32_16x16x64_i8 v[74:77], v[188:191], v[224:227], v[74:77]
	s_setprio 0
	s_barrier
; #define PG8_STAGE(bufoff, gbase, voff) do { _Pragma("unroll") for (int _i = 0; _i < 2; ++_i) \
;         __builtin_amdgcn_global_load_lds((const unsigned*)((const char*)(gbase) + (voff)[_i]), (LAS unsigned*)(lds + (bufoff) + ldsw + _i * 8192), 16, 0, 0); } while (0)
; #define PG8_LDA(dst, b, h) do { _Pragma("unroll") for (int m = 0; m < 4; ++m) dst[m] = PG8_LD32(lds + PG8_SA(b, h) + aoff + m * 2048); } while (0)
; #define PG8_WAIT_V(n) asm volatile("s_waitcnt vmcnt(" #n ")" ::: "memory")
; #define PG8_WAIT_L(n) asm volatile("s_waitcnt lgkmcnt(" #n ")" ::: "memory")
; #define PG8_BAR __builtin_amdgcn_s_barrier()
; #define PG8_SCHED __builtin_amdgcn_sched_barrier(0)
; #define PG8_STA(bufoff, nextflag, h, koff) do { if constexpr (Sched::GATHER) { unsigned _o[2]; _o[0] = (nextflag) ? nxtA[h][0] : curA[h][0]; _o[1] = (nextflag) ? nxtA[h][1] : curA[h][1]; PG8_STAGE(bufoff, Ab + (koff), _o); } \
;         else { PG8_STAGE(bufoff, ((nextflag) ? nA : cA) + (size_t)(h) * hstep + (koff), voffA); } } while (0)
; template <class Epi, class Sched, bool ALIGN_EPI, int DT>
; __device__ __forceinline__ void gemm_phase(LAS unsigned char* lds, const int KB, const Sched& S, const Epi& E) {
;     ...
;             PG8_LDA(At, 1, 1); PG8_STAGE(PG8_SB(1, 0), b3, voffB); PG8_STAGE(PG8_SB(1, 1), b3 + hstep, voffB); PG8_STA(PG8_SA(1, 0), last, 0, k3);
;             PG8_WAIT_V(8); PG8_WAIT_L(0); PG8_BAR; PG8_MMA(1, 0, At, B0); PG8_MMA(1, 1, At, B1); PG8_BAR; PG8_SCHED;
;         }
;         if constexpr (ALIGN_EPI) { if (wr == 0) PG8_BAR; }
	s_add_i32 s28, s36, s38
	v_lshl_add_u64 v[192:193], v[192:193], 0, s[12:13]
	s_mov_b32 m0, s28
	ds_read_b128 v[196:199], v169 offset:49152
	ds_read_b128 v[200:203], v169 offset:50176
	ds_read_b128 v[204:207], v169 offset:51200
	ds_read_b128 v[208:211], v169 offset:52224
	ds_read_b128 v[212:215], v169 offset:53248
	ds_read_b128 v[216:219], v169 offset:54272
	ds_read_b128 v[220:223], v169 offset:55296
	ds_read_b128 v[224:227], v169 offset:56320
	global_load_lds_dwordx4 v[192:193], off
	s_add_i32 m0, s28, 0x2000
	s_add_u32 s28, s34, 0x40080
	v_lshl_add_u64 v[192:193], v[228:229], 0, s[12:13]
	s_addc_u32 s29, s35, 0
	s_add_i32 s34, s37, s38
	global_load_lds_dwordx4 v[192:193], off
	v_lshl_add_u64 v[192:193], s[28:29], 0, v[140:141]
	s_mov_b32 m0, s34
	s_nop 0
	global_load_lds_dwordx4 v[192:193], off
	v_lshl_add_u64 v[192:193], s[28:29], 0, v[138:139]
	s_add_i32 m0, s34, 0x2000
	s_nop 0
	global_load_lds_dwordx4 v[192:193], off
	v_lshl_add_u64 v[192:193], v[230:231], 0, s[12:13]
	s_mov_b32 m0, s45
	s_nop 0
	global_load_lds_dwordx4 v[192:193], off
	v_lshl_add_u64 v[192:193], v[232:233], 0, s[12:13]
	s_mov_b32 m0, s46
	s_nop 0
	global_load_lds_dwordx4 v[192:193], off
	s_waitcnt vmcnt(8)
	s_waitcnt lgkmcnt(0)
	s_barrier
	s_setprio 1
	v_mfma_i32_16x16x64_i8 v[62:65], v[70:73], v[196:199], v[62:65]
	v_mfma_i32_16x16x64_i8 v[54:57], v[160:163], v[196:199], v[54:57]
	v_mfma_i32_16x16x64_i8 v[46:49], v[70:73], v[204:207], v[46:49]
	v_mfma_i32_16x16x64_i8 v[38:41], v[160:163], v[204:207], v[38:41]
	v_mfma_i32_16x16x64_i8 v[30:33], v[70:73], v[212:215], v[30:33]
	v_mfma_i32_16x16x64_i8 v[22:25], v[160:163], v[212:215], v[22:25]
	v_mfma_i32_16x16x64_i8 v[6:9], v[70:73], v[220:223], v[6:9]
	v_mfma_i32_16x16x64_i8 v[2:5], v[160:163], v[220:223], v[2:5]
	v_mfma_i32_16x16x64_i8 v[62:65], v[156:159], v[200:203], v[62:65]
	v_mfma_i32_16x16x64_i8 v[54:57], v[172:175], v[200:203], v[54:57]
	v_mfma_i32_16x16x64_i8 v[46:49], v[156:159], v[208:211], v[46:49]
	v_mfma_i32_16x16x64_i8 v[38:41], v[172:175], v[208:211], v[38:41]
	v_mfma_i32_16x16x64_i8 v[30:33], v[156:159], v[216:219], v[30:33]
	v_mfma_i32_16x16x64_i8 v[22:25], v[172:175], v[216:219], v[22:25]
	v_mfma_i32_16x16x64_i8 v[6:9], v[156:159], v[224:227], v[6:9]
	v_mfma_i32_16x16x64_i8 v[2:5], v[172:175], v[224:227], v[2:5]
	v_mfma_i32_16x16x64_i8 v[58:61], v[176:179], v[196:199], v[58:61]
	v_mfma_i32_16x16x64_i8 v[50:53], v[184:187], v[196:199], v[50:53]
	v_mfma_i32_16x16x64_i8 v[42:45], v[176:179], v[204:207], v[42:45]
	v_mfma_i32_16x16x64_i8 v[34:37], v[184:187], v[204:207], v[34:37]
	v_mfma_i32_16x16x64_i8 v[26:29], v[176:179], v[212:215], v[26:29]
	v_mfma_i32_16x16x64_i8 v[18:21], v[184:187], v[212:215], v[18:21]
	v_mfma_i32_16x16x64_i8 v[14:17], v[176:179], v[220:223], v[14:17]
	v_mfma_i32_16x16x64_i8 v[10:13], v[184:187], v[220:223], v[10:13]
	v_mfma_i32_16x16x64_i8 v[58:61], v[180:183], v[200:203], v[58:61]
	v_mfma_i32_16x16x64_i8 v[50:53], v[188:191], v[200:203], v[50:53]
	v_mfma_i32_16x16x64_i8 v[42:45], v[180:183], v[208:211], v[42:45]
	v_mfma_i32_16x16x64_i8 v[34:37], v[188:191], v[208:211], v[34:37]
	v_mfma_i32_16x16x64_i8 v[26:29], v[180:183], v[216:219], v[26:29]
	v_mfma_i32_16x16x64_i8 v[18:21], v[188:191], v[216:219], v[18:21]
	v_mfma_i32_16x16x64_i8 v[14:17], v[180:183], v[224:227], v[14:17]
	v_mfma_i32_16x16x64_i8 v[10:13], v[188:191], v[224:227], v[10:13]
	s_setprio 0
	s_barrier
	s_add_i32 s62, s62, 2
	s_cmp_gt_u32 s62, 13
	s_mov_b64 s[28:29], s[30:31]
	s_cbranch_scc0 .LBB0_1154
	s_and_b64 vcc, exec, s[14:15]
	s_cbranch_vccz .LBB0_1157
	s_barrier

; #define PG8_STAGE(bufoff, gbase, voff) do { _Pragma("unroll") for (int _i = 0; _i < 2; ++_i) \
;         __builtin_amdgcn_global_load_lds((const unsigned*)((const char*)(gbase) + (voff)[_i]), (LAS unsigned*)(lds + (bufoff) + ldsw + _i * 8192), 16, 0, 0); } while (0)
; #define PG8_LDA(dst, b, h) do { _Pragma("unroll") for (int m = 0; m < 4; ++m) dst[m] = PG8_LD32(lds + PG8_SA(b, h) + aoff + m * 2048); } while (0)
; #define PG8_LDB(dst, b, h) do { _Pragma("unroll") for (int n = 0; n < 2; ++n) dst[n] = PG8_LD32(lds + PG8_SB(b, h) + boff + n * 2048); } while (0)
; #define PG8_WAIT_V(n) asm volatile("s_waitcnt vmcnt(" #n ")" ::: "memory")
; #define PG8_WAIT_L(n) asm volatile("s_waitcnt lgkmcnt(" #n ")" ::: "memory")
; #define PG8_BAR __builtin_amdgcn_s_barrier()
; #define PG8_SCHED __builtin_amdgcn_sched_barrier(0)
; #define PG8_STA(bufoff, nextflag, h, koff) do { if constexpr (Sched::GATHER) { unsigned _o[2]; _o[0] = (nextflag) ? nxtA[h][0] : curA[h][0]; _o[1] = (nextflag) ? nxtA[h][1] : curA[h][1]; PG8_STAGE(bufoff, Ab + (koff), _o); } \
;         else { PG8_STAGE(bufoff, ((nextflag) ? nA : cA) + (size_t)(h) * hstep + (koff), voffA); } } while (0)
; template <class Epi, class Sched, bool ALIGN_EPI, int DT>
; __device__ __forceinline__ void gemm_phase(LAS unsigned char* lds, const int KB, const Sched& S, const Epi& E) {
;     ...
;             PG8_LDB(B0, 0, 0); PG8_LDB(B1, 0, 1); PG8_SCHED; PG8_LDA(At, 0, 0); PG8_STA(PG8_SA(1, 1), false, 1, k1);
;             PG8_WAIT_V(8); PG8_WAIT_L(0); PG8_BAR; PG8_MMA(0, 0, At, B0); PG8_MMA(0, 1, At, B1); PG8_BAR; PG8_SCHED;
;             PG8_LDA(At, 0, 1); PG8_STAGE(PG8_SB(0, 0), b2, voffB); PG8_STAGE(PG8_SB(0, 1), b2 + hstep, voffB); PG8_STA(PG8_SA(0, 0), last, 0, k2);
;             PG8_WAIT_V(8); PG8_WAIT_L(0); PG8_BAR; PG8_MMA(1, 0, At, B0); PG8_MMA(1, 1, At, B1); PG8_BAR; PG8_SCHED;
.LBB0_1237:
	ds_read_b128 v[18:21], v193
	ds_read_b128 v[22:25], v193 offset:1024
	ds_read_b128 v[26:29], v193 offset:2048
	ds_read_b128 v[30:33], v193 offset:3072
	ds_read_b128 v[2:5], v195
	ds_read_b128 v[6:9], v195 offset:1024
	ds_read_b128 v[10:13], v195 offset:2048
	ds_read_b128 v[14:17], v195 offset:3072
	s_add_u32 s26, s30, 0x100
	s_addc_u32 s27, s31, 0
	s_add_u32 s28, s56, s30
	s_addc_u32 s29, s57, s31
	s_add_i32 s68, s43, s34
	s_add_i32 m0, s35, 0xc000
	s_add_i32 s69, s35, 0xe000
	s_add_i32 s63, s68, 0x2000
	s_cmp_eq_u32 s62, 40
	s_cselect_b32 s29, s23, s29
	s_cselect_b32 s28, s22, s28
	s_cselect_b32 s66, 0, s27
	s_cselect_b32 s67, 0, s26
	v_lshl_add_u64 v[222:223], v[178:179], 0, s[30:31]
	ds_read_b128 v[182:185], v196
	ds_read_b128 v[186:189], v196 offset:1024
	ds_read_b128 v[198:201], v196 offset:2048
	ds_read_b128 v[202:205], v196 offset:3072
	ds_read_b128 v[206:209], v196 offset:4096
	ds_read_b128 v[210:213], v196 offset:5120
	ds_read_b128 v[214:217], v196 offset:6144
	ds_read_b128 v[218:221], v196 offset:7168
	global_load_lds_dwordx4 v[222:223], off
	v_lshl_add_u64 v[222:223], v[180:181], 0, s[30:31]
	s_mov_b32 m0, s69
	s_nop 0
	global_load_lds_dwordx4 v[222:223], off
	s_waitcnt vmcnt(8)
	s_waitcnt lgkmcnt(0)
	s_barrier
	s_setprio 1
	v_mfma_scale_f32_16x16x128_f8f6f4 v[158:161], v[18:25], v[182:189], v[158:161], v190, v190 op_sel_hi:[0,0,0]
	v_mfma_scale_f32_16x16x128_f8f6f4 v[154:157], v[26:33], v[182:189], v[154:157], v190, v190 op_sel_hi:[0,0,0]
	v_mfma_scale_f32_16x16x128_f8f6f4 v[150:153], v[18:25], v[198:205], v[150:153], v190, v190 op_sel_hi:[0,0,0]
	v_mfma_scale_f32_16x16x128_f8f6f4 v[142:145], v[26:33], v[198:205], v[142:145], v190, v190 op_sel_hi:[0,0,0]
	v_mfma_scale_f32_16x16x128_f8f6f4 v[134:137], v[18:25], v[206:213], v[134:137], v190, v190 op_sel_hi:[0,0,0]
	v_mfma_scale_f32_16x16x128_f8f6f4 v[126:129], v[26:33], v[206:213], v[126:129], v190, v190 op_sel_hi:[0,0,0]
	v_mfma_scale_f32_16x16x128_f8f6f4 v[118:121], v[18:25], v[214:221], v[118:121], v190, v190 op_sel_hi:[0,0,0]
	v_mfma_scale_f32_16x16x128_f8f6f4 v[110:113], v[26:33], v[214:221], v[110:113], v190, v190 op_sel_hi:[0,0,0]
	v_mfma_scale_f32_16x16x128_f8f6f4 v[146:149], v[2:9], v[182:189], v[146:149], v190, v190 op_sel_hi:[0,0,0]
	v_mfma_scale_f32_16x16x128_f8f6f4 v[138:141], v[10:17], v[182:189], v[138:141], v190, v190 op_sel_hi:[0,0,0]
	v_mfma_scale_f32_16x16x128_f8f6f4 v[130:133], v[2:9], v[198:205], v[130:133], v190, v190 op_sel_hi:[0,0,0]
	v_mfma_scale_f32_16x16x128_f8f6f4 v[122:125], v[10:17], v[198:205], v[122:125], v190, v190 op_sel_hi:[0,0,0]
	v_mfma_scale_f32_16x16x128_f8f6f4 v[114:117], v[2:9], v[206:213], v[114:117], v190, v190 op_sel_hi:[0,0,0]
	v_mfma_scale_f32_16x16x128_f8f6f4 v[106:109], v[10:17], v[206:213], v[106:109], v190, v190 op_sel_hi:[0,0,0]
	v_mfma_scale_f32_16x16x128_f8f6f4 v[102:105], v[2:9], v[214:221], v[102:105], v190, v190 op_sel_hi:[0,0,0]
	v_mfma_scale_f32_16x16x128_f8f6f4 v[98:101], v[10:17], v[214:221], v[98:101], v190, v190 op_sel_hi:[0,0,0]
	s_setprio 0
	s_barrier
	s_mov_b32 m0, s68
	v_lshl_add_u64 v[184:185], s[28:29], 0, v[162:163]
	ds_read_b128 v[198:201], v196 offset:16384
	ds_read_b128 v[202:205], v196 offset:17408
	ds_read_b128 v[206:209], v196 offset:18432
	ds_read_b128 v[210:213], v196 offset:19456
	ds_read_b128 v[214:217], v196 offset:20480
	ds_read_b128 v[218:221], v196 offset:21504
	ds_read_b128 v[222:225], v196 offset:22528
	ds_read_b128 v[226:229], v196 offset:23552
	global_load_lds_dwordx4 v[184:185], off
	s_mov_b32 m0, s63
	s_cselect_b32 s63, s9, s25
	s_cselect_b32 s68, s8, s24
	s_add_u32 s30, s28, 0xb0000
	v_lshl_add_u64 v[182:183], s[28:29], 0, v[164:165]
	s_addc_u32 s31, s29, 0
	s_add_i32 s69, s44, s34
	global_load_lds_dwordx4 v[182:183], off
	v_lshl_add_u64 v[186:187], s[30:31], 0, v[162:163]
	s_mov_b32 m0, s69
	s_nop 0
	global_load_lds_dwordx4 v[186:187], off
	s_add_i32 m0, s69, 0x2000
	v_lshl_add_u64 v[186:187], s[30:31], 0, v[164:165]
	s_add_u32 s30, s68, s67
	s_addc_u32 s31, s63, s66
	global_load_lds_dwordx4 v[186:187], off
	v_lshl_add_u64 v[186:187], s[30:31], 0, v[166:167]
	s_mov_b32 m0, s35
	v_lshl_add_u64 v[188:189], s[30:31], 0, v[168:169]
	global_load_lds_dwordx4 v[186:187], off
	s_mov_b32 m0, s36
	s_nop 0
	global_load_lds_dwordx4 v[188:189], off
	s_waitcnt vmcnt(8)
	s_waitcnt lgkmcnt(0)
	s_barrier
	s_setprio 1
	v_mfma_scale_f32_16x16x128_f8f6f4 v[94:97], v[18:25], v[198:205], v[94:97], v190, v190 op_sel_hi:[0,0,0]
	v_mfma_scale_f32_16x16x128_f8f6f4 v[90:93], v[26:33], v[198:205], v[90:93], v190, v190 op_sel_hi:[0,0,0]
	v_mfma_scale_f32_16x16x128_f8f6f4 v[86:89], v[18:25], v[206:213], v[86:89], v190, v190 op_sel_hi:[0,0,0]
	v_mfma_scale_f32_16x16x128_f8f6f4 v[78:81], v[26:33], v[206:213], v[78:81], v190, v190 op_sel_hi:[0,0,0]
	v_mfma_scale_f32_16x16x128_f8f6f4 v[62:65], v[18:25], v[214:221], v[62:65], v190, v190 op_sel_hi:[0,0,0]
	v_mfma_scale_f32_16x16x128_f8f6f4 v[54:57], v[26:33], v[214:221], v[54:57], v190, v190 op_sel_hi:[0,0,0]
	v_mfma_scale_f32_16x16x128_f8f6f4 v[46:49], v[18:25], v[222:229], v[46:49], v190, v190 op_sel_hi:[0,0,0]
	v_mfma_scale_f32_16x16x128_f8f6f4 v[38:41], v[26:33], v[222:229], v[38:41], v190, v190 op_sel_hi:[0,0,0]
	v_mfma_scale_f32_16x16x128_f8f6f4 v[82:85], v[2:9], v[198:205], v[82:85], v190, v190 op_sel_hi:[0,0,0]
	v_mfma_scale_f32_16x16x128_f8f6f4 v[74:77], v[10:17], v[198:205], v[74:77], v190, v190 op_sel_hi:[0,0,0]
	v_mfma_scale_f32_16x16x128_f8f6f4 v[58:61], v[2:9], v[206:213], v[58:61], v190, v190 op_sel_hi:[0,0,0]
	v_mfma_scale_f32_16x16x128_f8f6f4 v[50:53], v[10:17], v[206:213], v[50:53], v190, v190 op_sel_hi:[0,0,0]
	v_mfma_scale_f32_16x16x128_f8f6f4 v[42:45], v[2:9], v[214:221], v[42:45], v190, v190 op_sel_hi:[0,0,0]
	v_mfma_scale_f32_16x16x128_f8f6f4 v[34:37], v[10:17], v[214:221], v[34:37], v190, v190 op_sel_hi:[0,0,0]
	v_mfma_scale_f32_16x16x128_f8f6f4 v[70:73], v[2:9], v[222:229], v[70:73], v190, v190 op_sel_hi:[0,0,0]
	v_mfma_scale_f32_16x16x128_f8f6f4 v[66:69], v[10:17], v[222:229], v[66:69], v190, v190 op_sel_hi:[0,0,0]
	s_setprio 0
	s_barrier
; #define PG8_STAGE(bufoff, gbase, voff) do { _Pragma("unroll") for (int _i = 0; _i < 2; ++_i) \
;         __builtin_amdgcn_global_load_lds((const unsigned*)((const char*)(gbase) + (voff)[_i]), (LAS unsigned*)(lds + (bufoff) + ldsw + _i * 8192), 16, 0, 0); } while (0)
; #define PG8_LDA(dst, b, h) do { _Pragma("unroll") for (int m = 0; m < 4; ++m) dst[m] = PG8_LD32(lds + PG8_SA(b, h) + aoff + m * 2048); } while (0)
; #define PG8_LDB(dst, b, h) do { _Pragma("unroll") for (int n = 0; n < 2; ++n) dst[n] = PG8_LD32(lds + PG8_SB(b, h) + boff + n * 2048); } while (0)
; #define PG8_WAIT_V(n) asm volatile("s_waitcnt vmcnt(" #n ")" ::: "memory")
; #define PG8_WAIT_L(n) asm volatile("s_waitcnt lgkmcnt(" #n ")" ::: "memory")
; #define PG8_BAR __builtin_amdgcn_s_barrier()
; #define PG8_SCHED __builtin_amdgcn_sched_barrier(0)
; #define PG8_STA(bufoff, nextflag, h, koff) do { if constexpr (Sched::GATHER) { unsigned _o[2]; _o[0] = (nextflag) ? nxtA[h][0] : curA[h][0]; _o[1] = (nextflag) ? nxtA[h][1] : curA[h][1]; PG8_STAGE(bufoff, Ab + (koff), _o); } \
;         else { PG8_STAGE(bufoff, ((nextflag) ? nA : cA) + (size_t)(h) * hstep + (koff), voffA); } } while (0)
; template <class Epi, class Sched, bool ALIGN_EPI, int DT>
; __device__ __forceinline__ void gemm_phase(LAS unsigned char* lds, const int KB, const Sched& S, const Epi& E) {
;     ...
;             PG8_LDB(B0, 1, 0); PG8_LDB(B1, 1, 1); PG8_SCHED; PG8_LDA(At, 1, 0); PG8_STA(PG8_SA(0, 1), last, 1, k2);
;             PG8_WAIT_V(8); PG8_WAIT_L(0); PG8_BAR; PG8_MMA(0, 0, At, B0); PG8_MMA(0, 1, At, B1); PG8_BAR; PG8_SCHED;
;             PG8_LDA(At, 1, 1); PG8_STAGE(PG8_SB(1, 0), b3, voffB); PG8_STAGE(PG8_SB(1, 1), b3 + hstep, voffB); PG8_STA(PG8_SA(1, 0), last, 0, k3);
;             PG8_WAIT_V(8); PG8_WAIT_L(0); PG8_BAR; PG8_MMA(1, 0, At, B0); PG8_MMA(1, 1, At, B1); PG8_BAR; PG8_SCHED;
;         }
;         if constexpr (ALIGN_EPI) { if (wr == 0) PG8_BAR; }
	s_add_i32 s63, 0, 0x18000
	s_add_i32 s66, 0, 0x1c000
	v_add_u32_e32 v14, s63, v191
	v_add_u32_e32 v30, s66, v191
	ds_read_b128 v[2:5], v14
	ds_read_b128 v[6:9], v14 offset:1024
	ds_read_b128 v[10:13], v14 offset:2048
	ds_read_b128 v[14:17], v14 offset:3072
	ds_read_b128 v[18:21], v30
	ds_read_b128 v[22:25], v30 offset:1024
	ds_read_b128 v[26:29], v30 offset:2048
	ds_read_b128 v[30:33], v30 offset:3072
	s_add_u32 s30, s30, 0xb0000
	s_addc_u32 s31, s31, 0
	s_mov_b32 m0, s37
	v_lshl_add_u64 v[230:231], s[30:31], 0, v[166:167]
	ds_read_b128 v[198:201], v196 offset:32768
	ds_read_b128 v[202:205], v196 offset:33792
	ds_read_b128 v[206:209], v196 offset:34816
	ds_read_b128 v[210:213], v196 offset:35840
	ds_read_b128 v[214:217], v196 offset:36864
	ds_read_b128 v[218:221], v196 offset:37888
	ds_read_b128 v[222:225], v196 offset:38912
	ds_read_b128 v[226:229], v196 offset:39936
	global_load_lds_dwordx4 v[230:231], off
	v_lshl_add_u64 v[230:231], s[30:31], 0, v[168:169]
	s_mov_b32 m0, s38
	s_nop 0
	global_load_lds_dwordx4 v[230:231], off
	s_waitcnt vmcnt(8)
	s_waitcnt lgkmcnt(0)
	s_barrier
	s_setprio 1
	v_mfma_scale_f32_16x16x128_f8f6f4 v[158:161], v[2:9], v[198:205], v[158:161], v190, v190 op_sel_hi:[0,0,0]
	v_mfma_scale_f32_16x16x128_f8f6f4 v[154:157], v[10:17], v[198:205], v[154:157], v190, v190 op_sel_hi:[0,0,0]
	v_mfma_scale_f32_16x16x128_f8f6f4 v[150:153], v[2:9], v[206:213], v[150:153], v190, v190 op_sel_hi:[0,0,0]
	v_mfma_scale_f32_16x16x128_f8f6f4 v[142:145], v[10:17], v[206:213], v[142:145], v190, v190 op_sel_hi:[0,0,0]
	v_mfma_scale_f32_16x16x128_f8f6f4 v[134:137], v[2:9], v[214:221], v[134:137], v190, v190 op_sel_hi:[0,0,0]
	v_mfma_scale_f32_16x16x128_f8f6f4 v[126:129], v[10:17], v[214:221], v[126:129], v190, v190 op_sel_hi:[0,0,0]
	v_mfma_scale_f32_16x16x128_f8f6f4 v[118:121], v[2:9], v[222:229], v[118:121], v190, v190 op_sel_hi:[0,0,0]
	v_mfma_scale_f32_16x16x128_f8f6f4 v[110:113], v[10:17], v[222:229], v[110:113], v190, v190 op_sel_hi:[0,0,0]
	v_mfma_scale_f32_16x16x128_f8f6f4 v[146:149], v[18:25], v[198:205], v[146:149], v190, v190 op_sel_hi:[0,0,0]
	v_mfma_scale_f32_16x16x128_f8f6f4 v[138:141], v[26:33], v[198:205], v[138:141], v190, v190 op_sel_hi:[0,0,0]
	v_mfma_scale_f32_16x16x128_f8f6f4 v[130:133], v[18:25], v[206:213], v[130:133], v190, v190 op_sel_hi:[0,0,0]
	v_mfma_scale_f32_16x16x128_f8f6f4 v[122:125], v[26:33], v[206:213], v[122:125], v190, v190 op_sel_hi:[0,0,0]
	v_mfma_scale_f32_16x16x128_f8f6f4 v[114:117], v[18:25], v[214:221], v[114:117], v190, v190 op_sel_hi:[0,0,0]
	v_mfma_scale_f32_16x16x128_f8f6f4 v[106:109], v[26:33], v[214:221], v[106:109], v190, v190 op_sel_hi:[0,0,0]
	v_mfma_scale_f32_16x16x128_f8f6f4 v[102:105], v[18:25], v[222:229], v[102:105], v190, v190 op_sel_hi:[0,0,0]
	v_mfma_scale_f32_16x16x128_f8f6f4 v[98:101], v[26:33], v[222:229], v[98:101], v190, v190 op_sel_hi:[0,0,0]
	s_setprio 0
	s_barrier
	s_add_i32 s30, s63, s34
	v_lshl_add_u64 v[184:185], v[184:185], 0, s[12:13]
	s_mov_b32 m0, s30
	ds_read_b128 v[198:201], v196 offset:49152
	ds_read_b128 v[202:205], v196 offset:50176
	ds_read_b128 v[206:209], v196 offset:51200
	ds_read_b128 v[210:213], v196 offset:52224
	ds_read_b128 v[214:217], v196 offset:53248
	ds_read_b128 v[218:221], v196 offset:54272
	ds_read_b128 v[222:225], v196 offset:55296
	ds_read_b128 v[226:229], v196 offset:56320
	global_load_lds_dwordx4 v[184:185], off
	s_add_i32 m0, s30, 0x2000
	s_add_u32 s28, s28, 0xb0080
	v_lshl_add_u64 v[182:183], v[182:183], 0, s[12:13]
	s_addc_u32 s29, s29, 0
	s_add_i32 s30, s66, s34
	global_load_lds_dwordx4 v[182:183], off
	v_lshl_add_u64 v[182:183], s[28:29], 0, v[162:163]
	s_mov_b32 m0, s30
	s_nop 0
	global_load_lds_dwordx4 v[182:183], off
	v_lshl_add_u64 v[182:183], s[28:29], 0, v[164:165]
	s_add_i32 m0, s30, 0x2000
	s_nop 0
	global_load_lds_dwordx4 v[182:183], off
	v_lshl_add_u64 v[182:183], v[186:187], 0, s[12:13]
	s_mov_b32 m0, s40
	s_nop 0
	global_load_lds_dwordx4 v[182:183], off
	v_lshl_add_u64 v[182:183], v[188:189], 0, s[12:13]
	s_mov_b32 m0, s41
	s_nop 0
	global_load_lds_dwordx4 v[182:183], off
	s_waitcnt vmcnt(8)
	s_waitcnt lgkmcnt(0)
	s_barrier
	s_setprio 1
	v_mfma_scale_f32_16x16x128_f8f6f4 v[94:97], v[2:9], v[198:205], v[94:97], v190, v190 op_sel_hi:[0,0,0]
	v_mfma_scale_f32_16x16x128_f8f6f4 v[90:93], v[10:17], v[198:205], v[90:93], v190, v190 op_sel_hi:[0,0,0]
	v_mfma_scale_f32_16x16x128_f8f6f4 v[86:89], v[2:9], v[206:213], v[86:89], v190, v190 op_sel_hi:[0,0,0]
	v_mfma_scale_f32_16x16x128_f8f6f4 v[78:81], v[10:17], v[206:213], v[78:81], v190, v190 op_sel_hi:[0,0,0]
	v_mfma_scale_f32_16x16x128_f8f6f4 v[62:65], v[2:9], v[214:221], v[62:65], v190, v190 op_sel_hi:[0,0,0]
	v_mfma_scale_f32_16x16x128_f8f6f4 v[54:57], v[10:17], v[214:221], v[54:57], v190, v190 op_sel_hi:[0,0,0]
	v_mfma_scale_f32_16x16x128_f8f6f4 v[46:49], v[2:9], v[222:229], v[46:49], v190, v190 op_sel_hi:[0,0,0]
	v_mfma_scale_f32_16x16x128_f8f6f4 v[38:41], v[10:17], v[222:229], v[38:41], v190, v190 op_sel_hi:[0,0,0]
	v_mfma_scale_f32_16x16x128_f8f6f4 v[82:85], v[18:25], v[198:205], v[82:85], v190, v190 op_sel_hi:[0,0,0]
	v_mfma_scale_f32_16x16x128_f8f6f4 v[74:77], v[26:33], v[198:205], v[74:77], v190, v190 op_sel_hi:[0,0,0]
	v_mfma_scale_f32_16x16x128_f8f6f4 v[58:61], v[18:25], v[206:213], v[58:61], v190, v190 op_sel_hi:[0,0,0]
	v_mfma_scale_f32_16x16x128_f8f6f4 v[50:53], v[26:33], v[206:213], v[50:53], v190, v190 op_sel_hi:[0,0,0]
	v_mfma_scale_f32_16x16x128_f8f6f4 v[42:45], v[18:25], v[214:221], v[42:45], v190, v190 op_sel_hi:[0,0,0]
	v_mfma_scale_f32_16x16x128_f8f6f4 v[34:37], v[26:33], v[214:221], v[34:37], v190, v190 op_sel_hi:[0,0,0]
	v_mfma_scale_f32_16x16x128_f8f6f4 v[70:73], v[18:25], v[222:229], v[70:73], v190, v190 op_sel_hi:[0,0,0]
	v_mfma_scale_f32_16x16x128_f8f6f4 v[66:69], v[26:33], v[222:229], v[66:69], v190, v190 op_sel_hi:[0,0,0]
	s_setprio 0
	s_barrier
	s_add_i32 s62, s62, 2
	s_cmp_gt_u32 s62, 41
	s_mov_b64 s[30:31], s[26:27]
	s_cbranch_scc0 .LBB0_1237
	s_and_b64 vcc, exec, s[14:15]
	s_cbranch_vccz .LBB0_1240
	s_barrier

; #define PG8_STAGE(bufoff, gbase, voff) do { _Pragma("unroll") for (int _i = 0; _i < 2; ++_i) \
;         __builtin_amdgcn_global_load_lds((const unsigned*)((const char*)(gbase) + (voff)[_i]), (LAS unsigned*)(lds + (bufoff) + ldsw + _i * 8192), 16, 0, 0); } while (0)
; #define PG8_LDA(dst, b, h) do { _Pragma("unroll") for (int m = 0; m < 4; ++m) dst[m] = PG8_LD32(lds + PG8_SA(b, h) + aoff + m * 2048); } while (0)
; #define PG8_LDB(dst, b, h) do { _Pragma("unroll") for (int n = 0; n < 2; ++n) dst[n] = PG8_LD32(lds + PG8_SB(b, h) + boff + n * 2048); } while (0)
; #define PG8_WAIT_V(n) asm volatile("s_waitcnt vmcnt(" #n ")" ::: "memory")
; #define PG8_WAIT_L(n) asm volatile("s_waitcnt lgkmcnt(" #n ")" ::: "memory")
; #define PG8_BAR __builtin_amdgcn_s_barrier()
; #define PG8_SCHED __builtin_amdgcn_sched_barrier(0)
; #define PG8_STA(bufoff, nextflag, h, koff) do { if constexpr (Sched::GATHER) { unsigned _o[2]; _o[0] = (nextflag) ? nxtA[h][0] : curA[h][0]; _o[1] = (nextflag) ? nxtA[h][1] : curA[h][1]; PG8_STAGE(bufoff, Ab + (koff), _o); } \
;         else { PG8_STAGE(bufoff, ((nextflag) ? nA : cA) + (size_t)(h) * hstep + (koff), voffA); } } while (0)
; template <class Epi, class Sched, bool ALIGN_EPI, int DT>
; __device__ __forceinline__ void gemm_phase(LAS unsigned char* lds, const int KB, const Sched& S, const Epi& E) {
;     ...
;             PG8_LDB(B0, 0, 0); PG8_LDB(B1, 0, 1); PG8_SCHED; PG8_LDA(At, 0, 0); PG8_STA(PG8_SA(1, 1), false, 1, k1);
;             PG8_WAIT_V(8); PG8_WAIT_L(0); PG8_BAR; PG8_MMA(0, 0, At, B0); PG8_MMA(0, 1, At, B1); PG8_BAR; PG8_SCHED;
;             PG8_LDA(At, 0, 1); PG8_STAGE(PG8_SB(0, 0), b2, voffB); PG8_STAGE(PG8_SB(0, 1), b2 + hstep, voffB); PG8_STA(PG8_SA(0, 0), last, 0, k2);
;             PG8_WAIT_V(8); PG8_WAIT_L(0); PG8_BAR; PG8_MMA(1, 0, At, B0); PG8_MMA(1, 1, At, B1); PG8_BAR; PG8_SCHED;
.LBB0_1385:
	ds_read_b128 v[152:155], v174
	ds_read_b128 v[156:159], v174 offset:1024
	ds_read_b128 v[160:163], v174 offset:2048
	ds_read_b128 v[164:167], v174 offset:3072
	ds_read_b128 v[168:171], v175
	ds_read_b128 v[180:183], v175 offset:1024
	ds_read_b128 v[184:187], v175 offset:2048
	ds_read_b128 v[188:191], v175 offset:3072
	s_add_u32 s38, s36, 0x100
	s_addc_u32 s39, s37, 0
	s_add_u32 s74, s25, s36
	s_addc_u32 s75, s70, s37
	s_cmp_eq_u32 s71, 12
	s_cselect_b64 s[42:43], -1, 0
	s_and_b64 s[40:41], s[42:43], exec
	s_cselect_b32 s76, 0, s38
	s_cselect_b32 s41, s0, s75
	s_cselect_b32 s40, s23, s74
	v_lshl_add_u64 v[192:193], v[148:149], 0, s[36:37]
	s_add_i32 m0, s47, 0xc000
	ds_read_b128 v[196:199], v176
	ds_read_b128 v[200:203], v176 offset:1024
	ds_read_b128 v[204:207], v176 offset:2048
	ds_read_b128 v[208:211], v176 offset:3072
	ds_read_b128 v[212:215], v176 offset:4096
	ds_read_b128 v[216:219], v176 offset:5120
	ds_read_b128 v[220:223], v176 offset:6144
	ds_read_b128 v[224:227], v176 offset:7168
	global_load_lds_dwordx4 v[192:193], off
	v_lshl_add_u64 v[192:193], v[150:151], 0, s[36:37]
	s_add_i32 m0, s47, 0xe000
	s_nop 0
	global_load_lds_dwordx4 v[192:193], off
	s_waitcnt vmcnt(8)
	s_waitcnt lgkmcnt(0)
	s_barrier
	s_setprio 1
	v_mfma_i32_16x16x64_i8 v[126:129], v[152:155], v[196:199], v[126:129]
	v_mfma_i32_16x16x64_i8 v[122:125], v[160:163], v[196:199], v[122:125]
	v_mfma_i32_16x16x64_i8 v[110:113], v[152:155], v[204:207], v[110:113]
	v_mfma_i32_16x16x64_i8 v[106:109], v[160:163], v[204:207], v[106:109]
	v_mfma_i32_16x16x64_i8 v[94:97], v[152:155], v[212:215], v[94:97]
	v_mfma_i32_16x16x64_i8 v[90:93], v[160:163], v[212:215], v[90:93]
	v_mfma_i32_16x16x64_i8 v[78:81], v[152:155], v[220:223], v[78:81]
	v_mfma_i32_16x16x64_i8 v[74:77], v[160:163], v[220:223], v[74:77]
	v_mfma_i32_16x16x64_i8 v[126:129], v[156:159], v[200:203], v[126:129]
	v_mfma_i32_16x16x64_i8 v[122:125], v[164:167], v[200:203], v[122:125]
	v_mfma_i32_16x16x64_i8 v[110:113], v[156:159], v[208:211], v[110:113]
	v_mfma_i32_16x16x64_i8 v[106:109], v[164:167], v[208:211], v[106:109]
	v_mfma_i32_16x16x64_i8 v[94:97], v[156:159], v[216:219], v[94:97]
	v_mfma_i32_16x16x64_i8 v[90:93], v[164:167], v[216:219], v[90:93]
	v_mfma_i32_16x16x64_i8 v[78:81], v[156:159], v[224:227], v[78:81]
	v_mfma_i32_16x16x64_i8 v[74:77], v[164:167], v[224:227], v[74:77]
	v_mfma_i32_16x16x64_i8 v[118:121], v[168:171], v[196:199], v[118:121]
	v_mfma_i32_16x16x64_i8 v[114:117], v[184:187], v[196:199], v[114:117]
	v_mfma_i32_16x16x64_i8 v[102:105], v[168:171], v[204:207], v[102:105]
	v_mfma_i32_16x16x64_i8 v[98:101], v[184:187], v[204:207], v[98:101]
	v_mfma_i32_16x16x64_i8 v[86:89], v[168:171], v[212:215], v[86:89]
	v_mfma_i32_16x16x64_i8 v[82:85], v[184:187], v[212:215], v[82:85]
	v_mfma_i32_16x16x64_i8 v[70:73], v[168:171], v[220:223], v[70:73]
	v_mfma_i32_16x16x64_i8 v[66:69], v[184:187], v[220:223], v[66:69]
	v_mfma_i32_16x16x64_i8 v[118:121], v[180:183], v[200:203], v[118:121]
	v_mfma_i32_16x16x64_i8 v[114:117], v[188:191], v[200:203], v[114:117]
	v_mfma_i32_16x16x64_i8 v[102:105], v[180:183], v[208:211], v[102:105]
	v_mfma_i32_16x16x64_i8 v[98:101], v[188:191], v[208:211], v[98:101]
	v_mfma_i32_16x16x64_i8 v[86:89], v[180:183], v[216:219], v[86:89]
	v_mfma_i32_16x16x64_i8 v[82:85], v[188:191], v[216:219], v[82:85]
	v_mfma_i32_16x16x64_i8 v[70:73], v[180:183], v[224:227], v[70:73]
	v_mfma_i32_16x16x64_i8 v[66:69], v[188:191], v[224:227], v[66:69]
	s_setprio 0
	s_barrier
	s_add_i32 s36, s66, s44
	v_lshl_add_u64 v[192:193], s[40:41], 0, v[134:135]
	s_mov_b32 m0, s36
	ds_read_b128 v[196:199], v176 offset:16384
	ds_read_b128 v[200:203], v176 offset:17408
	ds_read_b128 v[204:207], v176 offset:18432
	ds_read_b128 v[208:211], v176 offset:19456
	ds_read_b128 v[212:215], v176 offset:20480
	ds_read_b128 v[216:219], v176 offset:21504
	ds_read_b128 v[220:223], v176 offset:22528
	ds_read_b128 v[224:227], v176 offset:23552
	global_load_lds_dwordx4 v[192:193], off
	s_add_i32 m0, s36, 0x2000
	s_add_u32 s36, s40, 0x40000
	v_lshl_add_u64 v[228:229], s[40:41], 0, v[132:133]
	s_addc_u32 s37, s41, 0
	s_add_i32 s74, s67, s44
	global_load_lds_dwordx4 v[228:229], off
	v_lshl_add_u64 v[230:231], s[36:37], 0, v[134:135]
	s_mov_b32 m0, s74
	s_nop 0
	global_load_lds_dwordx4 v[230:231], off
	v_lshl_add_u64 v[230:231], s[36:37], 0, v[132:133]
	s_add_i32 m0, s74, 0x2000
	s_and_b64 s[36:37], s[8:9], s[42:43]
	s_and_b64 s[36:37], s[36:37], exec
	s_cselect_b32 s36, s26, s34
	s_cselect_b32 s37, s27, s35
	s_add_u32 s36, s36, s76
	s_addc_u32 s37, s37, 0
	global_load_lds_dwordx4 v[230:231], off
	v_lshl_add_u64 v[230:231], s[36:37], 0, v[136:137]
	s_mov_b32 m0, s47
	v_lshl_add_u64 v[232:233], s[36:37], 0, v[138:139]
	global_load_lds_dwordx4 v[230:231], off
	s_mov_b32 m0, s49
	s_nop 0
	global_load_lds_dwordx4 v[232:233], off
	s_waitcnt vmcnt(8)
	s_waitcnt lgkmcnt(0)
	s_barrier
; #define PG8_LDA(dst, b, h) do { _Pragma("unroll") for (int m = 0; m < 4; ++m) dst[m] = PG8_LD32(lds + PG8_SA(b, h) + aoff + m * 2048); } while (0)
; #define PG8_LDB(dst, b, h) do { _Pragma("unroll") for (int n = 0; n < 2; ++n) dst[n] = PG8_LD32(lds + PG8_SB(b, h) + boff + n * 2048); } while (0)
; #define PG8_WAIT_V(n) asm volatile("s_waitcnt vmcnt(" #n ")" ::: "memory")
; #define PG8_WAIT_L(n) asm volatile("s_waitcnt lgkmcnt(" #n ")" ::: "memory")
; #define PG8_BAR __builtin_amdgcn_s_barrier()
; #define PG8_SCHED __builtin_amdgcn_sched_barrier(0)
; #define PG8_STA(bufoff, nextflag, h, koff) do { if constexpr (Sched::GATHER) { unsigned _o[2]; _o[0] = (nextflag) ? nxtA[h][0] : curA[h][0]; _o[1] = (nextflag) ? nxtA[h][1] : curA[h][1]; PG8_STAGE(bufoff, Ab + (koff), _o); } \
;         else { PG8_STAGE(bufoff, ((nextflag) ? nA : cA) + (size_t)(h) * hstep + (koff), voffA); } } while (0)
; template <class Epi, class Sched, bool ALIGN_EPI, int DT>
; __device__ __forceinline__ void gemm_phase(LAS unsigned char* lds, const int KB, const Sched& S, const Epi& E) {
;     ...
;             PG8_WAIT_V(8); PG8_WAIT_L(0); PG8_BAR; PG8_MMA(1, 0, At, B0); PG8_MMA(1, 1, At, B1); PG8_BAR; PG8_SCHED;
;             PG8_LDB(B0, 1, 0); PG8_LDB(B1, 1, 1); PG8_SCHED; PG8_LDA(At, 1, 0); PG8_STA(PG8_SA(0, 1), last, 1, k2);
;             PG8_WAIT_V(8); PG8_WAIT_L(0); PG8_BAR; PG8_MMA(0, 0, At, B0); PG8_MMA(0, 1, At, B1); PG8_BAR; PG8_SCHED;
	s_setprio 1
	v_mfma_i32_16x16x64_i8 v[62:65], v[152:155], v[196:199], v[62:65]
	v_mfma_i32_16x16x64_i8 v[58:61], v[160:163], v[196:199], v[58:61]
	v_mfma_i32_16x16x64_i8 v[46:49], v[152:155], v[204:207], v[46:49]
	v_mfma_i32_16x16x64_i8 v[42:45], v[160:163], v[204:207], v[42:45]
	v_mfma_i32_16x16x64_i8 v[30:33], v[152:155], v[212:215], v[30:33]
	v_mfma_i32_16x16x64_i8 v[26:29], v[160:163], v[212:215], v[26:29]
	v_mfma_i32_16x16x64_i8 v[6:9], v[152:155], v[220:223], v[6:9]
	v_mfma_i32_16x16x64_i8 v[2:5], v[160:163], v[220:223], v[2:5]
	v_mfma_i32_16x16x64_i8 v[62:65], v[156:159], v[200:203], v[62:65]
	v_mfma_i32_16x16x64_i8 v[58:61], v[164:167], v[200:203], v[58:61]
	v_mfma_i32_16x16x64_i8 v[46:49], v[156:159], v[208:211], v[46:49]
	v_mfma_i32_16x16x64_i8 v[42:45], v[164:167], v[208:211], v[42:45]
	v_mfma_i32_16x16x64_i8 v[30:33], v[156:159], v[216:219], v[30:33]
	v_mfma_i32_16x16x64_i8 v[26:29], v[164:167], v[216:219], v[26:29]
	v_mfma_i32_16x16x64_i8 v[6:9], v[156:159], v[224:227], v[6:9]
	v_mfma_i32_16x16x64_i8 v[2:5], v[164:167], v[224:227], v[2:5]
	v_mfma_i32_16x16x64_i8 v[54:57], v[168:171], v[196:199], v[54:57]
	v_mfma_i32_16x16x64_i8 v[50:53], v[184:187], v[196:199], v[50:53]
	v_mfma_i32_16x16x64_i8 v[38:41], v[168:171], v[204:207], v[38:41]
	v_mfma_i32_16x16x64_i8 v[34:37], v[184:187], v[204:207], v[34:37]
	v_mfma_i32_16x16x64_i8 v[14:17], v[168:171], v[212:215], v[14:17]
	v_mfma_i32_16x16x64_i8 v[10:13], v[184:187], v[212:215], v[10:13]
	v_mfma_i32_16x16x64_i8 v[22:25], v[168:171], v[220:223], v[22:25]
	v_mfma_i32_16x16x64_i8 v[18:21], v[184:187], v[220:223], v[18:21]
	v_mfma_i32_16x16x64_i8 v[54:57], v[180:183], v[200:203], v[54:57]
	v_mfma_i32_16x16x64_i8 v[50:53], v[188:191], v[200:203], v[50:53]
	v_mfma_i32_16x16x64_i8 v[38:41], v[180:183], v[208:211], v[38:41]
	v_mfma_i32_16x16x64_i8 v[34:37], v[188:191], v[208:211], v[34:37]
	v_mfma_i32_16x16x64_i8 v[14:17], v[180:183], v[216:219], v[14:17]
	v_mfma_i32_16x16x64_i8 v[10:13], v[188:191], v[216:219], v[10:13]
	v_mfma_i32_16x16x64_i8 v[22:25], v[180:183], v[224:227], v[22:25]
	v_mfma_i32_16x16x64_i8 v[18:21], v[188:191], v[224:227], v[18:21]
	s_setprio 0
	s_barrier
	s_add_i32 s42, 0, 0x18000
	v_add_u32_e32 v1, s42, v172
	s_add_i32 s43, 0, 0x1c000
	ds_read_b128 v[152:155], v1
	ds_read_b128 v[156:159], v1 offset:1024
	ds_read_b128 v[160:163], v1 offset:2048
	ds_read_b128 v[164:167], v1 offset:3072
	v_add_u32_e32 v1, s43, v172
	ds_read_b128 v[168:171], v1
	ds_read_b128 v[180:183], v1 offset:1024
	ds_read_b128 v[184:187], v1 offset:2048
	ds_read_b128 v[188:191], v1 offset:3072
	s_add_u32 s36, s36, 0x40000
	s_addc_u32 s37, s37, 0
	s_mov_b32 m0, s52
	v_lshl_add_u64 v[234:235], s[36:37], 0, v[136:137]
	ds_read_b128 v[196:199], v176 offset:32768
	ds_read_b128 v[200:203], v176 offset:33792
	ds_read_b128 v[204:207], v176 offset:34816
	ds_read_b128 v[208:211], v176 offset:35840
	ds_read_b128 v[212:215], v176 offset:36864
	ds_read_b128 v[216:219], v176 offset:37888
	ds_read_b128 v[220:223], v176 offset:38912
	ds_read_b128 v[224:227], v176 offset:39936
	global_load_lds_dwordx4 v[234:235], off
	v_lshl_add_u64 v[234:235], s[36:37], 0, v[138:139]
	s_mov_b32 m0, s53
	s_nop 0
	global_load_lds_dwordx4 v[234:235], off
	s_waitcnt vmcnt(8)
	s_waitcnt lgkmcnt(0)
	s_barrier
	s_setprio 1
	v_mfma_i32_16x16x64_i8 v[126:129], v[152:155], v[196:199], v[126:129]
	v_mfma_i32_16x16x64_i8 v[122:125], v[160:163], v[196:199], v[122:125]
	v_mfma_i32_16x16x64_i8 v[110:113], v[152:155], v[204:207], v[110:113]
	v_mfma_i32_16x16x64_i8 v[106:109], v[160:163], v[204:207], v[106:109]
	v_mfma_i32_16x16x64_i8 v[94:97], v[152:155], v[212:215], v[94:97]
	v_mfma_i32_16x16x64_i8 v[90:93], v[160:163], v[212:215], v[90:93]
	v_mfma_i32_16x16x64_i8 v[78:81], v[152:155], v[220:223], v[78:81]
	v_mfma_i32_16x16x64_i8 v[74:77], v[160:163], v[220:223], v[74:77]
	v_mfma_i32_16x16x64_i8 v[126:129], v[156:159], v[200:203], v[126:129]
	v_mfma_i32_16x16x64_i8 v[122:125], v[164:167], v[200:203], v[122:125]
	v_mfma_i32_16x16x64_i8 v[110:113], v[156:159], v[208:211], v[110:113]
	v_mfma_i32_16x16x64_i8 v[106:109], v[164:167], v[208:211], v[106:109]
	v_mfma_i32_16x16x64_i8 v[94:97], v[156:159], v[216:219], v[94:97]
	v_mfma_i32_16x16x64_i8 v[90:93], v[164:167], v[216:219], v[90:93]
	v_mfma_i32_16x16x64_i8 v[78:81], v[156:159], v[224:227], v[78:81]
	v_mfma_i32_16x16x64_i8 v[74:77], v[164:167], v[224:227], v[74:77]
	v_mfma_i32_16x16x64_i8 v[118:121], v[168:171], v[196:199], v[118:121]
	v_mfma_i32_16x16x64_i8 v[114:117], v[184:187], v[196:199], v[114:117]
	v_mfma_i32_16x16x64_i8 v[102:105], v[168:171], v[204:207], v[102:105]
	v_mfma_i32_16x16x64_i8 v[98:101], v[184:187], v[204:207], v[98:101]
	v_mfma_i32_16x16x64_i8 v[86:89], v[168:171], v[212:215], v[86:89]
	v_mfma_i32_16x16x64_i8 v[82:85], v[184:187], v[212:215], v[82:85]
	v_mfma_i32_16x16x64_i8 v[70:73], v[168:171], v[220:223], v[70:73]
	v_mfma_i32_16x16x64_i8 v[66:69], v[184:187], v[220:223], v[66:69]
	v_mfma_i32_16x16x64_i8 v[118:121], v[180:183], v[200:203], v[118:121]
	v_mfma_i32_16x16x64_i8 v[114:117], v[188:191], v[200:203], v[114:117]
	v_mfma_i32_16x16x64_i8 v[102:105], v[180:183], v[208:211], v[102:105]
	v_mfma_i32_16x16x64_i8 v[98:101], v[188:191], v[208:211], v[98:101]
	v_mfma_i32_16x16x64_i8 v[86:89], v[180:183], v[216:219], v[86:89]
	v_mfma_i32_16x16x64_i8 v[82:85], v[188:191], v[216:219], v[82:85]
	v_mfma_i32_16x16x64_i8 v[70:73], v[180:183], v[224:227], v[70:73]
	v_mfma_i32_16x16x64_i8 v[66:69], v[188:191], v[224:227], v[66:69]
	s_setprio 0
	s_barrier
; #define PG8_STAGE(bufoff, gbase, voff) do { _Pragma("unroll") for (int _i = 0; _i < 2; ++_i) \
;         __builtin_amdgcn_global_load_lds((const unsigned*)((const char*)(gbase) + (voff)[_i]), (LAS unsigned*)(lds + (bufoff) + ldsw + _i * 8192), 16, 0, 0); } while (0)
; #define PG8_LDA(dst, b, h) do { _Pragma("unroll") for (int m = 0; m < 4; ++m) dst[m] = PG8_LD32(lds + PG8_SA(b, h) + aoff + m * 2048); } while (0)
; #define PG8_WAIT_V(n) asm volatile("s_waitcnt vmcnt(" #n ")" ::: "memory")
; #define PG8_WAIT_L(n) asm volatile("s_waitcnt lgkmcnt(" #n ")" ::: "memory")
; #define PG8_BAR __builtin_amdgcn_s_barrier()
; #define PG8_SCHED __builtin_amdgcn_sched_barrier(0)
; #define PG8_STA(bufoff, nextflag, h, koff) do { if constexpr (Sched::GATHER) { unsigned _o[2]; _o[0] = (nextflag) ? nxtA[h][0] : curA[h][0]; _o[1] = (nextflag) ? nxtA[h][1] : curA[h][1]; PG8_STAGE(bufoff, Ab + (koff), _o); } \
;         else { PG8_STAGE(bufoff, ((nextflag) ? nA : cA) + (size_t)(h) * hstep + (koff), voffA); } } while (0)
; template <class Epi, class Sched, bool ALIGN_EPI, int DT>
; __device__ __forceinline__ void gemm_phase(LAS unsigned char* lds, const int KB, const Sched& S, const Epi& E) {
;     ...
;             PG8_LDA(At, 1, 1); PG8_STAGE(PG8_SB(1, 0), b3, voffB); PG8_STAGE(PG8_SB(1, 1), b3 + hstep, voffB); PG8_STA(PG8_SA(1, 0), last, 0, k3);
;             PG8_WAIT_V(8); PG8_WAIT_L(0); PG8_BAR; PG8_MMA(1, 0, At, B0); PG8_MMA(1, 1, At, B1); PG8_BAR; PG8_SCHED;
;         }
;         if constexpr (ALIGN_EPI) { if (wr == 0) PG8_BAR; }
	s_add_i32 s36, s42, s44
	v_lshl_add_u64 v[192:193], v[192:193], 0, s[18:19]
	s_mov_b32 m0, s36
	ds_read_b128 v[196:199], v176 offset:49152
	ds_read_b128 v[200:203], v176 offset:50176
	ds_read_b128 v[204:207], v176 offset:51200
	ds_read_b128 v[208:211], v176 offset:52224
	ds_read_b128 v[212:215], v176 offset:53248
	ds_read_b128 v[216:219], v176 offset:54272
	ds_read_b128 v[220:223], v176 offset:55296
	ds_read_b128 v[224:227], v176 offset:56320
	global_load_lds_dwordx4 v[192:193], off
	s_add_i32 m0, s36, 0x2000
	s_add_u32 s36, s40, 0x40080
	v_lshl_add_u64 v[192:193], v[228:229], 0, s[18:19]
	s_addc_u32 s37, s41, 0
	s_add_i32 s40, s43, s44
	global_load_lds_dwordx4 v[192:193], off
	v_lshl_add_u64 v[192:193], s[36:37], 0, v[134:135]
	s_mov_b32 m0, s40
	s_nop 0
	global_load_lds_dwordx4 v[192:193], off
	v_lshl_add_u64 v[192:193], s[36:37], 0, v[132:133]
	s_add_i32 m0, s40, 0x2000
	s_nop 0
	global_load_lds_dwordx4 v[192:193], off
	v_lshl_add_u64 v[192:193], v[230:231], 0, s[18:19]
	s_mov_b32 m0, s57
	s_nop 0
	global_load_lds_dwordx4 v[192:193], off
	v_lshl_add_u64 v[192:193], v[232:233], 0, s[18:19]
	s_mov_b32 m0, s62
	s_nop 0
	global_load_lds_dwordx4 v[192:193], off
	s_waitcnt vmcnt(8)
	s_waitcnt lgkmcnt(0)
	s_barrier
	s_setprio 1
	v_mfma_i32_16x16x64_i8 v[62:65], v[152:155], v[196:199], v[62:65]
	v_mfma_i32_16x16x64_i8 v[58:61], v[160:163], v[196:199], v[58:61]
	v_mfma_i32_16x16x64_i8 v[46:49], v[152:155], v[204:207], v[46:49]
	v_mfma_i32_16x16x64_i8 v[42:45], v[160:163], v[204:207], v[42:45]
	v_mfma_i32_16x16x64_i8 v[30:33], v[152:155], v[212:215], v[30:33]
	v_mfma_i32_16x16x64_i8 v[26:29], v[160:163], v[212:215], v[26:29]
	v_mfma_i32_16x16x64_i8 v[6:9], v[152:155], v[220:223], v[6:9]
	v_mfma_i32_16x16x64_i8 v[2:5], v[160:163], v[220:223], v[2:5]
	v_mfma_i32_16x16x64_i8 v[62:65], v[156:159], v[200:203], v[62:65]
	v_mfma_i32_16x16x64_i8 v[58:61], v[164:167], v[200:203], v[58:61]
	v_mfma_i32_16x16x64_i8 v[46:49], v[156:159], v[208:211], v[46:49]
	v_mfma_i32_16x16x64_i8 v[42:45], v[164:167], v[208:211], v[42:45]
	v_mfma_i32_16x16x64_i8 v[30:33], v[156:159], v[216:219], v[30:33]
	v_mfma_i32_16x16x64_i8 v[26:29], v[164:167], v[216:219], v[26:29]
	v_mfma_i32_16x16x64_i8 v[6:9], v[156:159], v[224:227], v[6:9]
	v_mfma_i32_16x16x64_i8 v[2:5], v[164:167], v[224:227], v[2:5]
	v_mfma_i32_16x16x64_i8 v[54:57], v[168:171], v[196:199], v[54:57]
	v_mfma_i32_16x16x64_i8 v[50:53], v[184:187], v[196:199], v[50:53]
	v_mfma_i32_16x16x64_i8 v[38:41], v[168:171], v[204:207], v[38:41]
	v_mfma_i32_16x16x64_i8 v[34:37], v[184:187], v[204:207], v[34:37]
	v_mfma_i32_16x16x64_i8 v[14:17], v[168:171], v[212:215], v[14:17]
	v_mfma_i32_16x16x64_i8 v[10:13], v[184:187], v[212:215], v[10:13]
	v_mfma_i32_16x16x64_i8 v[22:25], v[168:171], v[220:223], v[22:25]
	v_mfma_i32_16x16x64_i8 v[18:21], v[184:187], v[220:223], v[18:21]
	v_mfma_i32_16x16x64_i8 v[54:57], v[180:183], v[200:203], v[54:57]
	v_mfma_i32_16x16x64_i8 v[50:53], v[188:191], v[200:203], v[50:53]
	v_mfma_i32_16x16x64_i8 v[38:41], v[180:183], v[208:211], v[38:41]
	v_mfma_i32_16x16x64_i8 v[34:37], v[188:191], v[208:211], v[34:37]
	v_mfma_i32_16x16x64_i8 v[14:17], v[180:183], v[216:219], v[14:17]
	v_mfma_i32_16x16x64_i8 v[10:13], v[188:191], v[216:219], v[10:13]
	v_mfma_i32_16x16x64_i8 v[22:25], v[180:183], v[224:227], v[22:25]
	v_mfma_i32_16x16x64_i8 v[18:21], v[188:191], v[224:227], v[18:21]
	s_setprio 0
	s_barrier
	s_add_i32 s71, s71, 2
	s_cmp_gt_u32 s71, 13
	s_mov_b64 s[36:37], s[38:39]
	s_cbranch_scc0 .LBB0_1385
	s_and_b64 vcc, exec, s[20:21]
	s_cbranch_vccz .LBB0_1388
	s_barrier

; #define PG8_STAGE(bufoff, gbase, voff) do { _Pragma("unroll") for (int _i = 0; _i < 2; ++_i) \
;         __builtin_amdgcn_global_load_lds((const unsigned*)((const char*)(gbase) + (voff)[_i]), (LAS unsigned*)(lds + (bufoff) + ldsw + _i * 8192), 16, 0, 0); } while (0)
; #define PG8_LDA(dst, b, h) do { _Pragma("unroll") for (int m = 0; m < 4; ++m) dst[m] = PG8_LD32(lds + PG8_SA(b, h) + aoff + m * 2048); } while (0)
; #define PG8_LDB(dst, b, h) do { _Pragma("unroll") for (int n = 0; n < 2; ++n) dst[n] = PG8_LD32(lds + PG8_SB(b, h) + boff + n * 2048); } while (0)
; #define PG8_WAIT_V(n) asm volatile("s_waitcnt vmcnt(" #n ")" ::: "memory")
; #define PG8_WAIT_L(n) asm volatile("s_waitcnt lgkmcnt(" #n ")" ::: "memory")
; #define PG8_BAR __builtin_amdgcn_s_barrier()
; #define PG8_SCHED __builtin_amdgcn_sched_barrier(0)
; #define PG8_STA(bufoff, nextflag, h, koff) do { if constexpr (Sched::GATHER) { unsigned _o[2]; _o[0] = (nextflag) ? nxtA[h][0] : curA[h][0]; _o[1] = (nextflag) ? nxtA[h][1] : curA[h][1]; PG8_STAGE(bufoff, Ab + (koff), _o); } \
;         else { PG8_STAGE(bufoff, ((nextflag) ? nA : cA) + (size_t)(h) * hstep + (koff), voffA); } } while (0)
; template <class Epi, class Sched, bool ALIGN_EPI, int DT>
; __device__ __forceinline__ void gemm_phase(LAS unsigned char* lds, const int KB, const Sched& S, const Epi& E) {
;     ...
;             PG8_LDB(B0, 0, 0); PG8_LDB(B1, 0, 1); PG8_SCHED; PG8_LDA(At, 0, 0); PG8_STA(PG8_SA(1, 1), false, 1, k1);
;             PG8_WAIT_V(8); PG8_WAIT_L(0); PG8_BAR; PG8_MMA(0, 0, At, B0); PG8_MMA(0, 1, At, B1); PG8_BAR; PG8_SCHED;
;             PG8_LDA(At, 0, 1); PG8_STAGE(PG8_SB(0, 0), b2, voffB); PG8_STAGE(PG8_SB(0, 1), b2 + hstep, voffB); PG8_STA(PG8_SA(0, 0), last, 0, k2);
;             PG8_WAIT_V(8); PG8_WAIT_L(0); PG8_BAR; PG8_MMA(1, 0, At, B0); PG8_MMA(1, 1, At, B1); PG8_BAR; PG8_SCHED;
.LBB0_2108:
	ds_read_b128 v[18:21], v193
	ds_read_b128 v[22:25], v193 offset:1024
	ds_read_b128 v[26:29], v193 offset:2048
	ds_read_b128 v[30:33], v193 offset:3072
	ds_read_b128 v[2:5], v195
	ds_read_b128 v[6:9], v195 offset:1024
	ds_read_b128 v[10:13], v195 offset:2048
	ds_read_b128 v[14:17], v195 offset:3072
	s_add_u32 s38, s42, 0x100
	s_addc_u32 s39, s43, 0
	s_add_u32 s71, s68, s42
	s_addc_u32 s74, s69, s43
	s_cmp_eq_u32 s70, 12
	s_cselect_b64 s[44:45], -1, 0
	s_and_b64 s[40:41], s[44:45], exec
	s_cselect_b32 s41, s25, s74
	s_cselect_b32 s40, s27, s71
	s_cselect_b32 s71, 0, s39
	s_cselect_b32 s74, 0, s38
	v_lshl_add_u64 v[222:223], v[178:179], 0, s[42:43]
	s_add_i32 m0, s35, 0xc000
	ds_read_b128 v[182:185], v196
	ds_read_b128 v[186:189], v196 offset:1024
	ds_read_b128 v[198:201], v196 offset:2048
	ds_read_b128 v[202:205], v196 offset:3072
	ds_read_b128 v[206:209], v196 offset:4096
	ds_read_b128 v[210:213], v196 offset:5120
	ds_read_b128 v[214:217], v196 offset:6144
	ds_read_b128 v[218:221], v196 offset:7168
	global_load_lds_dwordx4 v[222:223], off
	v_lshl_add_u64 v[222:223], v[180:181], 0, s[42:43]
	s_add_i32 m0, s35, 0xe000
	s_nop 0
	global_load_lds_dwordx4 v[222:223], off
	s_waitcnt vmcnt(8)
	s_waitcnt lgkmcnt(0)
	s_barrier
	s_setprio 1
	v_mfma_scale_f32_16x16x128_f8f6f4 v[158:161], v[18:25], v[182:189], v[158:161], v1, v1 op_sel_hi:[0,0,0]
	v_mfma_scale_f32_16x16x128_f8f6f4 v[154:157], v[26:33], v[182:189], v[154:157], v1, v1 op_sel_hi:[0,0,0]
	v_mfma_scale_f32_16x16x128_f8f6f4 v[150:153], v[18:25], v[198:205], v[150:153], v1, v1 op_sel_hi:[0,0,0]
	v_mfma_scale_f32_16x16x128_f8f6f4 v[142:145], v[26:33], v[198:205], v[142:145], v1, v1 op_sel_hi:[0,0,0]
	v_mfma_scale_f32_16x16x128_f8f6f4 v[134:137], v[18:25], v[206:213], v[134:137], v1, v1 op_sel_hi:[0,0,0]
	v_mfma_scale_f32_16x16x128_f8f6f4 v[126:129], v[26:33], v[206:213], v[126:129], v1, v1 op_sel_hi:[0,0,0]
	v_mfma_scale_f32_16x16x128_f8f6f4 v[118:121], v[18:25], v[214:221], v[118:121], v1, v1 op_sel_hi:[0,0,0]
	v_mfma_scale_f32_16x16x128_f8f6f4 v[110:113], v[26:33], v[214:221], v[110:113], v1, v1 op_sel_hi:[0,0,0]
	v_mfma_scale_f32_16x16x128_f8f6f4 v[146:149], v[2:9], v[182:189], v[146:149], v1, v1 op_sel_hi:[0,0,0]
	v_mfma_scale_f32_16x16x128_f8f6f4 v[138:141], v[10:17], v[182:189], v[138:141], v1, v1 op_sel_hi:[0,0,0]
	v_mfma_scale_f32_16x16x128_f8f6f4 v[130:133], v[2:9], v[198:205], v[130:133], v1, v1 op_sel_hi:[0,0,0]
	v_mfma_scale_f32_16x16x128_f8f6f4 v[122:125], v[10:17], v[198:205], v[122:125], v1, v1 op_sel_hi:[0,0,0]
	v_mfma_scale_f32_16x16x128_f8f6f4 v[114:117], v[2:9], v[206:213], v[114:117], v1, v1 op_sel_hi:[0,0,0]
	v_mfma_scale_f32_16x16x128_f8f6f4 v[106:109], v[10:17], v[206:213], v[106:109], v1, v1 op_sel_hi:[0,0,0]
	v_mfma_scale_f32_16x16x128_f8f6f4 v[102:105], v[2:9], v[214:221], v[102:105], v1, v1 op_sel_hi:[0,0,0]
	v_mfma_scale_f32_16x16x128_f8f6f4 v[98:101], v[10:17], v[214:221], v[98:101], v1, v1 op_sel_hi:[0,0,0]
	s_setprio 0
	s_barrier
	s_add_i32 s42, s57, s46
	v_lshl_add_u64 v[182:183], s[40:41], 0, v[162:163]
	s_mov_b32 m0, s42
	ds_read_b128 v[198:201], v196 offset:16384
	ds_read_b128 v[202:205], v196 offset:17408
	ds_read_b128 v[206:209], v196 offset:18432
	ds_read_b128 v[210:213], v196 offset:19456
	ds_read_b128 v[214:217], v196 offset:20480
	ds_read_b128 v[218:221], v196 offset:21504
	ds_read_b128 v[222:225], v196 offset:22528
	ds_read_b128 v[226:229], v196 offset:23552
	global_load_lds_dwordx4 v[182:183], off
	s_add_i32 m0, s42, 0x2000
	s_add_u32 s42, s40, 0x40000
	v_lshl_add_u64 v[184:185], s[40:41], 0, v[164:165]
	s_addc_u32 s43, s41, 0
	s_add_i32 s75, s62, s46
	global_load_lds_dwordx4 v[184:185], off
	v_lshl_add_u64 v[186:187], s[42:43], 0, v[162:163]
	s_mov_b32 m0, s75
	s_nop 0
	global_load_lds_dwordx4 v[186:187], off
	v_lshl_add_u64 v[186:187], s[42:43], 0, v[164:165]
	s_add_i32 m0, s75, 0x2000
	s_and_b64 s[42:43], s[6:7], s[44:45]
	s_and_b64 s[42:43], s[42:43], exec
	s_cselect_b32 s42, s28, s36
	s_cselect_b32 s43, s29, s37
	s_add_u32 s42, s42, s74
	s_addc_u32 s43, s43, s71
	global_load_lds_dwordx4 v[186:187], off
	v_lshl_add_u64 v[186:187], s[42:43], 0, v[166:167]
	s_mov_b32 m0, s35
	v_lshl_add_u64 v[188:189], s[42:43], 0, v[168:169]
	global_load_lds_dwordx4 v[186:187], off
	s_mov_b32 m0, s47
	s_nop 0
	global_load_lds_dwordx4 v[188:189], off
	s_waitcnt vmcnt(8)
	s_waitcnt lgkmcnt(0)
	s_barrier
	s_setprio 1
	v_mfma_scale_f32_16x16x128_f8f6f4 v[94:97], v[18:25], v[198:205], v[94:97], v1, v1 op_sel_hi:[0,0,0]
	v_mfma_scale_f32_16x16x128_f8f6f4 v[90:93], v[26:33], v[198:205], v[90:93], v1, v1 op_sel_hi:[0,0,0]
	v_mfma_scale_f32_16x16x128_f8f6f4 v[86:89], v[18:25], v[206:213], v[86:89], v1, v1 op_sel_hi:[0,0,0]
	v_mfma_scale_f32_16x16x128_f8f6f4 v[78:81], v[26:33], v[206:213], v[78:81], v1, v1 op_sel_hi:[0,0,0]
	v_mfma_scale_f32_16x16x128_f8f6f4 v[62:65], v[18:25], v[214:221], v[62:65], v1, v1 op_sel_hi:[0,0,0]
	v_mfma_scale_f32_16x16x128_f8f6f4 v[54:57], v[26:33], v[214:221], v[54:57], v1, v1 op_sel_hi:[0,0,0]
	v_mfma_scale_f32_16x16x128_f8f6f4 v[46:49], v[18:25], v[222:229], v[46:49], v1, v1 op_sel_hi:[0,0,0]
	v_mfma_scale_f32_16x16x128_f8f6f4 v[38:41], v[26:33], v[222:229], v[38:41], v1, v1 op_sel_hi:[0,0,0]
	v_mfma_scale_f32_16x16x128_f8f6f4 v[82:85], v[2:9], v[198:205], v[82:85], v1, v1 op_sel_hi:[0,0,0]
	v_mfma_scale_f32_16x16x128_f8f6f4 v[74:77], v[10:17], v[198:205], v[74:77], v1, v1 op_sel_hi:[0,0,0]
	v_mfma_scale_f32_16x16x128_f8f6f4 v[58:61], v[2:9], v[206:213], v[58:61], v1, v1 op_sel_hi:[0,0,0]
	v_mfma_scale_f32_16x16x128_f8f6f4 v[50:53], v[10:17], v[206:213], v[50:53], v1, v1 op_sel_hi:[0,0,0]
	v_mfma_scale_f32_16x16x128_f8f6f4 v[42:45], v[2:9], v[214:221], v[42:45], v1, v1 op_sel_hi:[0,0,0]
	v_mfma_scale_f32_16x16x128_f8f6f4 v[34:37], v[10:17], v[214:221], v[34:37], v1, v1 op_sel_hi:[0,0,0]
	v_mfma_scale_f32_16x16x128_f8f6f4 v[70:73], v[2:9], v[222:229], v[70:73], v1, v1 op_sel_hi:[0,0,0]
	v_mfma_scale_f32_16x16x128_f8f6f4 v[66:69], v[10:17], v[222:229], v[66:69], v1, v1 op_sel_hi:[0,0,0]
	s_setprio 0
	s_barrier
; #define PG8_STAGE(bufoff, gbase, voff) do { _Pragma("unroll") for (int _i = 0; _i < 2; ++_i) \
;         __builtin_amdgcn_global_load_lds((const unsigned*)((const char*)(gbase) + (voff)[_i]), (LAS unsigned*)(lds + (bufoff) + ldsw + _i * 8192), 16, 0, 0); } while (0)
; #define PG8_LDA(dst, b, h) do { _Pragma("unroll") for (int m = 0; m < 4; ++m) dst[m] = PG8_LD32(lds + PG8_SA(b, h) + aoff + m * 2048); } while (0)
; #define PG8_LDB(dst, b, h) do { _Pragma("unroll") for (int n = 0; n < 2; ++n) dst[n] = PG8_LD32(lds + PG8_SB(b, h) + boff + n * 2048); } while (0)
; #define PG8_WAIT_V(n) asm volatile("s_waitcnt vmcnt(" #n ")" ::: "memory")
; #define PG8_WAIT_L(n) asm volatile("s_waitcnt lgkmcnt(" #n ")" ::: "memory")
; #define PG8_BAR __builtin_amdgcn_s_barrier()
; #define PG8_SCHED __builtin_amdgcn_sched_barrier(0)
; #define PG8_STA(bufoff, nextflag, h, koff) do { if constexpr (Sched::GATHER) { unsigned _o[2]; _o[0] = (nextflag) ? nxtA[h][0] : curA[h][0]; _o[1] = (nextflag) ? nxtA[h][1] : curA[h][1]; PG8_STAGE(bufoff, Ab + (koff), _o); } \
;         else { PG8_STAGE(bufoff, ((nextflag) ? nA : cA) + (size_t)(h) * hstep + (koff), voffA); } } while (0)
; template <class Epi, class Sched, bool ALIGN_EPI, int DT>
; __device__ __forceinline__ void gemm_phase(LAS unsigned char* lds, const int KB, const Sched& S, const Epi& E) {
;     ...
;             PG8_LDB(B0, 1, 0); PG8_LDB(B1, 1, 1); PG8_SCHED; PG8_LDA(At, 1, 0); PG8_STA(PG8_SA(0, 1), last, 1, k2);
;             PG8_WAIT_V(8); PG8_WAIT_L(0); PG8_BAR; PG8_MMA(0, 0, At, B0); PG8_MMA(0, 1, At, B1); PG8_BAR; PG8_SCHED;
;             PG8_LDA(At, 1, 1); PG8_STAGE(PG8_SB(1, 0), b3, voffB); PG8_STAGE(PG8_SB(1, 1), b3 + hstep, voffB); PG8_STA(PG8_SA(1, 0), last, 0, k3);
;             PG8_WAIT_V(8); PG8_WAIT_L(0); PG8_BAR; PG8_MMA(1, 0, At, B0); PG8_MMA(1, 1, At, B1); PG8_BAR; PG8_SCHED;
;         }
;         if constexpr (ALIGN_EPI) { if (wr == 0) PG8_BAR; }
	s_add_i32 s44, 0, 0x18000
	s_add_i32 s45, 0, 0x1c000
	v_add_u32_e32 v14, s44, v191
	v_add_u32_e32 v30, s45, v191
	ds_read_b128 v[2:5], v14
	ds_read_b128 v[6:9], v14 offset:1024
	ds_read_b128 v[10:13], v14 offset:2048
	ds_read_b128 v[14:17], v14 offset:3072
	ds_read_b128 v[18:21], v30
	ds_read_b128 v[22:25], v30 offset:1024
	ds_read_b128 v[26:29], v30 offset:2048
	ds_read_b128 v[30:33], v30 offset:3072
	s_add_u32 s42, s42, 0x40000
	s_addc_u32 s43, s43, 0
	s_mov_b32 m0, s49
	v_lshl_add_u64 v[230:231], s[42:43], 0, v[166:167]
	ds_read_b128 v[198:201], v196 offset:32768
	ds_read_b128 v[202:205], v196 offset:33792
	ds_read_b128 v[206:209], v196 offset:34816
	ds_read_b128 v[210:213], v196 offset:35840
	ds_read_b128 v[214:217], v196 offset:36864
	ds_read_b128 v[218:221], v196 offset:37888
	ds_read_b128 v[222:225], v196 offset:38912
	ds_read_b128 v[226:229], v196 offset:39936
	global_load_lds_dwordx4 v[230:231], off
	v_lshl_add_u64 v[230:231], s[42:43], 0, v[168:169]
	s_mov_b32 m0, s52
	s_nop 0
	global_load_lds_dwordx4 v[230:231], off
	s_waitcnt vmcnt(8)
	s_waitcnt lgkmcnt(0)
	s_barrier
	s_setprio 1
	v_mfma_scale_f32_16x16x128_f8f6f4 v[158:161], v[2:9], v[198:205], v[158:161], v1, v1 op_sel_hi:[0,0,0]
	v_mfma_scale_f32_16x16x128_f8f6f4 v[154:157], v[10:17], v[198:205], v[154:157], v1, v1 op_sel_hi:[0,0,0]
	v_mfma_scale_f32_16x16x128_f8f6f4 v[150:153], v[2:9], v[206:213], v[150:153], v1, v1 op_sel_hi:[0,0,0]
	v_mfma_scale_f32_16x16x128_f8f6f4 v[142:145], v[10:17], v[206:213], v[142:145], v1, v1 op_sel_hi:[0,0,0]
	v_mfma_scale_f32_16x16x128_f8f6f4 v[134:137], v[2:9], v[214:221], v[134:137], v1, v1 op_sel_hi:[0,0,0]
	v_mfma_scale_f32_16x16x128_f8f6f4 v[126:129], v[10:17], v[214:221], v[126:129], v1, v1 op_sel_hi:[0,0,0]
	v_mfma_scale_f32_16x16x128_f8f6f4 v[118:121], v[2:9], v[222:229], v[118:121], v1, v1 op_sel_hi:[0,0,0]
	v_mfma_scale_f32_16x16x128_f8f6f4 v[110:113], v[10:17], v[222:229], v[110:113], v1, v1 op_sel_hi:[0,0,0]
	v_mfma_scale_f32_16x16x128_f8f6f4 v[146:149], v[18:25], v[198:205], v[146:149], v1, v1 op_sel_hi:[0,0,0]
	v_mfma_scale_f32_16x16x128_f8f6f4 v[138:141], v[26:33], v[198:205], v[138:141], v1, v1 op_sel_hi:[0,0,0]
	v_mfma_scale_f32_16x16x128_f8f6f4 v[130:133], v[18:25], v[206:213], v[130:133], v1, v1 op_sel_hi:[0,0,0]
	v_mfma_scale_f32_16x16x128_f8f6f4 v[122:125], v[26:33], v[206:213], v[122:125], v1, v1 op_sel_hi:[0,0,0]
	v_mfma_scale_f32_16x16x128_f8f6f4 v[114:117], v[18:25], v[214:221], v[114:117], v1, v1 op_sel_hi:[0,0,0]
	v_mfma_scale_f32_16x16x128_f8f6f4 v[106:109], v[26:33], v[214:221], v[106:109], v1, v1 op_sel_hi:[0,0,0]
	v_mfma_scale_f32_16x16x128_f8f6f4 v[102:105], v[18:25], v[222:229], v[102:105], v1, v1 op_sel_hi:[0,0,0]
	v_mfma_scale_f32_16x16x128_f8f6f4 v[98:101], v[26:33], v[222:229], v[98:101], v1, v1 op_sel_hi:[0,0,0]
	s_setprio 0
	s_barrier
	s_add_i32 s42, s44, s46
	v_lshl_add_u64 v[182:183], v[182:183], 0, s[10:11]
	s_mov_b32 m0, s42
	ds_read_b128 v[198:201], v196 offset:49152
	ds_read_b128 v[202:205], v196 offset:50176
	ds_read_b128 v[206:209], v196 offset:51200
	ds_read_b128 v[210:213], v196 offset:52224
	ds_read_b128 v[214:217], v196 offset:53248
	ds_read_b128 v[218:221], v196 offset:54272
	ds_read_b128 v[222:225], v196 offset:55296
	ds_read_b128 v[226:229], v196 offset:56320
	global_load_lds_dwordx4 v[182:183], off
	s_add_i32 m0, s42, 0x2000
	s_add_u32 s40, s40, 0x40080
	v_lshl_add_u64 v[182:183], v[184:185], 0, s[10:11]
	s_addc_u32 s41, s41, 0
	s_add_i32 s42, s45, s46
	global_load_lds_dwordx4 v[182:183], off
	v_lshl_add_u64 v[182:183], s[40:41], 0, v[162:163]
	s_mov_b32 m0, s42
	s_nop 0
	global_load_lds_dwordx4 v[182:183], off
	v_lshl_add_u64 v[182:183], s[40:41], 0, v[164:165]
	s_add_i32 m0, s42, 0x2000
	s_nop 0
	global_load_lds_dwordx4 v[182:183], off
	v_lshl_add_u64 v[182:183], v[186:187], 0, s[10:11]
	s_mov_b32 m0, s54
	s_nop 0
	global_load_lds_dwordx4 v[182:183], off
	v_lshl_add_u64 v[182:183], v[188:189], 0, s[10:11]
	s_mov_b32 m0, s55
	s_nop 0
	global_load_lds_dwordx4 v[182:183], off
	s_waitcnt vmcnt(8)
	s_waitcnt lgkmcnt(0)
	s_barrier
	s_setprio 1
	v_mfma_scale_f32_16x16x128_f8f6f4 v[94:97], v[2:9], v[198:205], v[94:97], v1, v1 op_sel_hi:[0,0,0]
	v_mfma_scale_f32_16x16x128_f8f6f4 v[90:93], v[10:17], v[198:205], v[90:93], v1, v1 op_sel_hi:[0,0,0]
	v_mfma_scale_f32_16x16x128_f8f6f4 v[86:89], v[2:9], v[206:213], v[86:89], v1, v1 op_sel_hi:[0,0,0]
	v_mfma_scale_f32_16x16x128_f8f6f4 v[78:81], v[10:17], v[206:213], v[78:81], v1, v1 op_sel_hi:[0,0,0]
	v_mfma_scale_f32_16x16x128_f8f6f4 v[62:65], v[2:9], v[214:221], v[62:65], v1, v1 op_sel_hi:[0,0,0]
	v_mfma_scale_f32_16x16x128_f8f6f4 v[54:57], v[10:17], v[214:221], v[54:57], v1, v1 op_sel_hi:[0,0,0]
	v_mfma_scale_f32_16x16x128_f8f6f4 v[46:49], v[2:9], v[222:229], v[46:49], v1, v1 op_sel_hi:[0,0,0]
	v_mfma_scale_f32_16x16x128_f8f6f4 v[38:41], v[10:17], v[222:229], v[38:41], v1, v1 op_sel_hi:[0,0,0]
	v_mfma_scale_f32_16x16x128_f8f6f4 v[82:85], v[18:25], v[198:205], v[82:85], v1, v1 op_sel_hi:[0,0,0]
	v_mfma_scale_f32_16x16x128_f8f6f4 v[74:77], v[26:33], v[198:205], v[74:77], v1, v1 op_sel_hi:[0,0,0]
	v_mfma_scale_f32_16x16x128_f8f6f4 v[58:61], v[18:25], v[206:213], v[58:61], v1, v1 op_sel_hi:[0,0,0]
	v_mfma_scale_f32_16x16x128_f8f6f4 v[50:53], v[26:33], v[206:213], v[50:53], v1, v1 op_sel_hi:[0,0,0]
	v_mfma_scale_f32_16x16x128_f8f6f4 v[42:45], v[18:25], v[214:221], v[42:45], v1, v1 op_sel_hi:[0,0,0]
	v_mfma_scale_f32_16x16x128_f8f6f4 v[34:37], v[26:33], v[214:221], v[34:37], v1, v1 op_sel_hi:[0,0,0]
	v_mfma_scale_f32_16x16x128_f8f6f4 v[70:73], v[18:25], v[222:229], v[70:73], v1, v1 op_sel_hi:[0,0,0]
	v_mfma_scale_f32_16x16x128_f8f6f4 v[66:69], v[26:33], v[222:229], v[66:69], v1, v1 op_sel_hi:[0,0,0]
	s_setprio 0
	s_barrier
	s_add_i32 s70, s70, 2
	s_cmp_gt_u32 s70, 13
	s_mov_b64 s[42:43], s[38:39]
	s_cbranch_scc0 .LBB0_2108
	s_and_b64 vcc, exec, s[12:13]
	s_cbranch_vccz .LBB0_2111
	s_barrier

;     __device__ __forceinline__ bool next(int i, Unit& u) const { u.e = 0; return static_next(i, G, c, nM, nN, u.pm, u.pn); }
; #define PG8_STAGE(bufoff, gbase, voff) do { _Pragma("unroll") for (int _i = 0; _i < 2; ++_i) \
;         __builtin_amdgcn_global_load_lds((const unsigned*)((const char*)(gbase) + (voff)[_i]), (LAS unsigned*)(lds + (bufoff) + ldsw + _i * 8192), 16, 0, 0); } while (0)
; #define PG8_LDA(dst, b, h) do { _Pragma("unroll") for (int m = 0; m < 4; ++m) dst[m] = PG8_LD32(lds + PG8_SA(b, h) + aoff + m * 2048); } while (0)
; template <class Epi, class Sched, bool ALIGN_EPI, int DT>
; __device__ __forceinline__ void gemm_phase(LAS unsigned char* lds, const int KB, const Sched& S, const Epi& E) {
;     ...
;     PG8_STAGE(PG8_SB(0, 0), cB, voffB); PG8_STAGE(PG8_SB(0, 1), cB + hstep, voffB); PG8_STA(PG8_SA(0, 0), false, 0, 0); PG8_STA(PG8_SA(0, 1), false, 1, 0);
;     if (wr == 1) PG8_BAR;
;     PG8_WAIT_V(2); PG8_BAR;
;     PG8_STAGE(PG8_SB(1, 0), cB + kstep, voffB); PG8_STA(PG8_SA(1, 0), false, 0, kstep); PG8_STAGE(PG8_SB(1, 1), cB + hstep + kstep, voffB);
;     PG8_WAIT_V(6); PG8_BAR;
;     for (;;) {
;         const bool has_next = S.next(ui + 1, nxt);
;         if constexpr (Sched::GATHER) {
;             if (has_next) S.a_offsets(nxt, Rr, Cc, nxtA);
;             else {
; #pragma unroll
;                 for (int h = 0; h < 2; ++h)
; #pragma unroll
;                     for (int i = 0; i < 2; ++i) nxtA[h][i] = curA[h][i]; }
;         } else nA = has_next ? Ab + (size_t)nxt.pm * 2 * hstep : cA;
;         const char* nB = has_next ? S.b_base(nxt) : cB;
;         for (int t = 0; t < nt; t += 2) {
;             const bool last = (t == nt - 2);
;             const size_t k1 = (size_t)(t + 1) * kstep, k2 = last ? 0 : (size_t)(t + 2) * kstep, k3 = k2 + kstep;
;             const char* b2 = last ? nB : cB + (size_t)(t + 2) * kstep; const char* b3 = b2 + kstep;
;             PG8_LDB(B0, 0, 0); PG8_LDB(B1, 0, 1); PG8_SCHED; PG8_LDA(At, 0, 0); PG8_STA(PG8_SA(1, 1), false, 1, k1);
;             PG8_WAIT_V(8); PG8_WAIT_L(0); PG8_BAR; PG8_MMA(0, 0, At, B0); PG8_MMA(0, 1, At, B1); PG8_BAR; PG8_SCHED;
;             PG8_LDA(At, 0, 1); PG8_STAGE(PG8_SB(0, 0), b2, voffB); PG8_STAGE(PG8_SB(0, 1), b2 + hstep, voffB); PG8_STA(PG8_SA(0, 0), last, 0, k2);
;             PG8_WAIT_V(8); PG8_WAIT_L(0); PG8_BAR; PG8_MMA(1, 0, At, B0); PG8_MMA(1, 1, At, B1); PG8_BAR; PG8_SCHED;
.LBB0_2294:
	v_add_u32_e32 v79, s65, v167
	ds_read_b128 v[142:145], v79
	ds_read_b128 v[156:159], v79 offset:1024
	ds_read_b128 v[178:181], v79 offset:2048
	ds_read_b128 v[182:185], v79 offset:3072
	v_add_u32_e32 v79, s66, v167
	ds_read_b128 v[186:189], v79
	ds_read_b128 v[190:193], v79 offset:1024
	ds_read_b128 v[196:199], v79 offset:2048
	ds_read_b128 v[200:203], v79 offset:3072
	s_add_u32 s40, s8, 0x100
	s_addc_u32 s41, s9, 0
	s_cmpk_eq_i32 s8, 0x700
	s_cselect_b64 vcc, -1, 0
	v_lshl_add_u64 v[160:161], v[88:89], 0, s[8:9]
	s_and_b64 s[76:77], vcc, exec
	v_cndmask_b32_e32 v161, v161, v155, vcc
	s_cselect_b32 s75, 0, s40
	v_cndmask_b32_e32 v160, v160, v154, vcc
	v_lshl_add_u64 v[236:237], v[140:141], 0, s[8:9]
	s_add_i32 m0, s42, 0xc000
	ds_read_b128 v[204:207], v169
	ds_read_b128 v[208:211], v169 offset:1024
	ds_read_b128 v[212:215], v169 offset:2048
	ds_read_b128 v[216:219], v169 offset:3072
	ds_read_b128 v[220:223], v169 offset:4096
	ds_read_b128 v[224:227], v169 offset:5120
	ds_read_b128 v[228:231], v169 offset:6144
	ds_read_b128 v[232:235], v169 offset:7168
	global_load_lds_dwordx4 v[236:237], off
	v_lshl_add_u64 v[236:237], v[138:139], 0, s[8:9]
	s_add_i32 m0, s42, 0xe000
	s_nop 0
	global_load_lds_dwordx4 v[236:237], off
	s_waitcnt vmcnt(8)
	s_waitcnt lgkmcnt(0)
	s_barrier
	s_setprio 1
	v_mfma_i32_16x16x64_i8 v[134:137], v[142:145], v[204:207], v[134:137]
	v_mfma_i32_16x16x64_i8 v[126:129], v[178:181], v[204:207], v[126:129]
	v_mfma_i32_16x16x64_i8 v[118:121], v[142:145], v[212:215], v[118:121]
	v_mfma_i32_16x16x64_i8 v[110:113], v[178:181], v[212:215], v[110:113]
	v_mfma_i32_16x16x64_i8 v[102:105], v[142:145], v[220:223], v[102:105]
	v_mfma_i32_16x16x64_i8 v[94:97], v[178:181], v[220:223], v[94:97]
	v_mfma_i32_16x16x64_i8 v[82:85], v[142:145], v[228:231], v[82:85]
	v_mfma_i32_16x16x64_i8 v[70:73], v[178:181], v[228:231], v[70:73]
	v_mfma_i32_16x16x64_i8 v[134:137], v[156:159], v[208:211], v[134:137]
	v_mfma_i32_16x16x64_i8 v[126:129], v[182:185], v[208:211], v[126:129]
	v_mfma_i32_16x16x64_i8 v[118:121], v[156:159], v[216:219], v[118:121]
	v_mfma_i32_16x16x64_i8 v[110:113], v[182:185], v[216:219], v[110:113]
	v_mfma_i32_16x16x64_i8 v[102:105], v[156:159], v[224:227], v[102:105]
	v_mfma_i32_16x16x64_i8 v[94:97], v[182:185], v[224:227], v[94:97]
	v_mfma_i32_16x16x64_i8 v[82:85], v[156:159], v[232:235], v[82:85]
	v_mfma_i32_16x16x64_i8 v[70:73], v[182:185], v[232:235], v[70:73]
	v_mfma_i32_16x16x64_i8 v[130:133], v[186:189], v[204:207], v[130:133]
	v_mfma_i32_16x16x64_i8 v[122:125], v[196:199], v[204:207], v[122:125]
	v_mfma_i32_16x16x64_i8 v[114:117], v[186:189], v[212:215], v[114:117]
	v_mfma_i32_16x16x64_i8 v[106:109], v[196:199], v[212:215], v[106:109]
	v_mfma_i32_16x16x64_i8 v[98:101], v[186:189], v[220:223], v[98:101]
	v_mfma_i32_16x16x64_i8 v[90:93], v[196:199], v[220:223], v[90:93]
	v_mfma_i32_16x16x64_i8 v[74:77], v[186:189], v[228:231], v[74:77]
	v_mfma_i32_16x16x64_i8 v[66:69], v[196:199], v[228:231], v[66:69]
	v_mfma_i32_16x16x64_i8 v[130:133], v[190:193], v[208:211], v[130:133]
	v_mfma_i32_16x16x64_i8 v[122:125], v[200:203], v[208:211], v[122:125]
	v_mfma_i32_16x16x64_i8 v[114:117], v[190:193], v[216:219], v[114:117]
	v_mfma_i32_16x16x64_i8 v[106:109], v[200:203], v[216:219], v[106:109]
	v_mfma_i32_16x16x64_i8 v[98:101], v[190:193], v[224:227], v[98:101]
	v_mfma_i32_16x16x64_i8 v[90:93], v[200:203], v[224:227], v[90:93]
	v_mfma_i32_16x16x64_i8 v[74:77], v[190:193], v[232:235], v[74:77]
	v_mfma_i32_16x16x64_i8 v[66:69], v[200:203], v[232:235], v[66:69]
	s_setprio 0
	s_barrier
	s_add_i32 s8, s65, s33
	v_lshl_add_u64 v[236:237], v[160:161], 0, v[148:149]
	s_mov_b32 m0, s8
	ds_read_b128 v[204:207], v169 offset:16384
	ds_read_b128 v[208:211], v169 offset:17408
	ds_read_b128 v[212:215], v169 offset:18432
	ds_read_b128 v[216:219], v169 offset:19456
	ds_read_b128 v[220:223], v169 offset:20480
	ds_read_b128 v[224:227], v169 offset:21504
	ds_read_b128 v[228:231], v169 offset:22528
	ds_read_b128 v[232:235], v169 offset:23552
	global_load_lds_dwordx4 v[236:237], off
	v_lshl_add_u64 v[238:239], v[160:161], 0, v[150:151]
	s_add_i32 m0, s8, 0x2000
	v_lshl_add_u64 v[240:241], v[160:161], 0, s[10:11]
	s_add_i32 s8, s66, s33
	global_load_lds_dwordx4 v[238:239], off
	v_lshl_add_u64 v[242:243], v[240:241], 0, v[148:149]
	s_mov_b32 m0, s8
	v_lshl_add_u64 v[240:241], v[240:241], 0, v[150:151]
	global_load_lds_dwordx4 v[242:243], off
	s_add_i32 m0, s8, 0x2000
	s_add_u32 s8, s60, s75
	global_load_lds_dwordx4 v[240:241], off
	v_cndmask_b32_e32 v146, v81, v173, vcc
	s_addc_u32 s9, s61, 0
	s_mov_b32 m0, s42
	v_cndmask_b32_e32 v240, v80, v174, vcc
	global_load_lds_dwordx4 v146, s[8:9]
	s_mov_b32 m0, s43
	v_mov_b32_e32 v241, v147
	global_load_lds_dwordx4 v240, s[8:9]
	s_waitcnt vmcnt(8)
	s_waitcnt lgkmcnt(0)
	v_lshl_add_u64 v[242:243], s[8:9], 0, v[146:147]
	v_lshl_add_u64 v[240:241], s[8:9], 0, v[240:241]
	s_barrier
; #define PG8_LDA(dst, b, h) do { _Pragma("unroll") for (int m = 0; m < 4; ++m) dst[m] = PG8_LD32(lds + PG8_SA(b, h) + aoff + m * 2048); } while (0)
; #define PG8_LDB(dst, b, h) do { _Pragma("unroll") for (int n = 0; n < 2; ++n) dst[n] = PG8_LD32(lds + PG8_SB(b, h) + boff + n * 2048); } while (0)
; #define PG8_WAIT_V(n) asm volatile("s_waitcnt vmcnt(" #n ")" ::: "memory")
; #define PG8_WAIT_L(n) asm volatile("s_waitcnt lgkmcnt(" #n ")" ::: "memory")
; #define PG8_BAR __builtin_amdgcn_s_barrier()
; #define PG8_SCHED __builtin_amdgcn_sched_barrier(0)
; #define PG8_STA(bufoff, nextflag, h, koff) do { if constexpr (Sched::GATHER) { unsigned _o[2]; _o[0] = (nextflag) ? nxtA[h][0] : curA[h][0]; _o[1] = (nextflag) ? nxtA[h][1] : curA[h][1]; PG8_STAGE(bufoff, Ab + (koff), _o); } \
;         else { PG8_STAGE(bufoff, ((nextflag) ? nA : cA) + (size_t)(h) * hstep + (koff), voffA); } } while (0)
; template <class Epi, class Sched, bool ALIGN_EPI, int DT>
; __device__ __forceinline__ void gemm_phase(LAS unsigned char* lds, const int KB, const Sched& S, const Epi& E) {
;     ...
;             PG8_WAIT_V(8); PG8_WAIT_L(0); PG8_BAR; PG8_MMA(1, 0, At, B0); PG8_MMA(1, 1, At, B1); PG8_BAR; PG8_SCHED;
;             PG8_LDB(B0, 1, 0); PG8_LDB(B1, 1, 1); PG8_SCHED; PG8_LDA(At, 1, 0); PG8_STA(PG8_SA(0, 1), last, 1, k2);
;             PG8_WAIT_V(8); PG8_WAIT_L(0); PG8_BAR; PG8_MMA(0, 0, At, B0); PG8_MMA(0, 1, At, B1); PG8_BAR; PG8_SCHED;
	s_setprio 1
	v_mfma_i32_16x16x64_i8 v[54:57], v[142:145], v[204:207], v[54:57]
	v_mfma_i32_16x16x64_i8 v[50:53], v[178:181], v[204:207], v[50:53]
	v_mfma_i32_16x16x64_i8 v[42:45], v[142:145], v[212:215], v[42:45]
	v_mfma_i32_16x16x64_i8 v[34:37], v[178:181], v[212:215], v[34:37]
	v_mfma_i32_16x16x64_i8 v[26:29], v[142:145], v[220:223], v[26:29]
	v_mfma_i32_16x16x64_i8 v[18:21], v[178:181], v[220:223], v[18:21]
	v_mfma_i32_16x16x64_i8 v[10:13], v[142:145], v[228:231], v[10:13]
	v_mfma_i32_16x16x64_i8 v[2:5], v[178:181], v[228:231], v[2:5]
	v_mfma_i32_16x16x64_i8 v[54:57], v[156:159], v[208:211], v[54:57]
	v_mfma_i32_16x16x64_i8 v[50:53], v[182:185], v[208:211], v[50:53]
	v_mfma_i32_16x16x64_i8 v[42:45], v[156:159], v[216:219], v[42:45]
	v_mfma_i32_16x16x64_i8 v[34:37], v[182:185], v[216:219], v[34:37]
	v_mfma_i32_16x16x64_i8 v[26:29], v[156:159], v[224:227], v[26:29]
	v_mfma_i32_16x16x64_i8 v[18:21], v[182:185], v[224:227], v[18:21]
	v_mfma_i32_16x16x64_i8 v[10:13], v[156:159], v[232:235], v[10:13]
	v_mfma_i32_16x16x64_i8 v[2:5], v[182:185], v[232:235], v[2:5]
	v_mfma_i32_16x16x64_i8 v[62:65], v[186:189], v[204:207], v[62:65]
	v_mfma_i32_16x16x64_i8 v[58:61], v[196:199], v[204:207], v[58:61]
	v_mfma_i32_16x16x64_i8 v[46:49], v[186:189], v[212:215], v[46:49]
	v_mfma_i32_16x16x64_i8 v[38:41], v[196:199], v[212:215], v[38:41]
	v_mfma_i32_16x16x64_i8 v[30:33], v[186:189], v[220:223], v[30:33]
	v_mfma_i32_16x16x64_i8 v[22:25], v[196:199], v[220:223], v[22:25]
	v_mfma_i32_16x16x64_i8 v[14:17], v[186:189], v[228:231], v[14:17]
	v_mfma_i32_16x16x64_i8 v[6:9], v[196:199], v[228:231], v[6:9]
	v_mfma_i32_16x16x64_i8 v[62:65], v[190:193], v[208:211], v[62:65]
	v_mfma_i32_16x16x64_i8 v[58:61], v[200:203], v[208:211], v[58:61]
	v_mfma_i32_16x16x64_i8 v[46:49], v[190:193], v[216:219], v[46:49]
	v_mfma_i32_16x16x64_i8 v[38:41], v[200:203], v[216:219], v[38:41]
	v_mfma_i32_16x16x64_i8 v[30:33], v[190:193], v[224:227], v[30:33]
	v_mfma_i32_16x16x64_i8 v[22:25], v[200:203], v[224:227], v[22:25]
	v_mfma_i32_16x16x64_i8 v[14:17], v[190:193], v[232:235], v[14:17]
	v_mfma_i32_16x16x64_i8 v[6:9], v[200:203], v[232:235], v[6:9]
	s_setprio 0
	s_barrier
	s_add_i32 s75, 0, 0x18000
	v_add_u32_e32 v79, s75, v167
	s_add_i32 s76, 0, 0x1c000
	ds_read_b128 v[142:145], v79
	ds_read_b128 v[156:159], v79 offset:1024
	ds_read_b128 v[178:181], v79 offset:2048
	ds_read_b128 v[182:185], v79 offset:3072
	v_add_u32_e32 v79, s76, v167
	ds_read_b128 v[186:189], v79
	ds_read_b128 v[190:193], v79 offset:1024
	ds_read_b128 v[196:199], v79 offset:2048
	ds_read_b128 v[200:203], v79 offset:3072
	s_mov_b32 m0, s44
	v_cndmask_b32_e32 v79, v78, v175, vcc
	ds_read_b128 v[204:207], v169 offset:32768
	ds_read_b128 v[208:211], v169 offset:33792
	ds_read_b128 v[212:215], v169 offset:34816
	ds_read_b128 v[216:219], v169 offset:35840
	ds_read_b128 v[220:223], v169 offset:36864
	ds_read_b128 v[224:227], v169 offset:37888
	ds_read_b128 v[228:231], v169 offset:38912
	ds_read_b128 v[232:235], v169 offset:39936
	v_cndmask_b32_e32 v87, v86, v176, vcc
	global_load_lds_dwordx4 v79, s[8:9]
	s_mov_b32 m0, s45
	s_nop 0
	global_load_lds_dwordx4 v87, s[8:9]
	s_waitcnt vmcnt(8)
	s_waitcnt lgkmcnt(0)
	s_barrier
	s_setprio 1
	v_mfma_i32_16x16x64_i8 v[134:137], v[142:145], v[204:207], v[134:137]
	v_mfma_i32_16x16x64_i8 v[126:129], v[178:181], v[204:207], v[126:129]
	v_mfma_i32_16x16x64_i8 v[118:121], v[142:145], v[212:215], v[118:121]
	v_mfma_i32_16x16x64_i8 v[110:113], v[178:181], v[212:215], v[110:113]
	v_mfma_i32_16x16x64_i8 v[102:105], v[142:145], v[220:223], v[102:105]
	v_mfma_i32_16x16x64_i8 v[94:97], v[178:181], v[220:223], v[94:97]
	v_mfma_i32_16x16x64_i8 v[82:85], v[142:145], v[228:231], v[82:85]
	v_mfma_i32_16x16x64_i8 v[70:73], v[178:181], v[228:231], v[70:73]
	v_mfma_i32_16x16x64_i8 v[134:137], v[156:159], v[208:211], v[134:137]
	v_mfma_i32_16x16x64_i8 v[126:129], v[182:185], v[208:211], v[126:129]
	v_mfma_i32_16x16x64_i8 v[118:121], v[156:159], v[216:219], v[118:121]
	v_mfma_i32_16x16x64_i8 v[110:113], v[182:185], v[216:219], v[110:113]
	v_mfma_i32_16x16x64_i8 v[102:105], v[156:159], v[224:227], v[102:105]
	v_mfma_i32_16x16x64_i8 v[94:97], v[182:185], v[224:227], v[94:97]
	v_mfma_i32_16x16x64_i8 v[82:85], v[156:159], v[232:235], v[82:85]
	v_mfma_i32_16x16x64_i8 v[70:73], v[182:185], v[232:235], v[70:73]
	v_mfma_i32_16x16x64_i8 v[130:133], v[186:189], v[204:207], v[130:133]
	v_mfma_i32_16x16x64_i8 v[122:125], v[196:199], v[204:207], v[122:125]
	v_mfma_i32_16x16x64_i8 v[114:117], v[186:189], v[212:215], v[114:117]
	v_mfma_i32_16x16x64_i8 v[106:109], v[196:199], v[212:215], v[106:109]
	v_mfma_i32_16x16x64_i8 v[98:101], v[186:189], v[220:223], v[98:101]
	v_mfma_i32_16x16x64_i8 v[90:93], v[196:199], v[220:223], v[90:93]
	v_mfma_i32_16x16x64_i8 v[74:77], v[186:189], v[228:231], v[74:77]
	v_mfma_i32_16x16x64_i8 v[66:69], v[196:199], v[228:231], v[66:69]
	v_mfma_i32_16x16x64_i8 v[130:133], v[190:193], v[208:211], v[130:133]
	v_mfma_i32_16x16x64_i8 v[122:125], v[200:203], v[208:211], v[122:125]
	v_mfma_i32_16x16x64_i8 v[114:117], v[190:193], v[216:219], v[114:117]
	v_mfma_i32_16x16x64_i8 v[106:109], v[200:203], v[216:219], v[106:109]
	v_mfma_i32_16x16x64_i8 v[98:101], v[190:193], v[224:227], v[98:101]
	v_mfma_i32_16x16x64_i8 v[90:93], v[200:203], v[224:227], v[90:93]
	v_mfma_i32_16x16x64_i8 v[74:77], v[190:193], v[232:235], v[74:77]
	v_mfma_i32_16x16x64_i8 v[66:69], v[200:203], v[232:235], v[66:69]
	s_setprio 0
	s_barrier
; #define PG8_STAGE(bufoff, gbase, voff) do { _Pragma("unroll") for (int _i = 0; _i < 2; ++_i) \
;         __builtin_amdgcn_global_load_lds((const unsigned*)((const char*)(gbase) + (voff)[_i]), (LAS unsigned*)(lds + (bufoff) + ldsw + _i * 8192), 16, 0, 0); } while (0)
; #define PG8_LDA(dst, b, h) do { _Pragma("unroll") for (int m = 0; m < 4; ++m) dst[m] = PG8_LD32(lds + PG8_SA(b, h) + aoff + m * 2048); } while (0)
; #define PG8_WAIT_V(n) asm volatile("s_waitcnt vmcnt(" #n ")" ::: "memory")
; #define PG8_WAIT_L(n) asm volatile("s_waitcnt lgkmcnt(" #n ")" ::: "memory")
; #define PG8_BAR __builtin_amdgcn_s_barrier()
; #define PG8_SCHED __builtin_amdgcn_sched_barrier(0)
; #define PG8_STA(bufoff, nextflag, h, koff) do { if constexpr (Sched::GATHER) { unsigned _o[2]; _o[0] = (nextflag) ? nxtA[h][0] : curA[h][0]; _o[1] = (nextflag) ? nxtA[h][1] : curA[h][1]; PG8_STAGE(bufoff, Ab + (koff), _o); } \
;         else { PG8_STAGE(bufoff, ((nextflag) ? nA : cA) + (size_t)(h) * hstep + (koff), voffA); } } while (0)
; template <class Epi, class Sched, bool ALIGN_EPI, int DT>
; __device__ __forceinline__ void gemm_phase(LAS unsigned char* lds, const int KB, const Sched& S, const Epi& E) {
;     ...
;             PG8_LDA(At, 1, 1); PG8_STAGE(PG8_SB(1, 0), b3, voffB); PG8_STAGE(PG8_SB(1, 1), b3 + hstep, voffB); PG8_STA(PG8_SA(1, 0), last, 0, k3);
;             PG8_WAIT_V(8); PG8_WAIT_L(0); PG8_BAR; PG8_MMA(1, 0, At, B0); PG8_MMA(1, 1, At, B1); PG8_BAR; PG8_SCHED;
;         }
;         if constexpr (ALIGN_EPI) { if (wr == 0) PG8_BAR; }
	s_add_i32 s8, s75, s33
	v_lshl_add_u64 v[236:237], v[236:237], 0, s[20:21]
	s_mov_b32 m0, s8
	ds_read_b128 v[204:207], v169 offset:49152
	ds_read_b128 v[208:211], v169 offset:50176
	ds_read_b128 v[212:215], v169 offset:51200
	ds_read_b128 v[216:219], v169 offset:52224
	ds_read_b128 v[220:223], v169 offset:53248
	ds_read_b128 v[224:227], v169 offset:54272
	ds_read_b128 v[228:231], v169 offset:55296
	ds_read_b128 v[232:235], v169 offset:56320
	global_load_lds_dwordx4 v[236:237], off
	v_lshl_add_u64 v[236:237], v[238:239], 0, s[20:21]
	s_add_i32 m0, s8, 0x2000
	v_lshl_add_u64 v[160:161], v[160:161], 0, s[24:25]
	s_add_i32 s8, s76, s33
	global_load_lds_dwordx4 v[236:237], off
	v_lshl_add_u64 v[236:237], v[160:161], 0, v[148:149]
	s_mov_b32 m0, s8
	v_lshl_add_u64 v[160:161], v[160:161], 0, v[150:151]
	global_load_lds_dwordx4 v[236:237], off
	s_add_i32 m0, s8, 0x2000
	s_nop 0
	global_load_lds_dwordx4 v[160:161], off
	v_lshl_add_u64 v[160:161], v[242:243], 0, s[20:21]
	s_mov_b32 m0, s46
	s_nop 0
	global_load_lds_dwordx4 v[160:161], off
	v_lshl_add_u64 v[160:161], v[240:241], 0, s[20:21]
	s_mov_b32 m0, s47
	s_nop 0
	global_load_lds_dwordx4 v[160:161], off
	s_waitcnt vmcnt(8)
	s_waitcnt lgkmcnt(0)
	s_barrier
	s_setprio 1
	v_mfma_i32_16x16x64_i8 v[54:57], v[142:145], v[204:207], v[54:57]
	v_mfma_i32_16x16x64_i8 v[50:53], v[178:181], v[204:207], v[50:53]
	v_mfma_i32_16x16x64_i8 v[42:45], v[142:145], v[212:215], v[42:45]
	v_mfma_i32_16x16x64_i8 v[34:37], v[178:181], v[212:215], v[34:37]
	v_mfma_i32_16x16x64_i8 v[26:29], v[142:145], v[220:223], v[26:29]
	v_mfma_i32_16x16x64_i8 v[18:21], v[178:181], v[220:223], v[18:21]
	v_mfma_i32_16x16x64_i8 v[10:13], v[142:145], v[228:231], v[10:13]
	v_mfma_i32_16x16x64_i8 v[2:5], v[178:181], v[228:231], v[2:5]
	v_mfma_i32_16x16x64_i8 v[54:57], v[156:159], v[208:211], v[54:57]
	v_mfma_i32_16x16x64_i8 v[50:53], v[182:185], v[208:211], v[50:53]
	v_mfma_i32_16x16x64_i8 v[42:45], v[156:159], v[216:219], v[42:45]
	v_mfma_i32_16x16x64_i8 v[34:37], v[182:185], v[216:219], v[34:37]
	v_mfma_i32_16x16x64_i8 v[26:29], v[156:159], v[224:227], v[26:29]
	v_mfma_i32_16x16x64_i8 v[18:21], v[182:185], v[224:227], v[18:21]
	v_mfma_i32_16x16x64_i8 v[10:13], v[156:159], v[232:235], v[10:13]
	v_mfma_i32_16x16x64_i8 v[2:5], v[182:185], v[232:235], v[2:5]
	v_mfma_i32_16x16x64_i8 v[62:65], v[186:189], v[204:207], v[62:65]
	v_mfma_i32_16x16x64_i8 v[58:61], v[196:199], v[204:207], v[58:61]
	v_mfma_i32_16x16x64_i8 v[46:49], v[186:189], v[212:215], v[46:49]
	v_mfma_i32_16x16x64_i8 v[38:41], v[196:199], v[212:215], v[38:41]
	v_mfma_i32_16x16x64_i8 v[30:33], v[186:189], v[220:223], v[30:33]
	v_mfma_i32_16x16x64_i8 v[22:25], v[196:199], v[220:223], v[22:25]
	v_mfma_i32_16x16x64_i8 v[14:17], v[186:189], v[228:231], v[14:17]
	v_mfma_i32_16x16x64_i8 v[6:9], v[196:199], v[228:231], v[6:9]
	v_mfma_i32_16x16x64_i8 v[62:65], v[190:193], v[208:211], v[62:65]
	v_mfma_i32_16x16x64_i8 v[58:61], v[200:203], v[208:211], v[58:61]
	v_mfma_i32_16x16x64_i8 v[46:49], v[190:193], v[216:219], v[46:49]
	v_mfma_i32_16x16x64_i8 v[38:41], v[200:203], v[216:219], v[38:41]
	v_mfma_i32_16x16x64_i8 v[30:33], v[190:193], v[224:227], v[30:33]
	v_mfma_i32_16x16x64_i8 v[22:25], v[200:203], v[224:227], v[22:25]
	v_mfma_i32_16x16x64_i8 v[14:17], v[190:193], v[232:235], v[14:17]
	v_mfma_i32_16x16x64_i8 v[6:9], v[200:203], v[232:235], v[6:9]
	s_setprio 0
	s_barrier
	s_add_i32 s37, s37, 2
	s_cmp_gt_u32 s37, 13
	s_mov_b64 s[8:9], s[40:41]
	s_cbranch_scc0 .LBB0_2294
	s_and_b64 vcc, exec, s[26:27]
	s_cbranch_vccz .LBB0_2297
	s_barrier

; #define PG8_STAGE(bufoff, gbase, voff) do { _Pragma("unroll") for (int _i = 0; _i < 2; ++_i) \
;         __builtin_amdgcn_global_load_lds((const unsigned*)((const char*)(gbase) + (voff)[_i]), (LAS unsigned*)(lds + (bufoff) + ldsw + _i * 8192), 16, 0, 0); } while (0)
; #define PG8_LDA(dst, b, h) do { _Pragma("unroll") for (int m = 0; m < 4; ++m) dst[m] = PG8_LD32(lds + PG8_SA(b, h) + aoff + m * 2048); } while (0)
; #define PG8_LDB(dst, b, h) do { _Pragma("unroll") for (int n = 0; n < 2; ++n) dst[n] = PG8_LD32(lds + PG8_SB(b, h) + boff + n * 2048); } while (0)
; #define PG8_WAIT_V(n) asm volatile("s_waitcnt vmcnt(" #n ")" ::: "memory")
; #define PG8_WAIT_L(n) asm volatile("s_waitcnt lgkmcnt(" #n ")" ::: "memory")
; #define PG8_BAR __builtin_amdgcn_s_barrier()
; #define PG8_SCHED __builtin_amdgcn_sched_barrier(0)
; #define PG8_STA(bufoff, nextflag, h, koff) do { if constexpr (Sched::GATHER) { unsigned _o[2]; _o[0] = (nextflag) ? nxtA[h][0] : curA[h][0]; _o[1] = (nextflag) ? nxtA[h][1] : curA[h][1]; PG8_STAGE(bufoff, Ab + (koff), _o); } \
;         else { PG8_STAGE(bufoff, ((nextflag) ? nA : cA) + (size_t)(h) * hstep + (koff), voffA); } } while (0)
; template <class Epi, class Sched, bool ALIGN_EPI, int DT>
; __device__ __forceinline__ void gemm_phase(LAS unsigned char* lds, const int KB, const Sched& S, const Epi& E) {
;     ...
;             PG8_LDB(B0, 0, 0); PG8_LDB(B1, 0, 1); PG8_SCHED; PG8_LDA(At, 0, 0); PG8_STA(PG8_SA(1, 1), false, 1, k1);
;             PG8_WAIT_V(8); PG8_WAIT_L(0); PG8_BAR; PG8_MMA(0, 0, At, B0); PG8_MMA(0, 1, At, B1); PG8_BAR; PG8_SCHED;
;             PG8_LDA(At, 0, 1); PG8_STAGE(PG8_SB(0, 0), b2, voffB); PG8_STAGE(PG8_SB(0, 1), b2 + hstep, voffB); PG8_STA(PG8_SA(0, 0), last, 0, k2);
;             PG8_WAIT_V(8); PG8_WAIT_L(0); PG8_BAR; PG8_MMA(1, 0, At, B0); PG8_MMA(1, 1, At, B1); PG8_BAR; PG8_SCHED;
.LBB0_2387:
	ds_read_b128 v[18:21], v198
	ds_read_b128 v[22:25], v198 offset:1024
	ds_read_b128 v[26:29], v198 offset:2048
	ds_read_b128 v[30:33], v198 offset:3072
	ds_read_b128 v[2:5], v199
	ds_read_b128 v[6:9], v199 offset:1024
	ds_read_b128 v[10:13], v199 offset:2048
	ds_read_b128 v[14:17], v199 offset:3072
	s_add_u32 s42, s44, 0x100
	s_addc_u32 s43, s45, 0
	s_add_i32 s76, s63, s4
	s_add_i32 m0, s33, 0xc000
	s_add_i32 s77, s33, 0xe000
	s_add_i32 s74, s76, 0x2000
	s_cmp_eq_u32 s71, 18
	v_lshl_add_u64 v[184:185], v[178:179], 0, s[44:45]
	s_cselect_b64 vcc, -1, 0
	s_cselect_b32 s75, 0, s42
	v_cndmask_b32_e32 v185, v185, v177, vcc
	v_cndmask_b32_e32 v184, v184, v176, vcc
	v_lshl_add_u64 v[226:227], v[180:181], 0, s[44:45]
	ds_read_b128 v[186:189], v200
	ds_read_b128 v[190:193], v200 offset:1024
	ds_read_b128 v[202:205], v200 offset:2048
	ds_read_b128 v[206:209], v200 offset:3072
	ds_read_b128 v[210:213], v200 offset:4096
	ds_read_b128 v[214:217], v200 offset:5120
	ds_read_b128 v[218:221], v200 offset:6144
	ds_read_b128 v[222:225], v200 offset:7168
	global_load_lds_dwordx4 v[226:227], off
	v_lshl_add_u64 v[226:227], v[182:183], 0, s[44:45]
	s_mov_b32 m0, s77
	s_nop 0
	global_load_lds_dwordx4 v[226:227], off
	s_waitcnt vmcnt(8)
	s_waitcnt lgkmcnt(0)
	s_barrier
	s_setprio 1
	v_mfma_scale_f32_16x16x128_f8f6f4 v[158:161], v[18:25], v[186:193], v[158:161], v1, v1 op_sel_hi:[0,0,0]
	v_mfma_scale_f32_16x16x128_f8f6f4 v[154:157], v[26:33], v[186:193], v[154:157], v1, v1 op_sel_hi:[0,0,0]
	v_mfma_scale_f32_16x16x128_f8f6f4 v[150:153], v[18:25], v[202:209], v[150:153], v1, v1 op_sel_hi:[0,0,0]
	v_mfma_scale_f32_16x16x128_f8f6f4 v[142:145], v[26:33], v[202:209], v[142:145], v1, v1 op_sel_hi:[0,0,0]
	v_mfma_scale_f32_16x16x128_f8f6f4 v[134:137], v[18:25], v[210:217], v[134:137], v1, v1 op_sel_hi:[0,0,0]
	v_mfma_scale_f32_16x16x128_f8f6f4 v[126:129], v[26:33], v[210:217], v[126:129], v1, v1 op_sel_hi:[0,0,0]
	v_mfma_scale_f32_16x16x128_f8f6f4 v[118:121], v[18:25], v[218:225], v[118:121], v1, v1 op_sel_hi:[0,0,0]
	v_mfma_scale_f32_16x16x128_f8f6f4 v[110:113], v[26:33], v[218:225], v[110:113], v1, v1 op_sel_hi:[0,0,0]
	v_mfma_scale_f32_16x16x128_f8f6f4 v[146:149], v[2:9], v[186:193], v[146:149], v1, v1 op_sel_hi:[0,0,0]
	v_mfma_scale_f32_16x16x128_f8f6f4 v[138:141], v[10:17], v[186:193], v[138:141], v1, v1 op_sel_hi:[0,0,0]
	v_mfma_scale_f32_16x16x128_f8f6f4 v[130:133], v[2:9], v[202:209], v[130:133], v1, v1 op_sel_hi:[0,0,0]
	v_mfma_scale_f32_16x16x128_f8f6f4 v[122:125], v[10:17], v[202:209], v[122:125], v1, v1 op_sel_hi:[0,0,0]
	v_mfma_scale_f32_16x16x128_f8f6f4 v[114:117], v[2:9], v[210:217], v[114:117], v1, v1 op_sel_hi:[0,0,0]
	v_mfma_scale_f32_16x16x128_f8f6f4 v[106:109], v[10:17], v[210:217], v[106:109], v1, v1 op_sel_hi:[0,0,0]
	v_mfma_scale_f32_16x16x128_f8f6f4 v[102:105], v[2:9], v[218:225], v[102:105], v1, v1 op_sel_hi:[0,0,0]
	v_mfma_scale_f32_16x16x128_f8f6f4 v[98:101], v[10:17], v[218:225], v[98:101], v1, v1 op_sel_hi:[0,0,0]
	s_setprio 0
	s_barrier
	s_mov_b32 m0, s76
	v_lshl_add_u64 v[188:189], v[184:185], 0, v[170:171]
	ds_read_b128 v[202:205], v200 offset:16384
	ds_read_b128 v[206:209], v200 offset:17408
	ds_read_b128 v[210:213], v200 offset:18432
	ds_read_b128 v[214:217], v200 offset:19456
	ds_read_b128 v[218:221], v200 offset:20480
	ds_read_b128 v[222:225], v200 offset:21504
	ds_read_b128 v[226:229], v200 offset:22528
	ds_read_b128 v[230:233], v200 offset:23552
	global_load_lds_dwordx4 v[188:189], off
	v_lshl_add_u64 v[186:187], v[184:185], 0, v[164:165]
	s_mov_b32 m0, s74
	s_cselect_b32 s45, s9, s41
	s_cselect_b32 s44, s8, s40
	v_lshl_add_u64 v[190:191], v[184:185], 0, s[12:13]
	s_add_i32 s74, s64, s4
	global_load_lds_dwordx4 v[186:187], off
	v_lshl_add_u64 v[192:193], v[190:191], 0, v[170:171]
	s_mov_b32 m0, s74
	v_lshl_add_u64 v[190:191], v[190:191], 0, v[164:165]
	global_load_lds_dwordx4 v[192:193], off
	s_add_i32 m0, s74, 0x2000
	s_add_u32 s44, s44, s75
	s_addc_u32 s45, s45, 0
	global_load_lds_dwordx4 v[190:191], off
	v_lshl_add_u64 v[190:191], s[44:45], 0, v[166:167]
	s_mov_b32 m0, s33
	v_lshl_add_u64 v[192:193], s[44:45], 0, v[168:169]
	global_load_lds_dwordx4 v[190:191], off
	s_mov_b32 m0, s39
	s_nop 0
	global_load_lds_dwordx4 v[192:193], off
	s_waitcnt vmcnt(8)
	s_waitcnt lgkmcnt(0)
	s_barrier
	s_setprio 1
	v_mfma_scale_f32_16x16x128_f8f6f4 v[94:97], v[18:25], v[202:209], v[94:97], v1, v1 op_sel_hi:[0,0,0]
	v_mfma_scale_f32_16x16x128_f8f6f4 v[90:93], v[26:33], v[202:209], v[90:93], v1, v1 op_sel_hi:[0,0,0]
	v_mfma_scale_f32_16x16x128_f8f6f4 v[86:89], v[18:25], v[210:217], v[86:89], v1, v1 op_sel_hi:[0,0,0]
	v_mfma_scale_f32_16x16x128_f8f6f4 v[78:81], v[26:33], v[210:217], v[78:81], v1, v1 op_sel_hi:[0,0,0]
	v_mfma_scale_f32_16x16x128_f8f6f4 v[62:65], v[18:25], v[218:225], v[62:65], v1, v1 op_sel_hi:[0,0,0]
	v_mfma_scale_f32_16x16x128_f8f6f4 v[54:57], v[26:33], v[218:225], v[54:57], v1, v1 op_sel_hi:[0,0,0]
	v_mfma_scale_f32_16x16x128_f8f6f4 v[46:49], v[18:25], v[226:233], v[46:49], v1, v1 op_sel_hi:[0,0,0]
	v_mfma_scale_f32_16x16x128_f8f6f4 v[38:41], v[26:33], v[226:233], v[38:41], v1, v1 op_sel_hi:[0,0,0]
	v_mfma_scale_f32_16x16x128_f8f6f4 v[82:85], v[2:9], v[202:209], v[82:85], v1, v1 op_sel_hi:[0,0,0]
	v_mfma_scale_f32_16x16x128_f8f6f4 v[74:77], v[10:17], v[202:209], v[74:77], v1, v1 op_sel_hi:[0,0,0]
	v_mfma_scale_f32_16x16x128_f8f6f4 v[58:61], v[2:9], v[210:217], v[58:61], v1, v1 op_sel_hi:[0,0,0]
	v_mfma_scale_f32_16x16x128_f8f6f4 v[50:53], v[10:17], v[210:217], v[50:53], v1, v1 op_sel_hi:[0,0,0]
	v_mfma_scale_f32_16x16x128_f8f6f4 v[42:45], v[2:9], v[218:225], v[42:45], v1, v1 op_sel_hi:[0,0,0]
	v_mfma_scale_f32_16x16x128_f8f6f4 v[34:37], v[10:17], v[218:225], v[34:37], v1, v1 op_sel_hi:[0,0,0]
	v_mfma_scale_f32_16x16x128_f8f6f4 v[70:73], v[2:9], v[226:233], v[70:73], v1, v1 op_sel_hi:[0,0,0]
	v_mfma_scale_f32_16x16x128_f8f6f4 v[66:69], v[10:17], v[226:233], v[66:69], v1, v1 op_sel_hi:[0,0,0]
	s_setprio 0
	s_barrier
; #define PG8_STAGE(bufoff, gbase, voff) do { _Pragma("unroll") for (int _i = 0; _i < 2; ++_i) \
;         __builtin_amdgcn_global_load_lds((const unsigned*)((const char*)(gbase) + (voff)[_i]), (LAS unsigned*)(lds + (bufoff) + ldsw + _i * 8192), 16, 0, 0); } while (0)
; #define PG8_LDA(dst, b, h) do { _Pragma("unroll") for (int m = 0; m < 4; ++m) dst[m] = PG8_LD32(lds + PG8_SA(b, h) + aoff + m * 2048); } while (0)
; #define PG8_LDB(dst, b, h) do { _Pragma("unroll") for (int n = 0; n < 2; ++n) dst[n] = PG8_LD32(lds + PG8_SB(b, h) + boff + n * 2048); } while (0)
; #define PG8_WAIT_V(n) asm volatile("s_waitcnt vmcnt(" #n ")" ::: "memory")
; #define PG8_WAIT_L(n) asm volatile("s_waitcnt lgkmcnt(" #n ")" ::: "memory")
; #define PG8_BAR __builtin_amdgcn_s_barrier()
; #define PG8_SCHED __builtin_amdgcn_sched_barrier(0)
; #define PG8_STA(bufoff, nextflag, h, koff) do { if constexpr (Sched::GATHER) { unsigned _o[2]; _o[0] = (nextflag) ? nxtA[h][0] : curA[h][0]; _o[1] = (nextflag) ? nxtA[h][1] : curA[h][1]; PG8_STAGE(bufoff, Ab + (koff), _o); } \
;         else { PG8_STAGE(bufoff, ((nextflag) ? nA : cA) + (size_t)(h) * hstep + (koff), voffA); } } while (0)
; template <class Epi, class Sched, bool ALIGN_EPI, int DT>
; __device__ __forceinline__ void gemm_phase(LAS unsigned char* lds, const int KB, const Sched& S, const Epi& E) {
;     ...
;             PG8_LDB(B0, 1, 0); PG8_LDB(B1, 1, 1); PG8_SCHED; PG8_LDA(At, 1, 0); PG8_STA(PG8_SA(0, 1), last, 1, k2);
;             PG8_WAIT_V(8); PG8_WAIT_L(0); PG8_BAR; PG8_MMA(0, 0, At, B0); PG8_MMA(0, 1, At, B1); PG8_BAR; PG8_SCHED;
;             PG8_LDA(At, 1, 1); PG8_STAGE(PG8_SB(1, 0), b3, voffB); PG8_STAGE(PG8_SB(1, 1), b3 + hstep, voffB); PG8_STA(PG8_SA(1, 0), last, 0, k3);
;             PG8_WAIT_V(8); PG8_WAIT_L(0); PG8_BAR; PG8_MMA(1, 0, At, B0); PG8_MMA(1, 1, At, B1); PG8_BAR; PG8_SCHED;
;         }
;         if constexpr (ALIGN_EPI) { if (wr == 0) PG8_BAR; }
	s_add_i32 s74, 0, 0x18000
	s_add_i32 s75, 0, 0x1c000
	v_add_u32_e32 v14, s74, v196
	v_add_u32_e32 v30, s75, v196
	ds_read_b128 v[2:5], v14
	ds_read_b128 v[6:9], v14 offset:1024
	ds_read_b128 v[10:13], v14 offset:2048
	ds_read_b128 v[14:17], v14 offset:3072
	ds_read_b128 v[18:21], v30
	ds_read_b128 v[22:25], v30 offset:1024
	ds_read_b128 v[26:29], v30 offset:2048
	ds_read_b128 v[30:33], v30 offset:3072
	s_add_u32 s44, s44, 0x58000
	s_addc_u32 s45, s45, 0
	s_mov_b32 m0, s46
	v_lshl_add_u64 v[234:235], s[44:45], 0, v[166:167]
	ds_read_b128 v[202:205], v200 offset:32768
	ds_read_b128 v[206:209], v200 offset:33792
	ds_read_b128 v[210:213], v200 offset:34816
	ds_read_b128 v[214:217], v200 offset:35840
	ds_read_b128 v[218:221], v200 offset:36864
	ds_read_b128 v[222:225], v200 offset:37888
	ds_read_b128 v[226:229], v200 offset:38912
	ds_read_b128 v[230:233], v200 offset:39936
	global_load_lds_dwordx4 v[234:235], off
	v_lshl_add_u64 v[234:235], s[44:45], 0, v[168:169]
	s_mov_b32 m0, s47
	s_nop 0
	global_load_lds_dwordx4 v[234:235], off
	s_waitcnt vmcnt(8)
	s_waitcnt lgkmcnt(0)
	s_barrier
	s_setprio 1
	v_mfma_scale_f32_16x16x128_f8f6f4 v[158:161], v[2:9], v[202:209], v[158:161], v1, v1 op_sel_hi:[0,0,0]
	v_mfma_scale_f32_16x16x128_f8f6f4 v[154:157], v[10:17], v[202:209], v[154:157], v1, v1 op_sel_hi:[0,0,0]
	v_mfma_scale_f32_16x16x128_f8f6f4 v[150:153], v[2:9], v[210:217], v[150:153], v1, v1 op_sel_hi:[0,0,0]
	v_mfma_scale_f32_16x16x128_f8f6f4 v[142:145], v[10:17], v[210:217], v[142:145], v1, v1 op_sel_hi:[0,0,0]
	v_mfma_scale_f32_16x16x128_f8f6f4 v[134:137], v[2:9], v[218:225], v[134:137], v1, v1 op_sel_hi:[0,0,0]
	v_mfma_scale_f32_16x16x128_f8f6f4 v[126:129], v[10:17], v[218:225], v[126:129], v1, v1 op_sel_hi:[0,0,0]
	v_mfma_scale_f32_16x16x128_f8f6f4 v[118:121], v[2:9], v[226:233], v[118:121], v1, v1 op_sel_hi:[0,0,0]
	v_mfma_scale_f32_16x16x128_f8f6f4 v[110:113], v[10:17], v[226:233], v[110:113], v1, v1 op_sel_hi:[0,0,0]
	v_mfma_scale_f32_16x16x128_f8f6f4 v[146:149], v[18:25], v[202:209], v[146:149], v1, v1 op_sel_hi:[0,0,0]
	v_mfma_scale_f32_16x16x128_f8f6f4 v[138:141], v[26:33], v[202:209], v[138:141], v1, v1 op_sel_hi:[0,0,0]
	v_mfma_scale_f32_16x16x128_f8f6f4 v[130:133], v[18:25], v[210:217], v[130:133], v1, v1 op_sel_hi:[0,0,0]
	v_mfma_scale_f32_16x16x128_f8f6f4 v[122:125], v[26:33], v[210:217], v[122:125], v1, v1 op_sel_hi:[0,0,0]
	v_mfma_scale_f32_16x16x128_f8f6f4 v[114:117], v[18:25], v[218:225], v[114:117], v1, v1 op_sel_hi:[0,0,0]
	v_mfma_scale_f32_16x16x128_f8f6f4 v[106:109], v[26:33], v[218:225], v[106:109], v1, v1 op_sel_hi:[0,0,0]
	v_mfma_scale_f32_16x16x128_f8f6f4 v[102:105], v[18:25], v[226:233], v[102:105], v1, v1 op_sel_hi:[0,0,0]
	v_mfma_scale_f32_16x16x128_f8f6f4 v[98:101], v[26:33], v[226:233], v[98:101], v1, v1 op_sel_hi:[0,0,0]
	s_setprio 0
	s_barrier
	s_add_i32 s44, s74, s4
	v_lshl_add_u64 v[188:189], v[188:189], 0, s[16:17]
	s_mov_b32 m0, s44
	ds_read_b128 v[202:205], v200 offset:49152
	ds_read_b128 v[206:209], v200 offset:50176
	ds_read_b128 v[210:213], v200 offset:51200
	ds_read_b128 v[214:217], v200 offset:52224
	ds_read_b128 v[218:221], v200 offset:53248
	ds_read_b128 v[222:225], v200 offset:54272
	ds_read_b128 v[226:229], v200 offset:55296
	ds_read_b128 v[230:233], v200 offset:56320
	global_load_lds_dwordx4 v[188:189], off
	v_lshl_add_u64 v[186:187], v[186:187], 0, s[16:17]
	s_add_i32 m0, s44, 0x2000
	v_lshl_add_u64 v[184:185], v[184:185], 0, s[18:19]
	s_add_i32 s44, s75, s4
	global_load_lds_dwordx4 v[186:187], off
	v_lshl_add_u64 v[186:187], v[184:185], 0, v[170:171]
	s_mov_b32 m0, s44
	v_lshl_add_u64 v[184:185], v[184:185], 0, v[164:165]
	global_load_lds_dwordx4 v[186:187], off
	s_add_i32 m0, s44, 0x2000
	s_nop 0
	global_load_lds_dwordx4 v[184:185], off
	v_lshl_add_u64 v[184:185], v[190:191], 0, s[16:17]
	s_mov_b32 m0, s52
	s_nop 0
	global_load_lds_dwordx4 v[184:185], off
	v_lshl_add_u64 v[184:185], v[192:193], 0, s[16:17]
	s_mov_b32 m0, s53
	s_nop 0
	global_load_lds_dwordx4 v[184:185], off
	s_waitcnt vmcnt(8)
	s_waitcnt lgkmcnt(0)
	s_barrier
	s_setprio 1
	v_mfma_scale_f32_16x16x128_f8f6f4 v[94:97], v[2:9], v[202:209], v[94:97], v1, v1 op_sel_hi:[0,0,0]
	v_mfma_scale_f32_16x16x128_f8f6f4 v[90:93], v[10:17], v[202:209], v[90:93], v1, v1 op_sel_hi:[0,0,0]
	v_mfma_scale_f32_16x16x128_f8f6f4 v[86:89], v[2:9], v[210:217], v[86:89], v1, v1 op_sel_hi:[0,0,0]
	v_mfma_scale_f32_16x16x128_f8f6f4 v[78:81], v[10:17], v[210:217], v[78:81], v1, v1 op_sel_hi:[0,0,0]
	v_mfma_scale_f32_16x16x128_f8f6f4 v[62:65], v[2:9], v[218:225], v[62:65], v1, v1 op_sel_hi:[0,0,0]
	v_mfma_scale_f32_16x16x128_f8f6f4 v[54:57], v[10:17], v[218:225], v[54:57], v1, v1 op_sel_hi:[0,0,0]
	v_mfma_scale_f32_16x16x128_f8f6f4 v[46:49], v[2:9], v[226:233], v[46:49], v1, v1 op_sel_hi:[0,0,0]
	v_mfma_scale_f32_16x16x128_f8f6f4 v[38:41], v[10:17], v[226:233], v[38:41], v1, v1 op_sel_hi:[0,0,0]
	v_mfma_scale_f32_16x16x128_f8f6f4 v[82:85], v[18:25], v[202:209], v[82:85], v1, v1 op_sel_hi:[0,0,0]
	v_mfma_scale_f32_16x16x128_f8f6f4 v[74:77], v[26:33], v[202:209], v[74:77], v1, v1 op_sel_hi:[0,0,0]
	v_mfma_scale_f32_16x16x128_f8f6f4 v[58:61], v[18:25], v[210:217], v[58:61], v1, v1 op_sel_hi:[0,0,0]
	v_mfma_scale_f32_16x16x128_f8f6f4 v[50:53], v[26:33], v[210:217], v[50:53], v1, v1 op_sel_hi:[0,0,0]
	v_mfma_scale_f32_16x16x128_f8f6f4 v[42:45], v[18:25], v[218:225], v[42:45], v1, v1 op_sel_hi:[0,0,0]
	v_mfma_scale_f32_16x16x128_f8f6f4 v[34:37], v[26:33], v[218:225], v[34:37], v1, v1 op_sel_hi:[0,0,0]
	v_mfma_scale_f32_16x16x128_f8f6f4 v[70:73], v[18:25], v[226:233], v[70:73], v1, v1 op_sel_hi:[0,0,0]
	v_mfma_scale_f32_16x16x128_f8f6f4 v[66:69], v[26:33], v[226:233], v[66:69], v1, v1 op_sel_hi:[0,0,0]
	s_setprio 0
	s_barrier
	s_add_i32 s71, s71, 2
	s_cmp_gt_u32 s71, 19
	s_mov_b64 s[44:45], s[42:43]
	s_cbranch_scc0 .LBB0_2387
	s_and_b64 vcc, exec, s[20:21]
	s_cbranch_vccz .LBB0_2390
	s_barrier
